# v4: no acc zeroing in all GEMMs, MoBA LUT read address folding, cross-attn fused behind q_x GEMM without grid barrier
# speedup vs baseline: 1.0065x; 1.0065x over previous
; template <bool I8, class AccT> __device__ __forceinline__ void mma1(AccT& c, const bf16x8& a, const bf16x8& b) {
;     if constexpr (I8) c = __builtin_amdgcn_mfma_i32_16x16x64_i8(__builtin_bit_cast(AccT, a), __builtin_bit_cast(AccT, b), c, 0, 0, 0);
;     else c = __builtin_amdgcn_mfma_f32_16x16x32_bf16(a, b, c, 0, 0, 0);
; }
.Lzwi_s0:
	v_mfma_i32_16x16x64_i8 v[92:95], v[64:67], v[172:175], 0
	v_mfma_i32_16x16x64_i8 v[88:91], v[72:75], v[172:175], 0
	v_mfma_i32_16x16x64_i8 v[144:147], v[64:67], v[180:183], 0
	v_mfma_i32_16x16x64_i8 v[140:143], v[72:75], v[180:183], 0
	v_mfma_i32_16x16x64_i8 v[128:131], v[64:67], v[188:191], 0
	v_mfma_i32_16x16x64_i8 v[124:127], v[72:75], v[188:191], 0
	v_mfma_i32_16x16x64_i8 v[108:111], v[64:67], v[196:199], 0
	v_mfma_i32_16x16x64_i8 v[104:107], v[72:75], v[196:199], 0
	v_mfma_i32_16x16x64_i8 v[92:95], v[68:71], v[176:179], v[92:95]
	v_mfma_i32_16x16x64_i8 v[88:91], v[76:79], v[176:179], v[88:91]
	v_mfma_i32_16x16x64_i8 v[144:147], v[68:71], v[184:187], v[144:147]
	v_mfma_i32_16x16x64_i8 v[140:143], v[76:79], v[184:187], v[140:143]
	v_mfma_i32_16x16x64_i8 v[128:131], v[68:71], v[192:195], v[128:131]
	v_mfma_i32_16x16x64_i8 v[124:127], v[76:79], v[192:195], v[124:127]
	v_mfma_i32_16x16x64_i8 v[108:111], v[68:71], v[200:203], v[108:111]
	v_mfma_i32_16x16x64_i8 v[104:107], v[76:79], v[200:203], v[104:107]
	s_setprio 0
	s_setprio 1
	v_mfma_i32_16x16x64_i8 v[84:87], v[148:151], v[172:175], 0
	v_mfma_i32_16x16x64_i8 v[80:83], v[156:159], v[172:175], 0
	v_mfma_i32_16x16x64_i8 v[136:139], v[148:151], v[180:183], 0
	v_mfma_i32_16x16x64_i8 v[132:135], v[156:159], v[180:183], 0
	v_mfma_i32_16x16x64_i8 v[120:123], v[148:151], v[188:191], 0
	v_mfma_i32_16x16x64_i8 v[114:117], v[156:159], v[188:191], 0
	v_mfma_i32_16x16x64_i8 v[100:103], v[148:151], v[196:199], 0
	v_mfma_i32_16x16x64_i8 v[96:99], v[156:159], v[196:199], 0
	v_mfma_i32_16x16x64_i8 v[84:87], v[152:155], v[176:179], v[84:87]
	v_mfma_i32_16x16x64_i8 v[80:83], v[160:163], v[176:179], v[80:83]
	v_mfma_i32_16x16x64_i8 v[136:139], v[152:155], v[184:187], v[136:139]
	v_mfma_i32_16x16x64_i8 v[132:135], v[160:163], v[184:187], v[132:135]
	v_mfma_i32_16x16x64_i8 v[120:123], v[152:155], v[192:195], v[120:123]
	v_mfma_i32_16x16x64_i8 v[114:117], v[160:163], v[192:195], v[114:117]
	v_mfma_i32_16x16x64_i8 v[100:103], v[152:155], v[200:203], v[100:103]
	v_mfma_i32_16x16x64_i8 v[96:99], v[160:163], v[200:203], v[96:99]
	s_setprio 0
	s_branch .Lzwi_r0
.Lzwi_s1:
	v_mfma_i32_16x16x64_i8 v[60:63], v[64:67], v[172:175], 0
	v_mfma_i32_16x16x64_i8 v[56:59], v[72:75], v[172:175], 0
	v_mfma_i32_16x16x64_i8 v[44:47], v[64:67], v[180:183], 0
	v_mfma_i32_16x16x64_i8 v[40:43], v[72:75], v[180:183], 0
	v_mfma_i32_16x16x64_i8 v[28:31], v[64:67], v[188:191], 0
	v_mfma_i32_16x16x64_i8 v[24:27], v[72:75], v[188:191], 0
	v_mfma_i32_16x16x64_i8 v[12:15], v[64:67], v[196:199], 0
	v_mfma_i32_16x16x64_i8 v[8:11], v[72:75], v[196:199], 0
	v_mfma_i32_16x16x64_i8 v[60:63], v[68:71], v[176:179], v[60:63]
	v_mfma_i32_16x16x64_i8 v[56:59], v[76:79], v[176:179], v[56:59]
	v_mfma_i32_16x16x64_i8 v[44:47], v[68:71], v[184:187], v[44:47]
	v_mfma_i32_16x16x64_i8 v[40:43], v[76:79], v[184:187], v[40:43]
	v_mfma_i32_16x16x64_i8 v[28:31], v[68:71], v[192:195], v[28:31]
	v_mfma_i32_16x16x64_i8 v[24:27], v[76:79], v[192:195], v[24:27]
	v_mfma_i32_16x16x64_i8 v[12:15], v[68:71], v[200:203], v[12:15]
	v_mfma_i32_16x16x64_i8 v[8:11], v[76:79], v[200:203], v[8:11]
	s_setprio 0
	s_setprio 1
	v_mfma_i32_16x16x64_i8 v[52:55], v[148:151], v[172:175], 0
	v_mfma_i32_16x16x64_i8 v[48:51], v[156:159], v[172:175], 0
	v_mfma_i32_16x16x64_i8 v[36:39], v[148:151], v[180:183], 0
	v_mfma_i32_16x16x64_i8 v[32:35], v[156:159], v[180:183], 0
	v_mfma_i32_16x16x64_i8 v[20:23], v[148:151], v[188:191], 0
	v_mfma_i32_16x16x64_i8 v[16:19], v[156:159], v[188:191], 0
	v_mfma_i32_16x16x64_i8 v[4:7], v[148:151], v[196:199], 0
	v_mfma_i32_16x16x64_i8 v[0:3], v[156:159], v[196:199], 0
	v_mfma_i32_16x16x64_i8 v[52:55], v[152:155], v[176:179], v[52:55]
	v_mfma_i32_16x16x64_i8 v[48:51], v[160:163], v[176:179], v[48:51]
	v_mfma_i32_16x16x64_i8 v[36:39], v[152:155], v[184:187], v[36:39]
	v_mfma_i32_16x16x64_i8 v[32:35], v[160:163], v[184:187], v[32:35]
	v_mfma_i32_16x16x64_i8 v[20:23], v[152:155], v[192:195], v[20:23]
	v_mfma_i32_16x16x64_i8 v[16:19], v[160:163], v[192:195], v[16:19]
	v_mfma_i32_16x16x64_i8 v[4:7], v[152:155], v[200:203], v[4:7]
	v_mfma_i32_16x16x64_i8 v[0:3], v[160:163], v[200:203], v[0:3]
	s_setprio 0
	s_branch .Lzwi_r1

; #define PG8_STAGE(bufoff, gbase, voff) do { _Pragma("unroll") for (int _i = 0; _i < 2; ++_i) { const char* gb_ = (const char*)(gbase) + _i * rstep; asm volatile("" : "+s"(gb_));   \
;         __builtin_amdgcn_global_load_lds((const unsigned*)(gb_ + (voff)), (LAS unsigned*)(lds + (bufoff) + ldsw + _i * 8192), 16, 0, 0); } } while (0)
; #define PG8_LDA(dst, b, h) do { _Pragma("unroll") for (int m = 0; m < 4; ++m) _Pragma("unroll") for (int k = 0; k < 2; ++k) dst[m][k] = *(const LAS bf16x8*)(lds + PG8_SA(b, h) + aoff + m * 2048 + k * 1024); } while (0)
; #define PG8_WAIT_V(n) asm volatile("s_waitcnt vmcnt(" #n ")" ::: "memory")
; #define PG8_WAIT_L(n) asm volatile("s_waitcnt lgkmcnt(" #n ")" ::: "memory")
; #define PG8_BAR __builtin_amdgcn_s_barrier()
; template <class Epi, class Sched, bool ALIGN_EPI = true, bool SP2 = true, bool I8 = false, bool F8 = false>
; __device__ __forceinline__ void gemm_phase(LAS unsigned char* lds, const int K, const Sched& S, const Epi& E, const int wave) {
;     ...
;         const bool has_next = S.next(ui + 1, nxt);
;         const char* nA = has_next ? nxt.a : cA; const char* nB = has_next ? nxt.b : cB;
;         for (int t = 0; t < nt; t += 2) {
;             const bool last = (t == nt - 2);
;             const char* a1 = cA + (size_t)(t + 1) * kstep;
;             const char* a2 = last ? nA : cA + (size_t)(t + 2) * kstep; const char* b2 = last ? nB : cB + (size_t)(t + 2) * kstep;
;             const char* a3 = a2 + kstep; const char* b3 = b2 + kstep;
;             if constexpr (SP2) {
;             PG8_LDB(B0, 0, 0); PG8_LDB(B1, 0, 1); PG8_SCHED; PG8_LDA(At, 0, 0); PG8_STAGE(PG8_SA(1, 1), a1 + hstep, voffA);
;             PG8_WAIT_V(8); PG8_WAIT_L(0); PG8_BAR; PG8_MMA(0, 0, At, B0); PG8_MMA(0, 1, At, B1); PG8_BAR; PG8_SCHED;
;             PG8_LDA(At, 0, 1); PG8_STAGE(PG8_SB(0, 0), b2, voffB); PG8_STAGE(PG8_SB(0, 1), b2 + hstep, voffB); PG8_STAGE(PG8_SA(0, 0), a2, voffA);
;             PG8_WAIT_V(8); PG8_WAIT_L(0); PG8_BAR; PG8_MMA(1, 0, At, B0); PG8_MMA(1, 1, At, B1); PG8_BAR; PG8_SCHED;
;     ...
;         if (!(Epi::KEEPS && cur.sub < 2)) {
; #pragma unroll
;         for (int a = 0; a < 2; ++a)
; #pragma unroll
;             for (int b = 0; b < 2; ++b)
; #pragma unroll
;                 for (int m = 0; m < 4; ++m)
; #pragma unroll
;                     for (int n = 0; n < 2; ++n) acc[a][b][m][n] = (acc_t){0, 0, 0, 0};
;         }
.LBB0_355:
	s_add_u32 s1, s52, 0x100
	s_addc_u32 s45, s53, 0
	s_add_u32 s4, s4, 0x30080
	s_addc_u32 s5, s5, 0
	s_mov_b32 s47, -2
.LBB0_356:
	s_add_u32 s52, s4, 0xfffd0080
	s_addc_u32 s53, s5, -1
	s_cmp_eq_u32 s47, 4
	s_cselect_b32 s52, s48, s52
	s_cselect_b32 s53, s49, s53
	s_cselect_b32 s56, s50, s1
	s_cselect_b32 s57, s51, s45
	s_add_u32 s54, s52, 0x80
	s_addc_u32 s55, s53, 0
	s_add_i32 s60, 0, 0x10000
	s_add_i32 s61, 0, 0x14000
	v_add_u32_e32 v76, s60, v165
	v_add_u32_e32 v112, s61, v165
	ds_read_b128 v[64:67], v76
	ds_read_b128 v[68:71], v76 offset:1024
	ds_read_b128 v[72:75], v76 offset:2048
	ds_read_b128 v[76:79], v76 offset:3072
	ds_read_b128 v[148:151], v112
	ds_read_b128 v[152:155], v112 offset:1024
	ds_read_b128 v[156:159], v112 offset:2048
	ds_read_b128 v[160:163], v112 offset:3072
	s_add_u32 s58, s4, 0xffff0000
	s_addc_u32 s59, s5, -1
	ds_read_b128 v[172:175], v166
	ds_read_b128 v[176:179], v166 offset:1024
	ds_read_b128 v[180:183], v166 offset:2048
	ds_read_b128 v[184:187], v166 offset:3072
	ds_read_b128 v[188:191], v166 offset:4096
	ds_read_b128 v[192:195], v166 offset:5120
	ds_read_b128 v[196:199], v166 offset:6144
	ds_read_b128 v[200:203], v166 offset:7168
	s_add_i32 m0, s73, 0xc000
	v_lshl_add_u64 v[114:115], s[58:59], 0, v[168:169]
	s_mov_b64 s[58:59], s[4:5]
	global_load_lds_dwordx4 v[114:115], off
	s_add_i32 m0, s73, 0xe000
	v_lshl_add_u64 v[114:115], s[58:59], 0, v[168:169]
	global_load_lds_dwordx4 v[114:115], off
	s_waitcnt vmcnt(8)
	s_waitcnt lgkmcnt(0)
	s_barrier
	s_setprio 1
	s_waitcnt lgkmcnt(0)
	s_cmp_eq_u32 s47, -2
	s_cbranch_scc1 .Lzwi_s0
	v_mfma_i32_16x16x64_i8 v[92:95], v[64:67], v[172:175], v[92:95]
	v_mfma_i32_16x16x64_i8 v[88:91], v[72:75], v[172:175], v[88:91]
	v_mfma_i32_16x16x64_i8 v[144:147], v[64:67], v[180:183], v[144:147]
	v_mfma_i32_16x16x64_i8 v[140:143], v[72:75], v[180:183], v[140:143]
	v_mfma_i32_16x16x64_i8 v[128:131], v[64:67], v[188:191], v[128:131]
	v_mfma_i32_16x16x64_i8 v[124:127], v[72:75], v[188:191], v[124:127]
	v_mfma_i32_16x16x64_i8 v[108:111], v[64:67], v[196:199], v[108:111]
	v_mfma_i32_16x16x64_i8 v[104:107], v[72:75], v[196:199], v[104:107]
	v_mfma_i32_16x16x64_i8 v[92:95], v[68:71], v[176:179], v[92:95]
	v_mfma_i32_16x16x64_i8 v[88:91], v[76:79], v[176:179], v[88:91]
	v_mfma_i32_16x16x64_i8 v[144:147], v[68:71], v[184:187], v[144:147]
	v_mfma_i32_16x16x64_i8 v[140:143], v[76:79], v[184:187], v[140:143]
	v_mfma_i32_16x16x64_i8 v[128:131], v[68:71], v[192:195], v[128:131]
	v_mfma_i32_16x16x64_i8 v[124:127], v[76:79], v[192:195], v[124:127]
	v_mfma_i32_16x16x64_i8 v[108:111], v[68:71], v[200:203], v[108:111]
	v_mfma_i32_16x16x64_i8 v[104:107], v[76:79], v[200:203], v[104:107]
	s_setprio 0
	s_setprio 1
	v_mfma_i32_16x16x64_i8 v[84:87], v[148:151], v[172:175], v[84:87]
	v_mfma_i32_16x16x64_i8 v[80:83], v[156:159], v[172:175], v[80:83]
	v_mfma_i32_16x16x64_i8 v[136:139], v[148:151], v[180:183], v[136:139]
	v_mfma_i32_16x16x64_i8 v[132:135], v[156:159], v[180:183], v[132:135]
	v_mfma_i32_16x16x64_i8 v[120:123], v[148:151], v[188:191], v[120:123]
	v_mfma_i32_16x16x64_i8 v[114:117], v[156:159], v[188:191], v[116:119]
	v_mfma_i32_16x16x64_i8 v[100:103], v[148:151], v[196:199], v[100:103]
	v_mfma_i32_16x16x64_i8 v[96:99], v[156:159], v[196:199], v[96:99]
	v_mfma_i32_16x16x64_i8 v[84:87], v[152:155], v[176:179], v[84:87]
	v_mfma_i32_16x16x64_i8 v[80:83], v[160:163], v[176:179], v[80:83]
	v_mfma_i32_16x16x64_i8 v[136:139], v[152:155], v[184:187], v[136:139]
	v_mfma_i32_16x16x64_i8 v[132:135], v[160:163], v[184:187], v[132:135]
	v_mfma_i32_16x16x64_i8 v[120:123], v[152:155], v[192:195], v[120:123]
	v_mfma_i32_16x16x64_i8 v[114:117], v[160:163], v[192:195], v[114:117]
	v_mfma_i32_16x16x64_i8 v[100:103], v[152:155], v[200:203], v[100:103]
	v_mfma_i32_16x16x64_i8 v[96:99], v[160:163], v[200:203], v[96:99]
	s_setprio 0
.Lzwi_r0:
	s_barrier
	s_mov_b64 s[58:59], s[56:57]
	ds_read_b128 v[172:175], v166 offset:16384
	ds_read_b128 v[176:179], v166 offset:17408
	ds_read_b128 v[180:183], v166 offset:18432
	ds_read_b128 v[184:187], v166 offset:19456
	ds_read_b128 v[188:191], v166 offset:20480
	ds_read_b128 v[192:195], v166 offset:21504
	ds_read_b128 v[196:199], v166 offset:22528
	ds_read_b128 v[200:203], v166 offset:23552
	s_add_i32 s60, s60, s72
	v_lshl_add_u64 v[118:119], s[58:59], 0, v[170:171]
	s_add_u32 s58, s56, 0x10000
	s_mov_b32 m0, s60
	s_addc_u32 s59, s57, 0
	global_load_lds_dwordx4 v[118:119], off
	s_add_i32 m0, s60, 0x2000
	v_lshl_add_u64 v[118:119], s[58:59], 0, v[170:171]
	s_add_u32 s58, s56, 0x20000
	s_addc_u32 s59, s57, 0
	global_load_lds_dwordx4 v[118:119], off
	s_add_i32 s60, s61, s72
	v_lshl_add_u64 v[118:119], s[58:59], 0, v[170:171]
	s_add_u32 s58, s56, 0x30000
	s_mov_b32 m0, s60
	s_addc_u32 s59, s57, 0
	global_load_lds_dwordx4 v[118:119], off
	s_add_i32 m0, s60, 0x2000
	v_lshl_add_u64 v[118:119], s[58:59], 0, v[170:171]
	s_mov_b64 s[58:59], s[52:53]
	global_load_lds_dwordx4 v[118:119], off
	s_mov_b32 m0, s73
	v_lshl_add_u64 v[118:119], s[58:59], 0, v[168:169]
	s_add_u32 s58, s52, 0x10000
	s_addc_u32 s59, s53, 0
	global_load_lds_dwordx4 v[118:119], off
	s_mov_b32 m0, s75
	v_lshl_add_u64 v[118:119], s[58:59], 0, v[168:169]
	global_load_lds_dwordx4 v[118:119], off
	s_waitcnt vmcnt(8)
	s_waitcnt lgkmcnt(0)
	s_barrier
	s_setprio 1
	s_waitcnt lgkmcnt(0)
	s_cmp_eq_u32 s47, -2
	s_cbranch_scc1 .Lzwi_s1
; #define PG8_STAGE(bufoff, gbase, voff) do { _Pragma("unroll") for (int _i = 0; _i < 2; ++_i) { const char* gb_ = (const char*)(gbase) + _i * rstep; asm volatile("" : "+s"(gb_));   \
;         __builtin_amdgcn_global_load_lds((const unsigned*)(gb_ + (voff)), (LAS unsigned*)(lds + (bufoff) + ldsw + _i * 8192), 16, 0, 0); } } while (0)
; #define PG8_LDA(dst, b, h) do { _Pragma("unroll") for (int m = 0; m < 4; ++m) _Pragma("unroll") for (int k = 0; k < 2; ++k) dst[m][k] = *(const LAS bf16x8*)(lds + PG8_SA(b, h) + aoff + m * 2048 + k * 1024); } while (0)
; #define PG8_LDB(dst, b, h) do { _Pragma("unroll") for (int n = 0; n < 2; ++n) _Pragma("unroll") for (int k = 0; k < 2; ++k) dst[n][k] = *(const LAS bf16x8*)(lds + PG8_SB(b, h) + boff + n * 2048 + k * 1024); } while (0)
; #define PG8_WAIT_V(n) asm volatile("s_waitcnt vmcnt(" #n ")" ::: "memory")
; #define PG8_WAIT_L(n) asm volatile("s_waitcnt lgkmcnt(" #n ")" ::: "memory")
; #define PG8_BAR __builtin_amdgcn_s_barrier()
; #define PG8_SCHED __builtin_amdgcn_sched_barrier(0)
; template <class Epi, class Sched, bool ALIGN_EPI = true, bool SP2 = true, bool I8 = false, bool F8 = false>
; __device__ __forceinline__ void gemm_phase(LAS unsigned char* lds, const int K, const Sched& S, const Epi& E, const int wave) {
;     ...
;             PG8_WAIT_V(8); PG8_WAIT_L(0); PG8_BAR; PG8_MMA(1, 0, At, B0); PG8_MMA(1, 1, At, B1); PG8_BAR; PG8_SCHED;
;             PG8_LDB(B0, 1, 0); PG8_LDB(B1, 1, 1); PG8_SCHED; PG8_LDA(At, 1, 0); PG8_STAGE(PG8_SA(0, 1), a2 + hstep, voffA);
;             PG8_WAIT_V(8); PG8_WAIT_L(0); PG8_BAR; PG8_MMA(0, 0, At, B0); PG8_MMA(0, 1, At, B1); PG8_BAR; PG8_SCHED;
	v_mfma_i32_16x16x64_i8 v[60:63], v[64:67], v[172:175], v[60:63]
	v_mfma_i32_16x16x64_i8 v[56:59], v[72:75], v[172:175], v[56:59]
	v_mfma_i32_16x16x64_i8 v[44:47], v[64:67], v[180:183], v[44:47]
	v_mfma_i32_16x16x64_i8 v[40:43], v[72:75], v[180:183], v[40:43]
	v_mfma_i32_16x16x64_i8 v[28:31], v[64:67], v[188:191], v[28:31]
	v_mfma_i32_16x16x64_i8 v[24:27], v[72:75], v[188:191], v[24:27]
	v_mfma_i32_16x16x64_i8 v[12:15], v[64:67], v[196:199], v[12:15]
	v_mfma_i32_16x16x64_i8 v[8:11], v[72:75], v[196:199], v[8:11]
	v_mfma_i32_16x16x64_i8 v[60:63], v[68:71], v[176:179], v[60:63]
	v_mfma_i32_16x16x64_i8 v[56:59], v[76:79], v[176:179], v[56:59]
	v_mfma_i32_16x16x64_i8 v[44:47], v[68:71], v[184:187], v[44:47]
	v_mfma_i32_16x16x64_i8 v[40:43], v[76:79], v[184:187], v[40:43]
	v_mfma_i32_16x16x64_i8 v[28:31], v[68:71], v[192:195], v[28:31]
	v_mfma_i32_16x16x64_i8 v[24:27], v[76:79], v[192:195], v[24:27]
	v_mfma_i32_16x16x64_i8 v[12:15], v[68:71], v[200:203], v[12:15]
	v_mfma_i32_16x16x64_i8 v[8:11], v[76:79], v[200:203], v[8:11]
	s_setprio 0
	s_setprio 1
	v_mfma_i32_16x16x64_i8 v[52:55], v[148:151], v[172:175], v[52:55]
	v_mfma_i32_16x16x64_i8 v[48:51], v[156:159], v[172:175], v[48:51]
	v_mfma_i32_16x16x64_i8 v[36:39], v[148:151], v[180:183], v[36:39]
	v_mfma_i32_16x16x64_i8 v[32:35], v[156:159], v[180:183], v[32:35]
	v_mfma_i32_16x16x64_i8 v[20:23], v[148:151], v[188:191], v[20:23]
	v_mfma_i32_16x16x64_i8 v[16:19], v[156:159], v[188:191], v[16:19]
	v_mfma_i32_16x16x64_i8 v[4:7], v[148:151], v[196:199], v[4:7]
	v_mfma_i32_16x16x64_i8 v[0:3], v[156:159], v[196:199], v[0:3]
	v_mfma_i32_16x16x64_i8 v[52:55], v[152:155], v[176:179], v[52:55]
	v_mfma_i32_16x16x64_i8 v[48:51], v[160:163], v[176:179], v[48:51]
	v_mfma_i32_16x16x64_i8 v[36:39], v[152:155], v[184:187], v[36:39]
	v_mfma_i32_16x16x64_i8 v[32:35], v[160:163], v[184:187], v[32:35]
	v_mfma_i32_16x16x64_i8 v[20:23], v[152:155], v[192:195], v[20:23]
	v_mfma_i32_16x16x64_i8 v[16:19], v[160:163], v[192:195], v[16:19]
	v_mfma_i32_16x16x64_i8 v[4:7], v[152:155], v[200:203], v[4:7]
	v_mfma_i32_16x16x64_i8 v[0:3], v[160:163], v[200:203], v[0:3]
	s_setprio 0
.Lzwi_r1:
	s_barrier
	s_add_i32 s60, 0, 0x18000
	s_add_i32 s61, 0, 0x1c000
	v_add_u32_e32 v76, s60, v165
	v_add_u32_e32 v112, s61, v165
	ds_read_b128 v[64:67], v76
	ds_read_b128 v[68:71], v76 offset:1024
	ds_read_b128 v[72:75], v76 offset:2048
	ds_read_b128 v[76:79], v76 offset:3072
	ds_read_b128 v[148:151], v112
	ds_read_b128 v[152:155], v112 offset:1024
	ds_read_b128 v[156:159], v112 offset:2048
	ds_read_b128 v[160:163], v112 offset:3072
	s_add_u32 s58, s52, 0x20000
	s_addc_u32 s59, s53, 0
	ds_read_b128 v[172:175], v166 offset:32768
	ds_read_b128 v[176:179], v166 offset:33792
	ds_read_b128 v[180:183], v166 offset:34816
	ds_read_b128 v[184:187], v166 offset:35840
	ds_read_b128 v[188:191], v166 offset:36864
	ds_read_b128 v[192:195], v166 offset:37888
	ds_read_b128 v[196:199], v166 offset:38912
	ds_read_b128 v[200:203], v166 offset:39936
	s_mov_b32 m0, s76
	v_lshl_add_u64 v[118:119], s[58:59], 0, v[168:169]
	s_add_u32 s58, s52, 0x30000
	s_addc_u32 s59, s53, 0
	global_load_lds_dwordx4 v[118:119], off
	s_mov_b32 m0, s77
	v_lshl_add_u64 v[118:119], s[58:59], 0, v[168:169]
	global_load_lds_dwordx4 v[118:119], off
	s_waitcnt vmcnt(8)
	s_waitcnt lgkmcnt(0)
	s_barrier
	s_setprio 1
	s_waitcnt lgkmcnt(0)
	v_mfma_i32_16x16x64_i8 v[92:95], v[64:67], v[172:175], v[92:95]
	v_mfma_i32_16x16x64_i8 v[88:91], v[72:75], v[172:175], v[88:91]
	v_mfma_i32_16x16x64_i8 v[144:147], v[64:67], v[180:183], v[144:147]
	v_mfma_i32_16x16x64_i8 v[140:143], v[72:75], v[180:183], v[140:143]
	v_mfma_i32_16x16x64_i8 v[128:131], v[64:67], v[188:191], v[128:131]
	v_mfma_i32_16x16x64_i8 v[124:127], v[72:75], v[188:191], v[124:127]
	v_mfma_i32_16x16x64_i8 v[108:111], v[64:67], v[196:199], v[108:111]
	v_mfma_i32_16x16x64_i8 v[104:107], v[72:75], v[196:199], v[104:107]
	v_mfma_i32_16x16x64_i8 v[92:95], v[68:71], v[176:179], v[92:95]
	v_mfma_i32_16x16x64_i8 v[88:91], v[76:79], v[176:179], v[88:91]
	v_mfma_i32_16x16x64_i8 v[144:147], v[68:71], v[184:187], v[144:147]
	v_mfma_i32_16x16x64_i8 v[140:143], v[76:79], v[184:187], v[140:143]
	v_mfma_i32_16x16x64_i8 v[128:131], v[68:71], v[192:195], v[128:131]
	v_mfma_i32_16x16x64_i8 v[124:127], v[76:79], v[192:195], v[124:127]
	v_mfma_i32_16x16x64_i8 v[108:111], v[68:71], v[200:203], v[108:111]
	v_mfma_i32_16x16x64_i8 v[104:107], v[76:79], v[200:203], v[104:107]
	s_setprio 0
	s_setprio 1
	v_mfma_i32_16x16x64_i8 v[84:87], v[148:151], v[172:175], v[84:87]
	v_mfma_i32_16x16x64_i8 v[80:83], v[156:159], v[172:175], v[80:83]
	v_mfma_i32_16x16x64_i8 v[136:139], v[148:151], v[180:183], v[136:139]
	v_mfma_i32_16x16x64_i8 v[132:135], v[156:159], v[180:183], v[132:135]
	v_mfma_i32_16x16x64_i8 v[118:121], v[148:151], v[188:191], v[120:123]
	v_mfma_i32_16x16x64_i8 v[114:117], v[156:159], v[188:191], v[114:117]
	v_mfma_i32_16x16x64_i8 v[100:103], v[148:151], v[196:199], v[100:103]
	v_mfma_i32_16x16x64_i8 v[96:99], v[156:159], v[196:199], v[96:99]
	v_mfma_i32_16x16x64_i8 v[84:87], v[152:155], v[176:179], v[84:87]
	v_mfma_i32_16x16x64_i8 v[80:83], v[160:163], v[176:179], v[80:83]
	v_mfma_i32_16x16x64_i8 v[136:139], v[152:155], v[184:187], v[136:139]
	v_mfma_i32_16x16x64_i8 v[132:135], v[160:163], v[184:187], v[132:135]
	v_mfma_i32_16x16x64_i8 v[120:123], v[152:155], v[192:195], v[118:121]
	v_mfma_i32_16x16x64_i8 v[116:119], v[160:163], v[192:195], v[114:117]
	v_mfma_i32_16x16x64_i8 v[100:103], v[152:155], v[200:203], v[100:103]
	v_mfma_i32_16x16x64_i8 v[96:99], v[160:163], v[200:203], v[96:99]
	s_setprio 0
	s_barrier
; #define PG8_STAGE(bufoff, gbase, voff) do { _Pragma("unroll") for (int _i = 0; _i < 2; ++_i) { const char* gb_ = (const char*)(gbase) + _i * rstep; asm volatile("" : "+s"(gb_));   \
;         __builtin_amdgcn_global_load_lds((const unsigned*)(gb_ + (voff)), (LAS unsigned*)(lds + (bufoff) + ldsw + _i * 8192), 16, 0, 0); } } while (0)
; #define PG8_LDA(dst, b, h) do { _Pragma("unroll") for (int m = 0; m < 4; ++m) _Pragma("unroll") for (int k = 0; k < 2; ++k) dst[m][k] = *(const LAS bf16x8*)(lds + PG8_SA(b, h) + aoff + m * 2048 + k * 1024); } while (0)
; #define PG8_WAIT_V(n) asm volatile("s_waitcnt vmcnt(" #n ")" ::: "memory")
; #define PG8_WAIT_L(n) asm volatile("s_waitcnt lgkmcnt(" #n ")" ::: "memory")
; #define PG8_BAR __builtin_amdgcn_s_barrier()
; #define PG8_SCHED __builtin_amdgcn_sched_barrier(0)
; template <class Epi, class Sched, bool ALIGN_EPI = true, bool SP2 = true, bool I8 = false, bool F8 = false>
; __device__ __forceinline__ void gemm_phase(LAS unsigned char* lds, const int K, const Sched& S, const Epi& E, const int wave) {
;     ...
;         for (int t = 0; t < nt; t += 2) {
;             const bool last = (t == nt - 2);
;     ...
;             PG8_LDA(At, 1, 1); PG8_STAGE(PG8_SB(1, 0), b3, voffB); PG8_STAGE(PG8_SB(1, 1), b3 + hstep, voffB); PG8_STAGE(PG8_SA(1, 0), a3, voffA);
;             PG8_WAIT_V(8); PG8_WAIT_L(0); PG8_BAR; PG8_MMA(1, 0, At, B0); PG8_MMA(1, 1, At, B1); PG8_BAR; PG8_SCHED;
	s_add_u32 s58, s56, 0x80
	s_addc_u32 s59, s57, 0
	ds_read_b128 v[172:175], v166 offset:49152
	ds_read_b128 v[176:179], v166 offset:50176
	ds_read_b128 v[180:183], v166 offset:51200
	ds_read_b128 v[184:187], v166 offset:52224
	ds_read_b128 v[188:191], v166 offset:53248
	ds_read_b128 v[192:195], v166 offset:54272
	ds_read_b128 v[196:199], v166 offset:55296
	ds_read_b128 v[200:203], v166 offset:56320
	s_add_i32 s60, s60, s72
	v_lshl_add_u64 v[114:115], s[58:59], 0, v[170:171]
	s_add_u32 s58, s56, 0x10080
	s_mov_b32 m0, s60
	s_addc_u32 s59, s57, 0
	global_load_lds_dwordx4 v[114:115], off
	s_add_i32 m0, s60, 0x2000
	v_lshl_add_u64 v[114:115], s[58:59], 0, v[170:171]
	s_add_u32 s58, s56, 0x20080
	s_addc_u32 s59, s57, 0
	global_load_lds_dwordx4 v[114:115], off
	s_nop 0
	v_lshl_add_u64 v[114:115], s[58:59], 0, v[170:171]
	s_add_i32 s58, s61, s72
	s_mov_b32 m0, s58
	s_add_u32 s56, s56, 0x30080
	global_load_lds_dwordx4 v[114:115], off
	s_addc_u32 s57, s57, 0
	s_add_i32 m0, s58, 0x2000
	s_add_u32 s52, s52, 0x10080
	v_lshl_add_u64 v[114:115], s[56:57], 0, v[170:171]
	global_load_lds_dwordx4 v[114:115], off
	s_mov_b32 m0, s81
	v_lshl_add_u64 v[114:115], s[54:55], 0, v[168:169]
	s_addc_u32 s53, s53, 0
	global_load_lds_dwordx4 v[114:115], off
	s_mov_b32 m0, s82
	v_lshl_add_u64 v[114:115], s[52:53], 0, v[168:169]
	global_load_lds_dwordx4 v[114:115], off
	s_waitcnt vmcnt(8)
	s_waitcnt lgkmcnt(0)
	s_barrier
	s_setprio 1
	s_waitcnt lgkmcnt(0)
	v_mfma_i32_16x16x64_i8 v[60:63], v[64:67], v[172:175], v[60:63]
	v_mfma_i32_16x16x64_i8 v[56:59], v[72:75], v[172:175], v[56:59]
	v_mfma_i32_16x16x64_i8 v[44:47], v[64:67], v[180:183], v[44:47]
	v_mfma_i32_16x16x64_i8 v[40:43], v[72:75], v[180:183], v[40:43]
	v_mfma_i32_16x16x64_i8 v[28:31], v[64:67], v[188:191], v[28:31]
	v_mfma_i32_16x16x64_i8 v[24:27], v[72:75], v[188:191], v[24:27]
	v_mfma_i32_16x16x64_i8 v[12:15], v[64:67], v[196:199], v[12:15]
	v_mfma_i32_16x16x64_i8 v[8:11], v[72:75], v[196:199], v[8:11]
	v_mfma_i32_16x16x64_i8 v[60:63], v[68:71], v[176:179], v[60:63]
	v_mfma_i32_16x16x64_i8 v[56:59], v[76:79], v[176:179], v[56:59]
	v_mfma_i32_16x16x64_i8 v[44:47], v[68:71], v[184:187], v[44:47]
	v_mfma_i32_16x16x64_i8 v[40:43], v[76:79], v[184:187], v[40:43]
	v_mfma_i32_16x16x64_i8 v[28:31], v[68:71], v[192:195], v[28:31]
	v_mfma_i32_16x16x64_i8 v[24:27], v[76:79], v[192:195], v[24:27]
	v_mfma_i32_16x16x64_i8 v[12:15], v[68:71], v[200:203], v[12:15]
	v_mfma_i32_16x16x64_i8 v[8:11], v[76:79], v[200:203], v[8:11]
	s_setprio 0
	s_setprio 1
	v_mfma_i32_16x16x64_i8 v[52:55], v[148:151], v[172:175], v[52:55]
	v_mfma_i32_16x16x64_i8 v[48:51], v[156:159], v[172:175], v[48:51]
	v_mfma_i32_16x16x64_i8 v[36:39], v[148:151], v[180:183], v[36:39]
	v_mfma_i32_16x16x64_i8 v[32:35], v[156:159], v[180:183], v[32:35]
	v_mfma_i32_16x16x64_i8 v[20:23], v[148:151], v[188:191], v[20:23]
	v_mfma_i32_16x16x64_i8 v[16:19], v[156:159], v[188:191], v[16:19]
	v_mfma_i32_16x16x64_i8 v[4:7], v[148:151], v[196:199], v[4:7]
	v_mfma_i32_16x16x64_i8 v[0:3], v[156:159], v[196:199], v[0:3]
	v_mfma_i32_16x16x64_i8 v[52:55], v[152:155], v[176:179], v[52:55]
	v_mfma_i32_16x16x64_i8 v[48:51], v[160:163], v[176:179], v[48:51]
	v_mfma_i32_16x16x64_i8 v[36:39], v[152:155], v[184:187], v[36:39]
	v_mfma_i32_16x16x64_i8 v[32:35], v[160:163], v[184:187], v[32:35]
	v_mfma_i32_16x16x64_i8 v[20:23], v[152:155], v[192:195], v[20:23]
	v_mfma_i32_16x16x64_i8 v[16:19], v[160:163], v[192:195], v[16:19]
	v_mfma_i32_16x16x64_i8 v[4:7], v[152:155], v[200:203], v[4:7]
	v_mfma_i32_16x16x64_i8 v[0:3], v[160:163], v[200:203], v[0:3]
	s_setprio 0
	s_barrier
	s_add_i32 s47, s47, 2
	s_add_u32 s1, s1, 0x100
	s_addc_u32 s45, s45, 0
	s_add_u32 s4, s4, 0x100
	s_addc_u32 s5, s5, 0
	s_cmp_gt_u32 s47, 5
	s_cbranch_scc0 .LBB0_356
	s_and_b64 vcc, exec, s[8:9]
	s_cbranch_vccz .LBB0_359
	s_barrier

; template <bool I8, class AccT> __device__ __forceinline__ void mma1(AccT& c, const bf16x8& a, const bf16x8& b) {
;     if constexpr (I8) c = __builtin_amdgcn_mfma_i32_16x16x64_i8(__builtin_bit_cast(AccT, a), __builtin_bit_cast(AccT, b), c, 0, 0, 0);
;     else c = __builtin_amdgcn_mfma_f32_16x16x32_bf16(a, b, c, 0, 0, 0);
; }
.Lzga_s0:
	v_mfma_i32_16x16x64_i8 v[138:141], v[68:71], v[170:173], 0
	v_mfma_i32_16x16x64_i8 v[134:137], v[76:79], v[170:173], 0
	v_mfma_i32_16x16x64_i8 v[122:125], v[68:71], v[178:181], 0
	v_mfma_i32_16x16x64_i8 v[118:121], v[76:79], v[178:181], 0
	v_mfma_i32_16x16x64_i8 v[104:107], v[68:71], v[186:189], 0
	v_mfma_i32_16x16x64_i8 v[100:103], v[76:79], v[186:189], 0
	v_mfma_i32_16x16x64_i8 v[88:91], v[68:71], v[194:197], 0
	v_mfma_i32_16x16x64_i8 v[84:87], v[76:79], v[194:197], 0
	v_mfma_i32_16x16x64_i8 v[138:141], v[72:75], v[174:177], v[138:141]
	v_mfma_i32_16x16x64_i8 v[134:137], v[144:147], v[174:177], v[134:137]
	v_mfma_i32_16x16x64_i8 v[122:125], v[72:75], v[182:185], v[122:125]
	v_mfma_i32_16x16x64_i8 v[118:121], v[144:147], v[182:185], v[118:121]
	v_mfma_i32_16x16x64_i8 v[104:107], v[72:75], v[190:193], v[104:107]
	v_mfma_i32_16x16x64_i8 v[100:103], v[144:147], v[190:193], v[100:103]
	v_mfma_i32_16x16x64_i8 v[88:91], v[72:75], v[198:201], v[88:91]
	v_mfma_i32_16x16x64_i8 v[84:87], v[144:147], v[198:201], v[84:87]
	s_setprio 0
	s_setprio 1
	v_mfma_i32_16x16x64_i8 v[130:133], v[148:151], v[170:173], 0
	v_mfma_i32_16x16x64_i8 v[60:63], v[156:159], v[170:173], 0
	v_mfma_i32_16x16x64_i8 v[114:117], v[148:151], v[178:181], 0
	v_mfma_i32_16x16x64_i8 v[126:129], v[156:159], v[178:181], 0
	v_mfma_i32_16x16x64_i8 v[96:99], v[148:151], v[186:189], 0
	v_mfma_i32_16x16x64_i8 v[108:111], v[156:159], v[186:189], 0
	v_mfma_i32_16x16x64_i8 v[80:83], v[148:151], v[194:197], 0
	v_mfma_i32_16x16x64_i8 v[92:95], v[156:159], v[194:197], 0
	v_mfma_i32_16x16x64_i8 v[130:133], v[152:155], v[174:177], v[130:133]
	v_mfma_i32_16x16x64_i8 v[60:63], v[166:169], v[174:177], v[60:63]
	v_mfma_i32_16x16x64_i8 v[114:117], v[152:155], v[182:185], v[114:117]
	v_mfma_i32_16x16x64_i8 v[126:129], v[166:169], v[182:185], v[126:129]
	v_mfma_i32_16x16x64_i8 v[96:99], v[152:155], v[190:193], v[96:99]
	v_mfma_i32_16x16x64_i8 v[108:111], v[166:169], v[190:193], v[108:111]
	v_mfma_i32_16x16x64_i8 v[80:83], v[152:155], v[198:201], v[80:83]
	v_mfma_i32_16x16x64_i8 v[92:95], v[166:169], v[198:201], v[92:95]
	s_setprio 0
	s_branch .Lzga_r0
.Lzga_s1:
	v_mfma_i32_16x16x64_i8 v[56:59], v[68:71], v[170:173], 0
	v_mfma_i32_16x16x64_i8 v[52:55], v[76:79], v[170:173], 0
	v_mfma_i32_16x16x64_i8 v[40:43], v[68:71], v[178:181], 0
	v_mfma_i32_16x16x64_i8 v[36:39], v[76:79], v[178:181], 0
	v_mfma_i32_16x16x64_i8 v[24:27], v[68:71], v[186:189], 0
	v_mfma_i32_16x16x64_i8 v[20:23], v[76:79], v[186:189], 0
	v_mfma_i32_16x16x64_i8 v[8:11], v[68:71], v[194:197], 0
	v_mfma_i32_16x16x64_i8 v[4:7], v[76:79], v[194:197], 0
	v_mfma_i32_16x16x64_i8 v[56:59], v[72:75], v[174:177], v[56:59]
	v_mfma_i32_16x16x64_i8 v[52:55], v[144:147], v[174:177], v[52:55]
	v_mfma_i32_16x16x64_i8 v[40:43], v[72:75], v[182:185], v[40:43]
	v_mfma_i32_16x16x64_i8 v[36:39], v[144:147], v[182:185], v[36:39]
	v_mfma_i32_16x16x64_i8 v[24:27], v[72:75], v[190:193], v[24:27]
	v_mfma_i32_16x16x64_i8 v[20:23], v[144:147], v[190:193], v[20:23]
	v_mfma_i32_16x16x64_i8 v[8:11], v[72:75], v[198:201], v[8:11]
	v_mfma_i32_16x16x64_i8 v[4:7], v[144:147], v[198:201], v[4:7]
	s_setprio 0
	s_setprio 1
	v_mfma_i32_16x16x64_i8 v[48:51], v[148:151], v[170:173], 0
	v_mfma_i32_16x16x64_i8 v[64:67], v[156:159], v[170:173], 0
	v_mfma_i32_16x16x64_i8 v[32:35], v[148:151], v[178:181], 0
	v_mfma_i32_16x16x64_i8 v[44:47], v[156:159], v[178:181], 0
	v_mfma_i32_16x16x64_i8 v[16:19], v[148:151], v[186:189], 0
	v_mfma_i32_16x16x64_i8 v[28:31], v[156:159], v[186:189], 0
	v_mfma_i32_16x16x64_i8 v[0:3], v[148:151], v[194:197], 0
	v_mfma_i32_16x16x64_i8 v[12:15], v[156:159], v[194:197], 0
	v_mfma_i32_16x16x64_i8 v[48:51], v[152:155], v[174:177], v[48:51]
	v_mfma_i32_16x16x64_i8 v[64:67], v[166:169], v[174:177], v[64:67]
	v_mfma_i32_16x16x64_i8 v[32:35], v[152:155], v[182:185], v[32:35]
	v_mfma_i32_16x16x64_i8 v[44:47], v[166:169], v[182:185], v[44:47]
	v_mfma_i32_16x16x64_i8 v[16:19], v[152:155], v[190:193], v[16:19]
	v_mfma_i32_16x16x64_i8 v[28:31], v[166:169], v[190:193], v[28:31]
	v_mfma_i32_16x16x64_i8 v[0:3], v[152:155], v[198:201], v[0:3]
	v_mfma_i32_16x16x64_i8 v[12:15], v[166:169], v[198:201], v[12:15]
	s_setprio 0
	s_branch .Lzga_r1

; #define PG8_STAGE(bufoff, gbase, voff) do { _Pragma("unroll") for (int _i = 0; _i < 2; ++_i) { const char* gb_ = (const char*)(gbase) + _i * rstep; asm volatile("" : "+s"(gb_));   \
;         __builtin_amdgcn_global_load_lds((const unsigned*)(gb_ + (voff)), (LAS unsigned*)(lds + (bufoff) + ldsw + _i * 8192), 16, 0, 0); } } while (0)
; #define PG8_LDA(dst, b, h) do { _Pragma("unroll") for (int m = 0; m < 4; ++m) _Pragma("unroll") for (int k = 0; k < 2; ++k) dst[m][k] = *(const LAS bf16x8*)(lds + PG8_SA(b, h) + aoff + m * 2048 + k * 1024); } while (0)
; #define PG8_WAIT_V(n) asm volatile("s_waitcnt vmcnt(" #n ")" ::: "memory")
; #define PG8_WAIT_L(n) asm volatile("s_waitcnt lgkmcnt(" #n ")" ::: "memory")
; #define PG8_BAR __builtin_amdgcn_s_barrier()
; template <class Epi, class Sched, bool ALIGN_EPI = true, bool SP2 = true, bool I8 = false, bool F8 = false>
; __device__ __forceinline__ void gemm_phase(LAS unsigned char* lds, const int K, const Sched& S, const Epi& E, const int wave) {
;     ...
;         const bool has_next = S.next(ui + 1, nxt);
;         const char* nA = has_next ? nxt.a : cA; const char* nB = has_next ? nxt.b : cB;
;         for (int t = 0; t < nt; t += 2) {
;             const bool last = (t == nt - 2);
;             const char* a1 = cA + (size_t)(t + 1) * kstep;
;             const char* a2 = last ? nA : cA + (size_t)(t + 2) * kstep; const char* b2 = last ? nB : cB + (size_t)(t + 2) * kstep;
;             const char* a3 = a2 + kstep; const char* b3 = b2 + kstep;
;             if constexpr (SP2) {
;             PG8_LDB(B0, 0, 0); PG8_LDB(B1, 0, 1); PG8_SCHED; PG8_LDA(At, 0, 0); PG8_STAGE(PG8_SA(1, 1), a1 + hstep, voffA);
;             PG8_WAIT_V(8); PG8_WAIT_L(0); PG8_BAR; PG8_MMA(0, 0, At, B0); PG8_MMA(0, 1, At, B1); PG8_BAR; PG8_SCHED;
;             PG8_LDA(At, 0, 1); PG8_STAGE(PG8_SB(0, 0), b2, voffB); PG8_STAGE(PG8_SB(0, 1), b2 + hstep, voffB); PG8_STAGE(PG8_SA(0, 0), a2, voffA);
;             PG8_WAIT_V(8); PG8_WAIT_L(0); PG8_BAR; PG8_MMA(1, 0, At, B0); PG8_MMA(1, 1, At, B1); PG8_BAR; PG8_SCHED;
;     ...
;         if (!(Epi::KEEPS && cur.sub < 2)) {
; #pragma unroll
;         for (int a = 0; a < 2; ++a)
; #pragma unroll
;             for (int b = 0; b < 2; ++b)
; #pragma unroll
;                 for (int m = 0; m < 4; ++m)
; #pragma unroll
;                     for (int n = 0; n < 2; ++n) acc[a][b][m][n] = (acc_t){0, 0, 0, 0};
;         }
.LBB0_445:
	s_add_u32 s13, s24, 0x100
	s_addc_u32 s15, s25, 0
	s_add_u32 s22, s22, 0x30080
	s_addc_u32 s23, s23, 0
	s_mov_b32 s52, -2
.LBB0_446:
	s_add_u32 s24, s22, 0xfffd0080
	s_addc_u32 s25, s23, -1
	s_cmp_eq_u32 s52, 4
	s_cselect_b32 s24, s16, s24
	s_cselect_b32 s25, s17, s25
	s_cselect_b32 s28, s18, s13
	s_cselect_b32 s29, s19, s15
	s_add_u32 s26, s24, 0x80
	s_addc_u32 s27, s25, 0
	s_add_i32 s53, 0, 0x10000
	s_add_i32 s56, 0, 0x14000
	v_add_u32_e32 v144, s53, v162
	v_add_u32_e32 v160, s56, v162
	ds_read_b128 v[68:71], v144
	ds_read_b128 v[72:75], v144 offset:1024
	ds_read_b128 v[76:79], v144 offset:2048
	ds_read_b128 v[144:147], v144 offset:3072
	ds_read_b128 v[148:151], v160
	ds_read_b128 v[152:155], v160 offset:1024
	ds_read_b128 v[156:159], v160 offset:2048
	ds_read_b128 v[166:169], v160 offset:3072
	s_add_u32 s54, s22, 0xffff0000
	s_addc_u32 s55, s23, -1
	ds_read_b128 v[170:173], v163
	ds_read_b128 v[174:177], v163 offset:1024
	ds_read_b128 v[178:181], v163 offset:2048
	ds_read_b128 v[182:185], v163 offset:3072
	ds_read_b128 v[186:189], v163 offset:4096
	ds_read_b128 v[190:193], v163 offset:5120
	ds_read_b128 v[194:197], v163 offset:6144
	ds_read_b128 v[198:201], v163 offset:7168
	s_add_i32 m0, s21, 0xc000
	v_lshl_add_u64 v[160:161], s[54:55], 0, v[142:143]
	s_mov_b64 s[54:55], s[22:23]
	global_load_lds_dwordx4 v[160:161], off
	s_add_i32 m0, s21, 0xe000
	v_lshl_add_u64 v[160:161], s[54:55], 0, v[142:143]
	global_load_lds_dwordx4 v[160:161], off
	s_waitcnt vmcnt(8)
	s_waitcnt lgkmcnt(0)
	s_barrier
	s_setprio 1
	s_waitcnt lgkmcnt(0)
	s_cmp_eq_u32 s52, -2
	s_cbranch_scc1 .Lzga_s0
	v_mfma_i32_16x16x64_i8 v[138:141], v[68:71], v[170:173], v[138:141]
	v_mfma_i32_16x16x64_i8 v[134:137], v[76:79], v[170:173], v[134:137]
	v_mfma_i32_16x16x64_i8 v[122:125], v[68:71], v[178:181], v[122:125]
	v_mfma_i32_16x16x64_i8 v[118:121], v[76:79], v[178:181], v[118:121]
	v_mfma_i32_16x16x64_i8 v[104:107], v[68:71], v[186:189], v[104:107]
	v_mfma_i32_16x16x64_i8 v[100:103], v[76:79], v[186:189], v[100:103]
	v_mfma_i32_16x16x64_i8 v[88:91], v[68:71], v[194:197], v[88:91]
	v_mfma_i32_16x16x64_i8 v[84:87], v[76:79], v[194:197], v[84:87]
	v_mfma_i32_16x16x64_i8 v[138:141], v[72:75], v[174:177], v[138:141]
	v_mfma_i32_16x16x64_i8 v[134:137], v[144:147], v[174:177], v[134:137]
	v_mfma_i32_16x16x64_i8 v[122:125], v[72:75], v[182:185], v[122:125]
	v_mfma_i32_16x16x64_i8 v[118:121], v[144:147], v[182:185], v[118:121]
	v_mfma_i32_16x16x64_i8 v[104:107], v[72:75], v[190:193], v[104:107]
	v_mfma_i32_16x16x64_i8 v[100:103], v[144:147], v[190:193], v[100:103]
	v_mfma_i32_16x16x64_i8 v[88:91], v[72:75], v[198:201], v[88:91]
	v_mfma_i32_16x16x64_i8 v[84:87], v[144:147], v[198:201], v[84:87]
	s_setprio 0
	s_setprio 1
	v_mfma_i32_16x16x64_i8 v[130:133], v[148:151], v[170:173], v[130:133]
	v_mfma_i32_16x16x64_i8 v[60:63], v[156:159], v[170:173], v[60:63]
	v_mfma_i32_16x16x64_i8 v[114:117], v[148:151], v[178:181], v[114:117]
	v_mfma_i32_16x16x64_i8 v[126:129], v[156:159], v[178:181], v[126:129]
	v_mfma_i32_16x16x64_i8 v[96:99], v[148:151], v[186:189], v[96:99]
	v_mfma_i32_16x16x64_i8 v[108:111], v[156:159], v[186:189], v[108:111]
	v_mfma_i32_16x16x64_i8 v[80:83], v[148:151], v[194:197], v[80:83]
	v_mfma_i32_16x16x64_i8 v[92:95], v[156:159], v[194:197], v[92:95]
	v_mfma_i32_16x16x64_i8 v[130:133], v[152:155], v[174:177], v[130:133]
	v_mfma_i32_16x16x64_i8 v[60:63], v[166:169], v[174:177], v[60:63]
	v_mfma_i32_16x16x64_i8 v[114:117], v[152:155], v[182:185], v[114:117]
	v_mfma_i32_16x16x64_i8 v[126:129], v[166:169], v[182:185], v[126:129]
	v_mfma_i32_16x16x64_i8 v[96:99], v[152:155], v[190:193], v[96:99]
	v_mfma_i32_16x16x64_i8 v[108:111], v[166:169], v[190:193], v[108:111]
	v_mfma_i32_16x16x64_i8 v[80:83], v[152:155], v[198:201], v[80:83]
	v_mfma_i32_16x16x64_i8 v[92:95], v[166:169], v[198:201], v[92:95]
	s_setprio 0
.Lzga_r0:
	s_barrier
	s_mov_b64 s[54:55], s[28:29]
	ds_read_b128 v[170:173], v163 offset:16384
	ds_read_b128 v[174:177], v163 offset:17408
	ds_read_b128 v[178:181], v163 offset:18432
	ds_read_b128 v[182:185], v163 offset:19456
	ds_read_b128 v[186:189], v163 offset:20480
	ds_read_b128 v[190:193], v163 offset:21504
	ds_read_b128 v[194:197], v163 offset:22528
	ds_read_b128 v[198:201], v163 offset:23552
	s_add_i32 s53, s53, s40
	v_lshl_add_u64 v[160:161], s[54:55], 0, v[112:113]
	s_add_u32 s54, s28, 0x10000
	s_mov_b32 m0, s53
	s_addc_u32 s55, s29, 0
	global_load_lds_dwordx4 v[160:161], off
	s_add_i32 m0, s53, 0x2000
	v_lshl_add_u64 v[160:161], s[54:55], 0, v[112:113]
	s_add_u32 s54, s28, 0x20000
	s_addc_u32 s55, s29, 0
	global_load_lds_dwordx4 v[160:161], off
	s_add_i32 s53, s56, s40
	v_lshl_add_u64 v[160:161], s[54:55], 0, v[112:113]
	s_add_u32 s54, s28, 0x30000
	s_mov_b32 m0, s53
	s_addc_u32 s55, s29, 0
	global_load_lds_dwordx4 v[160:161], off
	s_add_i32 m0, s53, 0x2000
	v_lshl_add_u64 v[160:161], s[54:55], 0, v[112:113]
	s_mov_b64 s[54:55], s[24:25]
	global_load_lds_dwordx4 v[160:161], off
	s_mov_b32 m0, s21
	v_lshl_add_u64 v[160:161], s[54:55], 0, v[142:143]
	s_add_u32 s54, s24, 0x10000
	s_addc_u32 s55, s25, 0
	global_load_lds_dwordx4 v[160:161], off
	s_mov_b32 m0, s42
	v_lshl_add_u64 v[160:161], s[54:55], 0, v[142:143]
	global_load_lds_dwordx4 v[160:161], off
	s_waitcnt vmcnt(8)
	s_waitcnt lgkmcnt(0)
	s_barrier
	s_setprio 1
	s_waitcnt lgkmcnt(0)
	s_cmp_eq_u32 s52, -2
	s_cbranch_scc1 .Lzga_s1
; #define PG8_STAGE(bufoff, gbase, voff) do { _Pragma("unroll") for (int _i = 0; _i < 2; ++_i) { const char* gb_ = (const char*)(gbase) + _i * rstep; asm volatile("" : "+s"(gb_));   \
;         __builtin_amdgcn_global_load_lds((const unsigned*)(gb_ + (voff)), (LAS unsigned*)(lds + (bufoff) + ldsw + _i * 8192), 16, 0, 0); } } while (0)
; #define PG8_LDA(dst, b, h) do { _Pragma("unroll") for (int m = 0; m < 4; ++m) _Pragma("unroll") for (int k = 0; k < 2; ++k) dst[m][k] = *(const LAS bf16x8*)(lds + PG8_SA(b, h) + aoff + m * 2048 + k * 1024); } while (0)
; #define PG8_LDB(dst, b, h) do { _Pragma("unroll") for (int n = 0; n < 2; ++n) _Pragma("unroll") for (int k = 0; k < 2; ++k) dst[n][k] = *(const LAS bf16x8*)(lds + PG8_SB(b, h) + boff + n * 2048 + k * 1024); } while (0)
; #define PG8_WAIT_V(n) asm volatile("s_waitcnt vmcnt(" #n ")" ::: "memory")
; #define PG8_WAIT_L(n) asm volatile("s_waitcnt lgkmcnt(" #n ")" ::: "memory")
; #define PG8_BAR __builtin_amdgcn_s_barrier()
; #define PG8_SCHED __builtin_amdgcn_sched_barrier(0)
; template <class Epi, class Sched, bool ALIGN_EPI = true, bool SP2 = true, bool I8 = false, bool F8 = false>
; __device__ __forceinline__ void gemm_phase(LAS unsigned char* lds, const int K, const Sched& S, const Epi& E, const int wave) {
;     ...
;             PG8_WAIT_V(8); PG8_WAIT_L(0); PG8_BAR; PG8_MMA(1, 0, At, B0); PG8_MMA(1, 1, At, B1); PG8_BAR; PG8_SCHED;
;             PG8_LDB(B0, 1, 0); PG8_LDB(B1, 1, 1); PG8_SCHED; PG8_LDA(At, 1, 0); PG8_STAGE(PG8_SA(0, 1), a2 + hstep, voffA);
;             PG8_WAIT_V(8); PG8_WAIT_L(0); PG8_BAR; PG8_MMA(0, 0, At, B0); PG8_MMA(0, 1, At, B1); PG8_BAR; PG8_SCHED;
	v_mfma_i32_16x16x64_i8 v[56:59], v[68:71], v[170:173], v[56:59]
	v_mfma_i32_16x16x64_i8 v[52:55], v[76:79], v[170:173], v[52:55]
	v_mfma_i32_16x16x64_i8 v[40:43], v[68:71], v[178:181], v[40:43]
	v_mfma_i32_16x16x64_i8 v[36:39], v[76:79], v[178:181], v[36:39]
	v_mfma_i32_16x16x64_i8 v[24:27], v[68:71], v[186:189], v[24:27]
	v_mfma_i32_16x16x64_i8 v[20:23], v[76:79], v[186:189], v[20:23]
	v_mfma_i32_16x16x64_i8 v[8:11], v[68:71], v[194:197], v[8:11]
	v_mfma_i32_16x16x64_i8 v[4:7], v[76:79], v[194:197], v[4:7]
	v_mfma_i32_16x16x64_i8 v[56:59], v[72:75], v[174:177], v[56:59]
	v_mfma_i32_16x16x64_i8 v[52:55], v[144:147], v[174:177], v[52:55]
	v_mfma_i32_16x16x64_i8 v[40:43], v[72:75], v[182:185], v[40:43]
	v_mfma_i32_16x16x64_i8 v[36:39], v[144:147], v[182:185], v[36:39]
	v_mfma_i32_16x16x64_i8 v[24:27], v[72:75], v[190:193], v[24:27]
	v_mfma_i32_16x16x64_i8 v[20:23], v[144:147], v[190:193], v[20:23]
	v_mfma_i32_16x16x64_i8 v[8:11], v[72:75], v[198:201], v[8:11]
	v_mfma_i32_16x16x64_i8 v[4:7], v[144:147], v[198:201], v[4:7]
	s_setprio 0
	s_setprio 1
	v_mfma_i32_16x16x64_i8 v[48:51], v[148:151], v[170:173], v[48:51]
	v_mfma_i32_16x16x64_i8 v[64:67], v[156:159], v[170:173], v[64:67]
	v_mfma_i32_16x16x64_i8 v[32:35], v[148:151], v[178:181], v[32:35]
	v_mfma_i32_16x16x64_i8 v[44:47], v[156:159], v[178:181], v[44:47]
	v_mfma_i32_16x16x64_i8 v[16:19], v[148:151], v[186:189], v[16:19]
	v_mfma_i32_16x16x64_i8 v[28:31], v[156:159], v[186:189], v[28:31]
	v_mfma_i32_16x16x64_i8 v[0:3], v[148:151], v[194:197], v[0:3]
	v_mfma_i32_16x16x64_i8 v[12:15], v[156:159], v[194:197], v[12:15]
	v_mfma_i32_16x16x64_i8 v[48:51], v[152:155], v[174:177], v[48:51]
	v_mfma_i32_16x16x64_i8 v[64:67], v[166:169], v[174:177], v[64:67]
	v_mfma_i32_16x16x64_i8 v[32:35], v[152:155], v[182:185], v[32:35]
	v_mfma_i32_16x16x64_i8 v[44:47], v[166:169], v[182:185], v[44:47]
	v_mfma_i32_16x16x64_i8 v[16:19], v[152:155], v[190:193], v[16:19]
	v_mfma_i32_16x16x64_i8 v[28:31], v[166:169], v[190:193], v[28:31]
	v_mfma_i32_16x16x64_i8 v[0:3], v[152:155], v[198:201], v[0:3]
	v_mfma_i32_16x16x64_i8 v[12:15], v[166:169], v[198:201], v[12:15]
	s_setprio 0
.Lzga_r1:
	s_barrier
	s_add_i32 s53, 0, 0x18000
	s_add_i32 s56, 0, 0x1c000
	v_add_u32_e32 v144, s53, v162
	v_add_u32_e32 v160, s56, v162
	ds_read_b128 v[68:71], v144
	ds_read_b128 v[72:75], v144 offset:1024
	ds_read_b128 v[76:79], v144 offset:2048
	ds_read_b128 v[144:147], v144 offset:3072
	ds_read_b128 v[148:151], v160
	ds_read_b128 v[152:155], v160 offset:1024
	ds_read_b128 v[156:159], v160 offset:2048
	ds_read_b128 v[166:169], v160 offset:3072
	s_add_u32 s54, s24, 0x20000
	s_addc_u32 s55, s25, 0
	ds_read_b128 v[170:173], v163 offset:32768
	ds_read_b128 v[174:177], v163 offset:33792
	ds_read_b128 v[178:181], v163 offset:34816
	ds_read_b128 v[182:185], v163 offset:35840
	ds_read_b128 v[186:189], v163 offset:36864
	ds_read_b128 v[190:193], v163 offset:37888
	ds_read_b128 v[194:197], v163 offset:38912
	ds_read_b128 v[198:201], v163 offset:39936
	s_mov_b32 m0, s43
	v_lshl_add_u64 v[160:161], s[54:55], 0, v[142:143]
	s_add_u32 s54, s24, 0x30000
	s_addc_u32 s55, s25, 0
	global_load_lds_dwordx4 v[160:161], off
	s_mov_b32 m0, s44
	v_lshl_add_u64 v[160:161], s[54:55], 0, v[142:143]
	global_load_lds_dwordx4 v[160:161], off
	s_waitcnt vmcnt(8)
	s_waitcnt lgkmcnt(0)
	s_barrier
	s_setprio 1
	s_waitcnt lgkmcnt(0)
	v_mfma_i32_16x16x64_i8 v[138:141], v[68:71], v[170:173], v[138:141]
	v_mfma_i32_16x16x64_i8 v[134:137], v[76:79], v[170:173], v[134:137]
	v_mfma_i32_16x16x64_i8 v[122:125], v[68:71], v[178:181], v[122:125]
	v_mfma_i32_16x16x64_i8 v[118:121], v[76:79], v[178:181], v[118:121]
	v_mfma_i32_16x16x64_i8 v[104:107], v[68:71], v[186:189], v[104:107]
	v_mfma_i32_16x16x64_i8 v[100:103], v[76:79], v[186:189], v[100:103]
	v_mfma_i32_16x16x64_i8 v[88:91], v[68:71], v[194:197], v[88:91]
	v_mfma_i32_16x16x64_i8 v[84:87], v[76:79], v[194:197], v[84:87]
	v_mfma_i32_16x16x64_i8 v[138:141], v[72:75], v[174:177], v[138:141]
	v_mfma_i32_16x16x64_i8 v[134:137], v[144:147], v[174:177], v[134:137]
	v_mfma_i32_16x16x64_i8 v[122:125], v[72:75], v[182:185], v[122:125]
	v_mfma_i32_16x16x64_i8 v[118:121], v[144:147], v[182:185], v[118:121]
	v_mfma_i32_16x16x64_i8 v[104:107], v[72:75], v[190:193], v[104:107]
	v_mfma_i32_16x16x64_i8 v[100:103], v[144:147], v[190:193], v[100:103]
	v_mfma_i32_16x16x64_i8 v[88:91], v[72:75], v[198:201], v[88:91]
	v_mfma_i32_16x16x64_i8 v[84:87], v[144:147], v[198:201], v[84:87]
	s_setprio 0
	s_setprio 1
	v_mfma_i32_16x16x64_i8 v[130:133], v[148:151], v[170:173], v[130:133]
	v_mfma_i32_16x16x64_i8 v[60:63], v[156:159], v[170:173], v[60:63]
	v_mfma_i32_16x16x64_i8 v[114:117], v[148:151], v[178:181], v[114:117]
	v_mfma_i32_16x16x64_i8 v[126:129], v[156:159], v[178:181], v[126:129]
	v_mfma_i32_16x16x64_i8 v[96:99], v[148:151], v[186:189], v[96:99]
	v_mfma_i32_16x16x64_i8 v[108:111], v[156:159], v[186:189], v[108:111]
	v_mfma_i32_16x16x64_i8 v[80:83], v[148:151], v[194:197], v[80:83]
	v_mfma_i32_16x16x64_i8 v[92:95], v[156:159], v[194:197], v[92:95]
	v_mfma_i32_16x16x64_i8 v[130:133], v[152:155], v[174:177], v[130:133]
	v_mfma_i32_16x16x64_i8 v[60:63], v[166:169], v[174:177], v[60:63]
	v_mfma_i32_16x16x64_i8 v[114:117], v[152:155], v[182:185], v[114:117]
	v_mfma_i32_16x16x64_i8 v[126:129], v[166:169], v[182:185], v[126:129]
	v_mfma_i32_16x16x64_i8 v[96:99], v[152:155], v[190:193], v[96:99]
	v_mfma_i32_16x16x64_i8 v[108:111], v[166:169], v[190:193], v[108:111]
	v_mfma_i32_16x16x64_i8 v[80:83], v[152:155], v[198:201], v[80:83]
	v_mfma_i32_16x16x64_i8 v[92:95], v[166:169], v[198:201], v[92:95]
	s_setprio 0
	s_barrier
; #define PG8_STAGE(bufoff, gbase, voff) do { _Pragma("unroll") for (int _i = 0; _i < 2; ++_i) { const char* gb_ = (const char*)(gbase) + _i * rstep; asm volatile("" : "+s"(gb_));   \
;         __builtin_amdgcn_global_load_lds((const unsigned*)(gb_ + (voff)), (LAS unsigned*)(lds + (bufoff) + ldsw + _i * 8192), 16, 0, 0); } } while (0)
; #define PG8_LDA(dst, b, h) do { _Pragma("unroll") for (int m = 0; m < 4; ++m) _Pragma("unroll") for (int k = 0; k < 2; ++k) dst[m][k] = *(const LAS bf16x8*)(lds + PG8_SA(b, h) + aoff + m * 2048 + k * 1024); } while (0)
; #define PG8_WAIT_V(n) asm volatile("s_waitcnt vmcnt(" #n ")" ::: "memory")
; #define PG8_WAIT_L(n) asm volatile("s_waitcnt lgkmcnt(" #n ")" ::: "memory")
; #define PG8_BAR __builtin_amdgcn_s_barrier()
; #define PG8_SCHED __builtin_amdgcn_sched_barrier(0)
; template <class Epi, class Sched, bool ALIGN_EPI = true, bool SP2 = true, bool I8 = false, bool F8 = false>
; __device__ __forceinline__ void gemm_phase(LAS unsigned char* lds, const int K, const Sched& S, const Epi& E, const int wave) {
;     ...
;         for (int t = 0; t < nt; t += 2) {
;             const bool last = (t == nt - 2);
;     ...
;             PG8_LDA(At, 1, 1); PG8_STAGE(PG8_SB(1, 0), b3, voffB); PG8_STAGE(PG8_SB(1, 1), b3 + hstep, voffB); PG8_STAGE(PG8_SA(1, 0), a3, voffA);
;             PG8_WAIT_V(8); PG8_WAIT_L(0); PG8_BAR; PG8_MMA(1, 0, At, B0); PG8_MMA(1, 1, At, B1); PG8_BAR; PG8_SCHED;
	s_add_u32 s54, s28, 0x80
	s_addc_u32 s55, s29, 0
	ds_read_b128 v[170:173], v163 offset:49152
	ds_read_b128 v[174:177], v163 offset:50176
	ds_read_b128 v[178:181], v163 offset:51200
	ds_read_b128 v[182:185], v163 offset:52224
	ds_read_b128 v[186:189], v163 offset:53248
	ds_read_b128 v[190:193], v163 offset:54272
	ds_read_b128 v[194:197], v163 offset:55296
	ds_read_b128 v[198:201], v163 offset:56320
	s_add_i32 s53, s53, s40
	v_lshl_add_u64 v[160:161], s[54:55], 0, v[112:113]
	s_add_u32 s54, s28, 0x10080
	s_mov_b32 m0, s53
	s_addc_u32 s55, s29, 0
	global_load_lds_dwordx4 v[160:161], off
	s_add_i32 m0, s53, 0x2000
	v_lshl_add_u64 v[160:161], s[54:55], 0, v[112:113]
	s_add_u32 s54, s28, 0x20080
	s_addc_u32 s55, s29, 0
	s_add_i32 s53, s56, s40
	global_load_lds_dwordx4 v[160:161], off
	s_mov_b32 m0, s53
	v_lshl_add_u64 v[160:161], s[54:55], 0, v[112:113]
	s_add_u32 s28, s28, 0x30080
	global_load_lds_dwordx4 v[160:161], off
	s_addc_u32 s29, s29, 0
	s_add_i32 m0, s53, 0x2000
	s_add_u32 s24, s24, 0x10080
	v_lshl_add_u64 v[160:161], s[28:29], 0, v[112:113]
	global_load_lds_dwordx4 v[160:161], off
	s_mov_b32 m0, s47
	v_lshl_add_u64 v[160:161], s[26:27], 0, v[142:143]
	s_addc_u32 s25, s25, 0
	global_load_lds_dwordx4 v[160:161], off
	s_mov_b32 m0, s48
	v_lshl_add_u64 v[160:161], s[24:25], 0, v[142:143]
	global_load_lds_dwordx4 v[160:161], off
	s_waitcnt vmcnt(8)
	s_waitcnt lgkmcnt(0)
	s_barrier
	s_setprio 1
	s_waitcnt lgkmcnt(0)
	v_mfma_i32_16x16x64_i8 v[56:59], v[68:71], v[170:173], v[56:59]
	v_mfma_i32_16x16x64_i8 v[52:55], v[76:79], v[170:173], v[52:55]
	v_mfma_i32_16x16x64_i8 v[40:43], v[68:71], v[178:181], v[40:43]
	v_mfma_i32_16x16x64_i8 v[36:39], v[76:79], v[178:181], v[36:39]
	v_mfma_i32_16x16x64_i8 v[24:27], v[68:71], v[186:189], v[24:27]
	v_mfma_i32_16x16x64_i8 v[20:23], v[76:79], v[186:189], v[20:23]
	v_mfma_i32_16x16x64_i8 v[8:11], v[68:71], v[194:197], v[8:11]
	v_mfma_i32_16x16x64_i8 v[4:7], v[76:79], v[194:197], v[4:7]
	v_mfma_i32_16x16x64_i8 v[56:59], v[72:75], v[174:177], v[56:59]
	v_mfma_i32_16x16x64_i8 v[52:55], v[144:147], v[174:177], v[52:55]
	v_mfma_i32_16x16x64_i8 v[40:43], v[72:75], v[182:185], v[40:43]
	v_mfma_i32_16x16x64_i8 v[36:39], v[144:147], v[182:185], v[36:39]
	v_mfma_i32_16x16x64_i8 v[24:27], v[72:75], v[190:193], v[24:27]
	v_mfma_i32_16x16x64_i8 v[20:23], v[144:147], v[190:193], v[20:23]
	v_mfma_i32_16x16x64_i8 v[8:11], v[72:75], v[198:201], v[8:11]
	v_mfma_i32_16x16x64_i8 v[4:7], v[144:147], v[198:201], v[4:7]
	s_setprio 0
	s_setprio 1
	v_mfma_i32_16x16x64_i8 v[48:51], v[148:151], v[170:173], v[48:51]
	v_mfma_i32_16x16x64_i8 v[64:67], v[156:159], v[170:173], v[64:67]
	v_mfma_i32_16x16x64_i8 v[32:35], v[148:151], v[178:181], v[32:35]
	v_mfma_i32_16x16x64_i8 v[44:47], v[156:159], v[178:181], v[44:47]
	v_mfma_i32_16x16x64_i8 v[16:19], v[148:151], v[186:189], v[16:19]
	v_mfma_i32_16x16x64_i8 v[28:31], v[156:159], v[186:189], v[28:31]
	v_mfma_i32_16x16x64_i8 v[0:3], v[148:151], v[194:197], v[0:3]
	v_mfma_i32_16x16x64_i8 v[12:15], v[156:159], v[194:197], v[12:15]
	v_mfma_i32_16x16x64_i8 v[48:51], v[152:155], v[174:177], v[48:51]
	v_mfma_i32_16x16x64_i8 v[64:67], v[166:169], v[174:177], v[64:67]
	v_mfma_i32_16x16x64_i8 v[32:35], v[152:155], v[182:185], v[32:35]
	v_mfma_i32_16x16x64_i8 v[44:47], v[166:169], v[182:185], v[44:47]
	v_mfma_i32_16x16x64_i8 v[16:19], v[152:155], v[190:193], v[16:19]
	v_mfma_i32_16x16x64_i8 v[28:31], v[166:169], v[190:193], v[28:31]
	v_mfma_i32_16x16x64_i8 v[0:3], v[152:155], v[198:201], v[0:3]
	v_mfma_i32_16x16x64_i8 v[12:15], v[166:169], v[198:201], v[12:15]
	s_setprio 0
	s_barrier
	s_add_i32 s52, s52, 2
	s_add_u32 s13, s13, 0x100
	s_addc_u32 s15, s15, 0
	s_add_u32 s22, s22, 0x100
	s_addc_u32 s23, s23, 0
	s_cmp_gt_u32 s52, 5
	s_cbranch_scc0 .LBB0_446
	s_and_b64 vcc, exec, s[36:37]
	s_cbranch_vccz .LBB0_449
	s_barrier

; #define LAS __attribute__((address_space(3)))
; __device__ __forceinline__ void moba_unit(const MobaArgs& A, int b, int h, int qb, LAS unsigned char* lds, int wave, bool tables) {
;     ...
;             if (near) {
;                 const LAS float* lp = lut + (LUTA_TOP - qpos + kt0 + 4 * hi);
; #pragma unroll
;                 for (int r = 0; r < 16; ++r) { const int c = (r & 3) + 8 * (r >> 2); a0[r] += lp[c]; a1[r] += lp[c + 32]; b0[r] += lp[c + 64]; b1[r] += lp[c + 96]; }
;                 if (own && kt0 + 127 > qmin) {
;                     const int lim = qpos - kt0 - 4 * hi;
; #pragma unroll
;                     for (int r = 0; r < 16; ++r) { const int c = (r & 3) + 8 * (r >> 2); if (c > lim) a0[r] = NEG; if (c + 32 > lim) a1[r] = NEG; if (c + 64 > lim) b0[r] = NEG; if (c + 96 > lim) b1[r] = NEG; }
;                 }
.LBB0_667:
	s_andn2_b64 vcc, exec, s[10:11]
	s_cbranch_vccnz .LBB0_670
	v_sub_u32_e32 v140, s16, v134
	v_lshl_add_u32 v167, v140, 2, v166
	v_add_u32_e32 v167, 0x10fc, v167
	ds_read2_b32 v[168:169], v167 offset1:1
	ds_read2_b32 v[170:171], v167 offset0:32 offset1:33
	ds_read2_b32 v[172:173], v167 offset0:64 offset1:65
	ds_read2_b32 v[140:141], v167 offset0:96 offset1:97
	ds_read2_b32 v[174:175], v167 offset0:2 offset1:3
	ds_read2_b32 v[176:177], v167 offset0:34 offset1:35
	ds_read2_b32 v[178:179], v167 offset0:66 offset1:67
	ds_read2_b32 v[142:143], v167 offset0:98 offset1:99
	ds_read2_b32 v[180:181], v167 offset0:8 offset1:9
	ds_read2_b32 v[182:183], v167 offset0:40 offset1:41
	ds_read2_b32 v[184:185], v167 offset0:72 offset1:73
	ds_read2_b32 v[144:145], v167 offset0:104 offset1:105
	ds_read2_b32 v[186:187], v167 offset0:10 offset1:11
	ds_read2_b32 v[188:189], v167 offset0:42 offset1:43
	ds_read2_b32 v[190:191], v167 offset0:74 offset1:75
	ds_read2_b32 v[146:147], v167 offset0:106 offset1:107
	ds_read2_b32 v[192:193], v167 offset0:16 offset1:17
	ds_read2_b32 v[194:195], v167 offset0:48 offset1:49
	ds_read2_b32 v[196:197], v167 offset0:80 offset1:81
	ds_read2_b32 v[148:149], v167 offset0:112 offset1:113
	ds_read2_b32 v[198:199], v167 offset0:18 offset1:19
	ds_read2_b32 v[200:201], v167 offset0:50 offset1:51
	ds_read2_b32 v[202:203], v167 offset0:82 offset1:83
	ds_read2_b32 v[150:151], v167 offset0:114 offset1:115
	ds_read2_b32 v[204:205], v167 offset0:24 offset1:25
	ds_read2_b32 v[206:207], v167 offset0:56 offset1:57
	ds_read2_b32 v[208:209], v167 offset0:88 offset1:89
	ds_read2_b32 v[152:153], v167 offset0:120 offset1:121
	ds_read2_b32 v[210:211], v167 offset0:26 offset1:27
	s_waitcnt lgkmcnt(0)
	v_pk_add_f32 v[80:81], v[80:81], v[168:169]
	ds_read2_b32 v[168:169], v167 offset0:58 offset1:59
	s_cmp_ge_i32 s96, s17
	s_cselect_b64 s[6:7], -1, 0
	s_waitcnt lgkmcnt(0)
	v_pk_add_f32 v[78:79], v[78:79], v[168:169]
	ds_read2_b32 v[168:169], v167 offset0:90 offset1:91
	s_xor_b64 s[8:9], s[8:9], -1
	s_or_b64 s[6:7], s[8:9], s[6:7]
	v_pk_add_f32 v[92:93], v[92:93], v[204:205]
	v_pk_add_f32 v[90:91], v[90:91], v[198:199]
	s_waitcnt lgkmcnt(0)
	v_pk_add_f32 v[110:111], v[110:111], v[168:169]
	ds_read2_b32 v[168:169], v167 offset0:122 offset1:123
	v_pk_add_f32 v[94:95], v[94:95], v[210:211]
	v_pk_add_f32 v[88:89], v[88:89], v[192:193]
	v_pk_add_f32 v[86:87], v[86:87], v[186:187]
	v_pk_add_f32 v[84:85], v[84:85], v[180:181]
	v_pk_add_f32 v[82:83], v[82:83], v[174:175]
	v_pk_add_f32 v[76:77], v[76:77], v[206:207]
	v_pk_add_f32 v[74:75], v[74:75], v[200:201]
	v_pk_add_f32 v[72:73], v[72:73], v[194:195]
	v_pk_add_f32 v[70:71], v[70:71], v[188:189]
	v_pk_add_f32 v[68:69], v[68:69], v[182:183]
	v_pk_add_f32 v[66:67], v[66:67], v[176:177]
	v_pk_add_f32 v[64:65], v[64:65], v[170:171]
	v_pk_add_f32 v[108:109], v[108:109], v[208:209]
	v_pk_add_f32 v[106:107], v[106:107], v[202:203]
	v_pk_add_f32 v[104:105], v[104:105], v[196:197]
	v_pk_add_f32 v[102:103], v[102:103], v[190:191]
	v_pk_add_f32 v[100:101], v[100:101], v[184:185]
	v_pk_add_f32 v[98:99], v[98:99], v[178:179]
	v_pk_add_f32 v[96:97], v[96:97], v[172:173]
	s_waitcnt lgkmcnt(0)
	v_pk_add_f32 v[62:63], v[62:63], v[168:169]
	v_pk_add_f32 v[60:61], v[60:61], v[152:153]
	v_pk_add_f32 v[58:59], v[58:59], v[150:151]
	v_pk_add_f32 v[56:57], v[56:57], v[148:149]
	v_pk_add_f32 v[54:55], v[54:55], v[146:147]
	v_pk_add_f32 v[52:53], v[52:53], v[144:145]
	v_pk_add_f32 v[50:51], v[50:51], v[142:143]
	v_pk_add_f32 v[48:49], v[48:49], v[140:141]
	s_and_b64 vcc, exec, s[6:7]
	s_cbranch_vccnz .LBB0_670
	v_add_u32_e32 v140, s16, v160
	v_sub_u32_e32 v140, v134, v140
	v_cmp_gt_i32_e64 s[44:45], 26, v140
	v_cmp_gt_i32_e64 s[60:61], 27, v140
	s_and_b64 s[44:45], s[60:61], s[44:45]
	v_cndmask_b32_e64 v94, v94, v252, s[44:45]
	v_cndmask_b32_e64 v95, v95, v252, s[60:61]
	v_cmp_gt_i32_e64 s[60:61], 25, v140
	s_and_b64 s[44:45], s[44:45], s[60:61]
	v_cmp_gt_i32_e64 s[60:61], 24, v140
	v_cndmask_b32_e64 v93, v93, v252, s[44:45]
	s_and_b64 s[44:45], s[44:45], s[60:61]
	v_cmp_gt_i32_e64 s[60:61], 19, v140
	v_cndmask_b32_e64 v92, v92, v252, s[44:45]
	s_and_b64 s[44:45], s[44:45], s[60:61]
	v_cmp_gt_i32_e64 s[60:61], 18, v140
	v_cndmask_b32_e64 v91, v91, v252, s[44:45]
	s_and_b64 s[44:45], s[44:45], s[60:61]
	v_cmp_gt_i32_e64 s[60:61], 17, v140
	v_cndmask_b32_e64 v90, v90, v252, s[44:45]
	s_and_b64 s[44:45], s[44:45], s[60:61]
	v_cmp_gt_i32_e64 s[60:61], 16, v140
	v_cndmask_b32_e64 v89, v89, v252, s[44:45]
	s_and_b64 s[44:45], s[44:45], s[60:61]
	v_cmp_gt_i32_e64 s[60:61], 11, v140
	v_cmp_gt_i32_e64 s[28:29], 10, v140
	s_and_b64 s[60:61], s[44:45], s[60:61]
	v_cmp_gt_i32_e64 s[58:59], 9, v140
	v_cndmask_b32_e64 v87, v87, v252, s[60:61]
	s_and_b64 s[60:61], s[60:61], s[28:29]
	v_cmp_gt_i32_e64 s[50:51], 8, v140
	v_cndmask_b32_e64 v86, v86, v252, s[60:61]
	s_and_b64 s[60:61], s[60:61], s[58:59]
	v_cmp_gt_i32_e64 s[36:37], 3, v140
	v_cndmask_b32_e64 v85, v85, v252, s[60:61]
	s_and_b64 s[60:61], s[60:61], s[50:51]
	v_cmp_gt_i32_e64 s[56:57], 2, v140
	v_cndmask_b32_e64 v84, v84, v252, s[60:61]
	s_and_b64 s[60:61], s[60:61], s[36:37]
	v_cmp_gt_i32_e64 s[52:53], 1, v140
	v_cndmask_b32_e64 v83, v83, v252, s[60:61]
	s_and_b64 s[60:61], s[60:61], s[56:57]
	v_cmp_gt_i32_e64 s[54:55], 0, v140
	v_cndmask_b32_e64 v82, v82, v252, s[60:61]
	s_and_b64 s[60:61], s[60:61], s[52:53]
	s_and_b64 s[54:55], s[60:61], s[54:55]
	v_cndmask_b32_e64 v81, v81, v252, s[60:61]
	v_cmp_gt_i32_e64 s[60:61], 58, v140
	v_cndmask_b32_e64 v80, v80, v252, s[54:55]
	v_cmp_gt_i32_e64 s[54:55], 59, v140
	v_cmp_gt_i32_e64 s[56:57], 48, v140
	v_cmp_gt_i32_e64 s[58:59], 43, v140
; __device__ __forceinline__ void moba_unit(const MobaArgs& A, int b, int h, int qb, LAS unsigned char* lds, int wave, bool tables) {
;     ...
;                 if (own && kt0 + 127 > qmin) {
;                     const int lim = qpos - kt0 - 4 * hi;
; #pragma unroll
;                     for (int r = 0; r < 16; ++r) { const int c = (r & 3) + 8 * (r >> 2); if (c > lim) a0[r] = NEG; if (c + 32 > lim) a1[r] = NEG; if (c + 64 > lim) b0[r] = NEG; if (c + 96 > lim) b1[r] = NEG; }
;                 }
	v_cndmask_b32_e64 v79, v79, v252, s[54:55]
	s_and_b64 s[54:55], s[54:55], s[60:61]
	v_cmp_gt_i32_e64 s[60:61], 57, v140
	v_cndmask_b32_e64 v78, v78, v252, s[54:55]
	s_and_b64 s[54:55], s[54:55], s[60:61]
	v_cmp_gt_i32_e64 s[60:61], 56, v140
	v_cndmask_b32_e64 v77, v77, v252, s[54:55]
	s_and_b64 s[54:55], s[54:55], s[60:61]
	v_cmp_gt_i32_e64 s[60:61], 51, v140
	v_cndmask_b32_e64 v76, v76, v252, s[54:55]
	s_and_b64 s[54:55], s[54:55], s[60:61]
	v_cmp_gt_i32_e64 s[60:61], 50, v140
	v_cndmask_b32_e64 v75, v75, v252, s[54:55]
	s_and_b64 s[54:55], s[54:55], s[60:61]
	v_cmp_gt_i32_e64 s[60:61], 49, v140
	s_and_b64 s[60:61], s[54:55], s[60:61]
	s_and_b64 s[56:57], s[60:61], s[56:57]
	v_cmp_gt_i32_e64 s[48:49], 42, v140
	s_and_b64 s[58:59], s[56:57], s[58:59]
	v_cmp_gt_i32_e64 s[46:47], 41, v140
	v_cndmask_b32_e64 v71, v71, v252, s[58:59]
	s_and_b64 s[58:59], s[58:59], s[48:49]
	v_cmp_gt_i32_e64 s[42:43], 40, v140
	v_cndmask_b32_e64 v70, v70, v252, s[58:59]
	s_and_b64 s[58:59], s[58:59], s[46:47]
	v_cmp_gt_i32_e64 s[40:41], 35, v140
	v_cndmask_b32_e64 v69, v69, v252, s[58:59]
	s_and_b64 s[58:59], s[58:59], s[42:43]
	v_cmp_gt_i32_e64 s[38:39], 34, v140
	v_cndmask_b32_e64 v68, v68, v252, s[58:59]
	s_and_b64 s[58:59], s[58:59], s[40:41]
	v_cmp_gt_i32_e64 s[34:35], 33, v140
	s_and_b64 s[38:39], s[58:59], s[38:39]
	v_cmp_gt_i32_e64 s[30:31], 32, v140
	v_cndmask_b32_e64 v66, v66, v252, s[38:39]
	s_and_b64 s[38:39], s[38:39], s[34:35]
	s_and_b64 s[30:31], s[38:39], s[30:31]
	v_cndmask_b32_e64 v65, v65, v252, s[38:39]
	s_movk_i32 s38, 0x5a
	v_cndmask_b32_e64 v64, v64, v252, s[30:31]
	s_movk_i32 s30, 0x5b
	v_cmp_gt_i32_e64 s[38:39], s38, v140
	v_cmp_gt_i32_e64 s[30:31], s30, v140
	v_cndmask_b32_e64 v67, v67, v252, s[58:59]
	s_movk_i32 s58, 0x58
	v_cndmask_b32_e64 v111, v111, v252, s[30:31]
	s_and_b64 s[30:31], s[30:31], s[38:39]
	s_movk_i32 s38, 0x59
	v_cmp_gt_i32_e64 s[38:39], s38, v140
	s_movk_i32 s42, 0x53
	v_cmp_gt_i32_e64 s[58:59], s58, v140
	v_cndmask_b32_e64 v110, v110, v252, s[30:31]
	s_and_b64 s[30:31], s[30:31], s[38:39]
	s_movk_i32 s48, 0x52
	v_cmp_gt_i32_e64 s[42:43], s42, v140
	v_cndmask_b32_e64 v109, v109, v252, s[30:31]
	s_and_b64 s[30:31], s[30:31], s[58:59]
	v_cndmask_b32_e64 v73, v73, v252, s[60:61]
	s_movk_i32 s60, 0x51
	v_cmp_gt_i32_e64 s[48:49], s48, v140
	v_cndmask_b32_e64 v108, v108, v252, s[30:31]
	s_and_b64 s[30:31], s[30:31], s[42:43]
	s_movk_i32 s52, 0x50
	v_cmp_gt_i32_e64 s[60:61], s60, v140
	v_cndmask_b32_e64 v107, v107, v252, s[30:31]
	s_and_b64 s[30:31], s[30:31], s[48:49]
	s_movk_i32 s50, 0x4b
	v_cmp_gt_i32_e64 s[52:53], s52, v140
	v_cndmask_b32_e64 v106, v106, v252, s[30:31]
	s_and_b64 s[30:31], s[30:31], s[60:61]
	v_cndmask_b32_e64 v88, v88, v252, s[44:45]
	s_movk_i32 s44, 0x4a
	v_cmp_gt_i32_e64 s[50:51], s50, v140
	v_cndmask_b32_e64 v105, v105, v252, s[30:31]
	s_and_b64 s[30:31], s[30:31], s[52:53]
	s_movk_i32 s14, 0x49
	v_cmp_gt_i32_e64 s[44:45], s44, v140
	v_cndmask_b32_e64 v104, v104, v252, s[30:31]
	s_and_b64 s[30:31], s[30:31], s[50:51]
	s_movk_i32 s12, 0x48
	v_cmp_gt_i32_e64 s[26:27], s14, v140
	v_cndmask_b32_e64 v103, v103, v252, s[30:31]
	s_and_b64 s[30:31], s[30:31], s[44:45]
	s_movk_i32 s10, 0x43
	v_cmp_gt_i32_e64 s[24:25], s12, v140
	s_and_b64 s[26:27], s[30:31], s[26:27]
	s_movk_i32 s6, 0x60
	s_movk_i32 s8, 0x42
	v_cmp_gt_i32_e64 s[22:23], s10, v140
	s_and_b64 s[24:25], s[26:27], s[24:25]
	v_cmp_gt_i32_e32 vcc, s6, v140
	s_movk_i32 s6, 0x41
	v_cmp_gt_i32_e64 s[20:21], s8, v140
	s_and_b64 s[22:23], s[24:25], s[22:23]
	v_cmp_gt_i32_e64 s[18:19], s6, v140
	s_and_b64 s[20:21], s[22:23], s[20:21]
	v_cmp_gt_i32_e64 s[16:17], 64, v140
	s_and_b64 s[18:19], s[20:21], s[18:19]
	s_and_b64 s[16:17], s[18:19], s[16:17]
	s_movk_i32 s58, 0x7a
	v_cndmask_b32_e64 v96, v96, v252, s[16:17]
	s_movk_i32 s16, 0x7b
	s_movk_i32 s38, 0x79
	v_cmp_gt_i32_e64 s[58:59], s58, v140
	v_cmp_gt_i32_e64 s[16:17], s16, v140
	s_movk_i32 s34, 0x78
	v_cmp_gt_i32_e64 s[38:39], s38, v140
	v_cndmask_b32_e64 v63, v63, v252, s[16:17]
	s_and_b64 s[16:17], s[16:17], s[58:59]
	s_movk_i32 s40, 0x73
	v_cmp_gt_i32_e64 s[34:35], s34, v140
	v_cndmask_b32_e64 v62, v62, v252, s[16:17]
	s_and_b64 s[16:17], s[16:17], s[38:39]
	s_movk_i32 s46, 0x72
	v_cmp_gt_i32_e64 s[40:41], s40, v140
	v_cndmask_b32_e64 v61, v61, v252, s[16:17]
	s_and_b64 s[16:17], s[16:17], s[34:35]
	v_cndmask_b32_e64 v72, v72, v252, s[56:57]
	s_movk_i32 s56, 0x71
	v_cmp_gt_i32_e64 s[46:47], s46, v140
	v_cndmask_b32_e64 v60, v60, v252, s[16:17]
	s_and_b64 s[16:17], s[16:17], s[40:41]
	v_cndmask_b32_e64 v74, v74, v252, s[54:55]
	s_movk_i32 s54, 0x70
	v_cmp_gt_i32_e64 s[56:57], s56, v140
	v_cndmask_b32_e64 v59, v59, v252, s[16:17]
	s_and_b64 s[16:17], s[16:17], s[46:47]
	s_movk_i32 s36, 0x6b
	v_cmp_gt_i32_e64 s[54:55], s54, v140
	v_cndmask_b32_e64 v58, v58, v252, s[16:17]
	s_and_b64 s[16:17], s[16:17], s[56:57]
	s_movk_i32 s28, 0x6a
	v_cmp_gt_i32_e64 s[36:37], s36, v140
	v_cndmask_b32_e64 v57, v57, v252, s[16:17]
	s_and_b64 s[16:17], s[16:17], s[54:55]
	s_movk_i32 s14, 0x69
	v_cmp_gt_i32_e64 s[28:29], s28, v140
	v_cndmask_b32_e64 v56, v56, v252, s[16:17]
	s_and_b64 s[16:17], s[16:17], s[36:37]
	s_movk_i32 s12, 0x68
	v_cmp_gt_i32_e64 s[14:15], s14, v140
	v_cndmask_b32_e64 v55, v55, v252, s[16:17]
	s_and_b64 s[16:17], s[16:17], s[28:29]
	s_movk_i32 s10, 0x63
	v_cmp_gt_i32_e64 s[12:13], s12, v140
	s_and_b64 s[14:15], s[16:17], s[14:15]
	s_movk_i32 s8, 0x62
	v_cmp_gt_i32_e64 s[10:11], s10, v140
	s_and_b64 s[12:13], s[14:15], s[12:13]
	s_movk_i32 s6, 0x61
	v_cmp_gt_i32_e64 s[8:9], s8, v140
	s_and_b64 s[10:11], s[12:13], s[10:11]
	v_cmp_gt_i32_e64 s[6:7], s6, v140
	s_and_b64 s[8:9], s[10:11], s[8:9]
	s_and_b64 s[6:7], s[8:9], s[6:7]
	s_and_b64 vcc, s[6:7], vcc
	s_mov_b32 s61, 0xe000
	s_mov_b32 s60, 0xc000
	v_cndmask_b32_e64 v102, v102, v252, s[30:31]
	v_cndmask_b32_e64 v101, v101, v252, s[26:27]
	v_cndmask_b32_e64 v100, v100, v252, s[24:25]
	v_cndmask_b32_e64 v99, v99, v252, s[22:23]
	v_cndmask_b32_e64 v98, v98, v252, s[20:21]
	v_cndmask_b32_e64 v97, v97, v252, s[18:19]
	v_cndmask_b32_e64 v54, v54, v252, s[16:17]
	v_cndmask_b32_e64 v53, v53, v252, s[14:15]
	v_cndmask_b32_e64 v52, v52, v252, s[12:13]
	v_cndmask_b32_e64 v51, v51, v252, s[10:11]
	v_cndmask_b32_e64 v50, v50, v252, s[8:9]
	v_cndmask_b32_e64 v49, v49, v252, s[6:7]
	v_cndmask_b32_e32 v48, v48, v252, vcc

; #define LAS __attribute__((address_space(3)))
; __device__ __forceinline__ void moba_unit(const MobaArgs& A, int b, int h, int qb, LAS unsigned char* lds, int wave, bool tables) {
;     ...
;             if (near) {
;                 const LAS float* lp = lut + (LUTA_TOP - qpos + kt0 + 4 * hi);
; #pragma unroll
;                 for (int r = 0; r < 16; ++r) { const int c = (r & 3) + 8 * (r >> 2); a0[r] += lp[c]; a1[r] += lp[c + 32]; b0[r] += lp[c + 64]; b1[r] += lp[c + 96]; }
;                 if (own && kt0 + 127 > qmin) {
;                     const int lim = qpos - kt0 - 4 * hi;
; #pragma unroll
;                     for (int r = 0; r < 16; ++r) { const int c = (r & 3) + 8 * (r >> 2); if (c > lim) a0[r] = NEG; if (c + 32 > lim) a1[r] = NEG; if (c + 64 > lim) b0[r] = NEG; if (c + 96 > lim) b1[r] = NEG; }
;                 }
.LBB0_745:
	s_andn2_b64 vcc, exec, s[10:11]
	s_cbranch_vccnz .LBB0_748
	v_sub_u32_e32 v138, s16, v132
	v_lshl_add_u32 v167, v138, 2, v166
	v_add_u32_e32 v167, 0x10fc, v167
	ds_read2_b32 v[168:169], v167 offset1:1
	ds_read2_b32 v[170:171], v167 offset0:32 offset1:33
	ds_read2_b32 v[172:173], v167 offset0:64 offset1:65
	ds_read2_b32 v[138:139], v167 offset0:96 offset1:97
	ds_read2_b32 v[174:175], v167 offset0:2 offset1:3
	ds_read2_b32 v[176:177], v167 offset0:34 offset1:35
	ds_read2_b32 v[178:179], v167 offset0:66 offset1:67
	ds_read2_b32 v[140:141], v167 offset0:98 offset1:99
	ds_read2_b32 v[180:181], v167 offset0:8 offset1:9
	ds_read2_b32 v[182:183], v167 offset0:40 offset1:41
	ds_read2_b32 v[184:185], v167 offset0:72 offset1:73
	ds_read2_b32 v[142:143], v167 offset0:104 offset1:105
	ds_read2_b32 v[186:187], v167 offset0:10 offset1:11
	ds_read2_b32 v[188:189], v167 offset0:42 offset1:43
	ds_read2_b32 v[190:191], v167 offset0:74 offset1:75
	ds_read2_b32 v[144:145], v167 offset0:106 offset1:107
	ds_read2_b32 v[192:193], v167 offset0:16 offset1:17
	ds_read2_b32 v[194:195], v167 offset0:48 offset1:49
	ds_read2_b32 v[196:197], v167 offset0:80 offset1:81
	ds_read2_b32 v[146:147], v167 offset0:112 offset1:113
	ds_read2_b32 v[198:199], v167 offset0:18 offset1:19
	ds_read2_b32 v[200:201], v167 offset0:50 offset1:51
	ds_read2_b32 v[202:203], v167 offset0:82 offset1:83
	ds_read2_b32 v[148:149], v167 offset0:114 offset1:115
	ds_read2_b32 v[204:205], v167 offset0:24 offset1:25
	ds_read2_b32 v[206:207], v167 offset0:56 offset1:57
	ds_read2_b32 v[208:209], v167 offset0:88 offset1:89
	ds_read2_b32 v[150:151], v167 offset0:120 offset1:121
	ds_read2_b32 v[210:211], v167 offset0:26 offset1:27
	s_waitcnt lgkmcnt(0)
	v_pk_add_f32 v[80:81], v[80:81], v[168:169]
	ds_read2_b32 v[168:169], v167 offset0:58 offset1:59
	s_cmp_ge_i32 s92, s17
	s_cselect_b64 s[6:7], -1, 0
	s_waitcnt lgkmcnt(0)
	v_pk_add_f32 v[78:79], v[78:79], v[168:169]
	ds_read2_b32 v[168:169], v167 offset0:90 offset1:91
	s_xor_b64 s[8:9], s[8:9], -1
	s_or_b64 s[6:7], s[8:9], s[6:7]
	v_pk_add_f32 v[92:93], v[92:93], v[204:205]
	v_pk_add_f32 v[90:91], v[90:91], v[198:199]
	s_waitcnt lgkmcnt(0)
	v_pk_add_f32 v[110:111], v[110:111], v[168:169]
	ds_read2_b32 v[168:169], v167 offset0:122 offset1:123
	v_pk_add_f32 v[94:95], v[94:95], v[210:211]
	v_pk_add_f32 v[88:89], v[88:89], v[192:193]
	v_pk_add_f32 v[86:87], v[86:87], v[186:187]
	v_pk_add_f32 v[84:85], v[84:85], v[180:181]
	v_pk_add_f32 v[82:83], v[82:83], v[174:175]
	v_pk_add_f32 v[76:77], v[76:77], v[206:207]
	v_pk_add_f32 v[74:75], v[74:75], v[200:201]
	v_pk_add_f32 v[72:73], v[72:73], v[194:195]
	v_pk_add_f32 v[70:71], v[70:71], v[188:189]
	v_pk_add_f32 v[68:69], v[68:69], v[182:183]
	v_pk_add_f32 v[66:67], v[66:67], v[176:177]
	v_pk_add_f32 v[64:65], v[64:65], v[170:171]
	v_pk_add_f32 v[108:109], v[108:109], v[208:209]
	v_pk_add_f32 v[106:107], v[106:107], v[202:203]
	v_pk_add_f32 v[104:105], v[104:105], v[196:197]
	v_pk_add_f32 v[102:103], v[102:103], v[190:191]
	v_pk_add_f32 v[100:101], v[100:101], v[184:185]
	v_pk_add_f32 v[98:99], v[98:99], v[178:179]
	v_pk_add_f32 v[96:97], v[96:97], v[172:173]
	s_waitcnt lgkmcnt(0)
	v_pk_add_f32 v[62:63], v[62:63], v[168:169]
	v_pk_add_f32 v[60:61], v[60:61], v[150:151]
	v_pk_add_f32 v[58:59], v[58:59], v[148:149]
	v_pk_add_f32 v[56:57], v[56:57], v[146:147]
	v_pk_add_f32 v[54:55], v[54:55], v[144:145]
	v_pk_add_f32 v[52:53], v[52:53], v[142:143]
	v_pk_add_f32 v[50:51], v[50:51], v[140:141]
	v_pk_add_f32 v[48:49], v[48:49], v[138:139]
	s_and_b64 vcc, exec, s[6:7]
	s_cbranch_vccnz .LBB0_748
	v_add_u32_e32 v138, s16, v160
	v_sub_u32_e32 v138, v132, v138
	v_cmp_gt_i32_e64 s[44:45], 26, v138
	v_cmp_gt_i32_e64 s[60:61], 27, v138
	s_and_b64 s[44:45], s[60:61], s[44:45]
	v_cndmask_b32_e64 v94, v94, v252, s[44:45]
	v_cndmask_b32_e64 v95, v95, v252, s[60:61]
	v_cmp_gt_i32_e64 s[60:61], 25, v138
	s_and_b64 s[44:45], s[44:45], s[60:61]
	v_cmp_gt_i32_e64 s[60:61], 24, v138
	v_cndmask_b32_e64 v93, v93, v252, s[44:45]
	s_and_b64 s[44:45], s[44:45], s[60:61]
	v_cmp_gt_i32_e64 s[60:61], 19, v138
	v_cndmask_b32_e64 v92, v92, v252, s[44:45]
	s_and_b64 s[44:45], s[44:45], s[60:61]
	v_cmp_gt_i32_e64 s[60:61], 18, v138
	v_cndmask_b32_e64 v91, v91, v252, s[44:45]
	s_and_b64 s[44:45], s[44:45], s[60:61]
	v_cmp_gt_i32_e64 s[60:61], 17, v138
	v_cndmask_b32_e64 v90, v90, v252, s[44:45]
	s_and_b64 s[44:45], s[44:45], s[60:61]
	v_cmp_gt_i32_e64 s[60:61], 16, v138
	v_cndmask_b32_e64 v89, v89, v252, s[44:45]
	s_and_b64 s[44:45], s[44:45], s[60:61]
	v_cmp_gt_i32_e64 s[60:61], 11, v138
	v_cmp_gt_i32_e64 s[28:29], 10, v138
	s_and_b64 s[60:61], s[44:45], s[60:61]
	v_cmp_gt_i32_e64 s[58:59], 9, v138
	v_cndmask_b32_e64 v87, v87, v252, s[60:61]
	s_and_b64 s[60:61], s[60:61], s[28:29]
	v_cmp_gt_i32_e64 s[50:51], 8, v138
	v_cndmask_b32_e64 v86, v86, v252, s[60:61]
	s_and_b64 s[60:61], s[60:61], s[58:59]
	v_cmp_gt_i32_e64 s[36:37], 3, v138
	v_cndmask_b32_e64 v85, v85, v252, s[60:61]
	s_and_b64 s[60:61], s[60:61], s[50:51]
	v_cmp_gt_i32_e64 s[56:57], 2, v138
	v_cndmask_b32_e64 v84, v84, v252, s[60:61]
	s_and_b64 s[60:61], s[60:61], s[36:37]
	v_cmp_gt_i32_e64 s[52:53], 1, v138
	v_cndmask_b32_e64 v83, v83, v252, s[60:61]
	s_and_b64 s[60:61], s[60:61], s[56:57]
	v_cmp_gt_i32_e64 s[54:55], 0, v138
	v_cndmask_b32_e64 v82, v82, v252, s[60:61]
	s_and_b64 s[60:61], s[60:61], s[52:53]
	s_and_b64 s[54:55], s[60:61], s[54:55]
	v_cndmask_b32_e64 v81, v81, v252, s[60:61]
	v_cmp_gt_i32_e64 s[60:61], 58, v138
	v_cndmask_b32_e64 v80, v80, v252, s[54:55]
	v_cmp_gt_i32_e64 s[54:55], 59, v138
	v_cmp_gt_i32_e64 s[56:57], 48, v138
	v_cmp_gt_i32_e64 s[58:59], 43, v138
; __device__ __forceinline__ void moba_unit(const MobaArgs& A, int b, int h, int qb, LAS unsigned char* lds, int wave, bool tables) {
;     ...
;                 if (own && kt0 + 127 > qmin) {
;                     const int lim = qpos - kt0 - 4 * hi;
; #pragma unroll
;                     for (int r = 0; r < 16; ++r) { const int c = (r & 3) + 8 * (r >> 2); if (c > lim) a0[r] = NEG; if (c + 32 > lim) a1[r] = NEG; if (c + 64 > lim) b0[r] = NEG; if (c + 96 > lim) b1[r] = NEG; }
;                 }
	v_cndmask_b32_e64 v79, v79, v252, s[54:55]
	s_and_b64 s[54:55], s[54:55], s[60:61]
	v_cmp_gt_i32_e64 s[60:61], 57, v138
	v_cndmask_b32_e64 v78, v78, v252, s[54:55]
	s_and_b64 s[54:55], s[54:55], s[60:61]
	v_cmp_gt_i32_e64 s[60:61], 56, v138
	v_cndmask_b32_e64 v77, v77, v252, s[54:55]
	s_and_b64 s[54:55], s[54:55], s[60:61]
	v_cmp_gt_i32_e64 s[60:61], 51, v138
	v_cndmask_b32_e64 v76, v76, v252, s[54:55]
	s_and_b64 s[54:55], s[54:55], s[60:61]
	v_cmp_gt_i32_e64 s[60:61], 50, v138
	v_cndmask_b32_e64 v75, v75, v252, s[54:55]
	s_and_b64 s[54:55], s[54:55], s[60:61]
	v_cmp_gt_i32_e64 s[60:61], 49, v138
	s_and_b64 s[60:61], s[54:55], s[60:61]
	s_and_b64 s[56:57], s[60:61], s[56:57]
	v_cmp_gt_i32_e64 s[48:49], 42, v138
	s_and_b64 s[58:59], s[56:57], s[58:59]
	v_cmp_gt_i32_e64 s[46:47], 41, v138
	v_cndmask_b32_e64 v71, v71, v252, s[58:59]
	s_and_b64 s[58:59], s[58:59], s[48:49]
	v_cmp_gt_i32_e64 s[42:43], 40, v138
	v_cndmask_b32_e64 v70, v70, v252, s[58:59]
	s_and_b64 s[58:59], s[58:59], s[46:47]
	v_cmp_gt_i32_e64 s[40:41], 35, v138
	v_cndmask_b32_e64 v69, v69, v252, s[58:59]
	s_and_b64 s[58:59], s[58:59], s[42:43]
	v_cmp_gt_i32_e64 s[38:39], 34, v138
	v_cndmask_b32_e64 v68, v68, v252, s[58:59]
	s_and_b64 s[58:59], s[58:59], s[40:41]
	v_cmp_gt_i32_e64 s[34:35], 33, v138
	s_and_b64 s[38:39], s[58:59], s[38:39]
	v_cmp_gt_i32_e64 s[30:31], 32, v138
	v_cndmask_b32_e64 v66, v66, v252, s[38:39]
	s_and_b64 s[38:39], s[38:39], s[34:35]
	s_and_b64 s[30:31], s[38:39], s[30:31]
	v_cndmask_b32_e64 v65, v65, v252, s[38:39]
	s_movk_i32 s38, 0x5a
	v_cndmask_b32_e64 v64, v64, v252, s[30:31]
	s_movk_i32 s30, 0x5b
	v_cmp_gt_i32_e64 s[38:39], s38, v138
	v_cmp_gt_i32_e64 s[30:31], s30, v138
	v_cndmask_b32_e64 v67, v67, v252, s[58:59]
	s_movk_i32 s58, 0x58
	v_cndmask_b32_e64 v111, v111, v252, s[30:31]
	s_and_b64 s[30:31], s[30:31], s[38:39]
	s_movk_i32 s38, 0x59
	v_cmp_gt_i32_e64 s[38:39], s38, v138
	s_movk_i32 s42, 0x53
	v_cmp_gt_i32_e64 s[58:59], s58, v138
	v_cndmask_b32_e64 v110, v110, v252, s[30:31]
	s_and_b64 s[30:31], s[30:31], s[38:39]
	s_movk_i32 s48, 0x52
	v_cmp_gt_i32_e64 s[42:43], s42, v138
	v_cndmask_b32_e64 v109, v109, v252, s[30:31]
	s_and_b64 s[30:31], s[30:31], s[58:59]
	v_cndmask_b32_e64 v73, v73, v252, s[60:61]
	s_movk_i32 s60, 0x51
	v_cmp_gt_i32_e64 s[48:49], s48, v138
	v_cndmask_b32_e64 v108, v108, v252, s[30:31]
	s_and_b64 s[30:31], s[30:31], s[42:43]
	s_movk_i32 s52, 0x50
	v_cmp_gt_i32_e64 s[60:61], s60, v138
	v_cndmask_b32_e64 v107, v107, v252, s[30:31]
	s_and_b64 s[30:31], s[30:31], s[48:49]
	s_movk_i32 s50, 0x4b
	v_cmp_gt_i32_e64 s[52:53], s52, v138
	v_cndmask_b32_e64 v106, v106, v252, s[30:31]
	s_and_b64 s[30:31], s[30:31], s[60:61]
	v_cndmask_b32_e64 v88, v88, v252, s[44:45]
	s_movk_i32 s44, 0x4a
	v_cmp_gt_i32_e64 s[50:51], s50, v138
	v_cndmask_b32_e64 v105, v105, v252, s[30:31]
	s_and_b64 s[30:31], s[30:31], s[52:53]
	s_movk_i32 s14, 0x49
	v_cmp_gt_i32_e64 s[44:45], s44, v138
	v_cndmask_b32_e64 v104, v104, v252, s[30:31]
	s_and_b64 s[30:31], s[30:31], s[50:51]
	s_movk_i32 s12, 0x48
	v_cmp_gt_i32_e64 s[26:27], s14, v138
	v_cndmask_b32_e64 v103, v103, v252, s[30:31]
	s_and_b64 s[30:31], s[30:31], s[44:45]
	s_movk_i32 s10, 0x43
	v_cmp_gt_i32_e64 s[24:25], s12, v138
	s_and_b64 s[26:27], s[30:31], s[26:27]
	s_movk_i32 s6, 0x60
	s_movk_i32 s8, 0x42
	v_cmp_gt_i32_e64 s[22:23], s10, v138
	s_and_b64 s[24:25], s[26:27], s[24:25]
	v_cmp_gt_i32_e32 vcc, s6, v138
	s_movk_i32 s6, 0x41
	v_cmp_gt_i32_e64 s[20:21], s8, v138
	s_and_b64 s[22:23], s[24:25], s[22:23]
	v_cmp_gt_i32_e64 s[18:19], s6, v138
	s_and_b64 s[20:21], s[22:23], s[20:21]
	v_cmp_gt_i32_e64 s[16:17], 64, v138
	s_and_b64 s[18:19], s[20:21], s[18:19]
	s_and_b64 s[16:17], s[18:19], s[16:17]
	s_movk_i32 s58, 0x7a
	v_cndmask_b32_e64 v96, v96, v252, s[16:17]
	s_movk_i32 s16, 0x7b
	s_movk_i32 s38, 0x79
	v_cmp_gt_i32_e64 s[58:59], s58, v138
	v_cmp_gt_i32_e64 s[16:17], s16, v138
	s_movk_i32 s34, 0x78
	v_cmp_gt_i32_e64 s[38:39], s38, v138
	v_cndmask_b32_e64 v63, v63, v252, s[16:17]
	s_and_b64 s[16:17], s[16:17], s[58:59]
	s_movk_i32 s40, 0x73
	v_cmp_gt_i32_e64 s[34:35], s34, v138
	v_cndmask_b32_e64 v62, v62, v252, s[16:17]
	s_and_b64 s[16:17], s[16:17], s[38:39]
	s_movk_i32 s46, 0x72
	v_cmp_gt_i32_e64 s[40:41], s40, v138
	v_cndmask_b32_e64 v61, v61, v252, s[16:17]
	s_and_b64 s[16:17], s[16:17], s[34:35]
	v_cndmask_b32_e64 v72, v72, v252, s[56:57]
	s_movk_i32 s56, 0x71
	v_cmp_gt_i32_e64 s[46:47], s46, v138
	v_cndmask_b32_e64 v60, v60, v252, s[16:17]
	s_and_b64 s[16:17], s[16:17], s[40:41]
	v_cndmask_b32_e64 v74, v74, v252, s[54:55]
	s_movk_i32 s54, 0x70
	v_cmp_gt_i32_e64 s[56:57], s56, v138
	v_cndmask_b32_e64 v59, v59, v252, s[16:17]
	s_and_b64 s[16:17], s[16:17], s[46:47]
	s_movk_i32 s36, 0x6b
	v_cmp_gt_i32_e64 s[54:55], s54, v138
	v_cndmask_b32_e64 v58, v58, v252, s[16:17]
	s_and_b64 s[16:17], s[16:17], s[56:57]
	s_movk_i32 s28, 0x6a
	v_cmp_gt_i32_e64 s[36:37], s36, v138
	v_cndmask_b32_e64 v57, v57, v252, s[16:17]
	s_and_b64 s[16:17], s[16:17], s[54:55]
	s_movk_i32 s14, 0x69
	v_cmp_gt_i32_e64 s[28:29], s28, v138
	v_cndmask_b32_e64 v56, v56, v252, s[16:17]
	s_and_b64 s[16:17], s[16:17], s[36:37]
	s_movk_i32 s12, 0x68
	v_cmp_gt_i32_e64 s[14:15], s14, v138
	v_cndmask_b32_e64 v55, v55, v252, s[16:17]
	s_and_b64 s[16:17], s[16:17], s[28:29]
	s_movk_i32 s10, 0x63
	v_cmp_gt_i32_e64 s[12:13], s12, v138
	s_and_b64 s[14:15], s[16:17], s[14:15]
	s_movk_i32 s8, 0x62
	v_cmp_gt_i32_e64 s[10:11], s10, v138
	s_and_b64 s[12:13], s[14:15], s[12:13]
	s_movk_i32 s6, 0x61
	v_cmp_gt_i32_e64 s[8:9], s8, v138
	s_and_b64 s[10:11], s[12:13], s[10:11]
	v_cmp_gt_i32_e64 s[6:7], s6, v138
	s_and_b64 s[8:9], s[10:11], s[8:9]
	s_and_b64 s[6:7], s[8:9], s[6:7]
	s_and_b64 vcc, s[6:7], vcc
	s_mov_b32 s61, 0xe000
	s_mov_b32 s60, 0xc000
	v_cndmask_b32_e64 v102, v102, v252, s[30:31]
	v_cndmask_b32_e64 v101, v101, v252, s[26:27]
	v_cndmask_b32_e64 v100, v100, v252, s[24:25]
	v_cndmask_b32_e64 v99, v99, v252, s[22:23]
	v_cndmask_b32_e64 v98, v98, v252, s[20:21]
	v_cndmask_b32_e64 v97, v97, v252, s[18:19]
	v_cndmask_b32_e64 v54, v54, v252, s[16:17]
	v_cndmask_b32_e64 v53, v53, v252, s[14:15]
	v_cndmask_b32_e64 v52, v52, v252, s[12:13]
	v_cndmask_b32_e64 v51, v51, v252, s[10:11]
	v_cndmask_b32_e64 v50, v50, v252, s[8:9]
	v_cndmask_b32_e64 v49, v49, v252, s[6:7]
	v_cndmask_b32_e32 v48, v48, v252, vcc

; template <bool I8, class AccT> __device__ __forceinline__ void mma1(AccT& c, const bf16x8& a, const bf16x8& b) {
;     if constexpr (I8) c = __builtin_amdgcn_mfma_i32_16x16x64_i8(__builtin_bit_cast(AccT, a), __builtin_bit_cast(AccT, b), c, 0, 0, 0);
;     else c = __builtin_amdgcn_mfma_f32_16x16x32_bf16(a, b, c, 0, 0, 0);
; }
.Lzwo_s0:
	v_mfma_f32_16x16x32_bf16 v[126:129], v[130:133], v[168:171], 0
	v_mfma_f32_16x16x32_bf16 v[122:125], v[138:141], v[168:171], 0
	v_mfma_f32_16x16x32_bf16 v[108:111], v[130:133], v[176:179], 0
	v_mfma_f32_16x16x32_bf16 v[104:107], v[138:141], v[176:179], 0
	v_mfma_f32_16x16x32_bf16 v[92:95], v[130:133], v[184:187], 0
	v_mfma_f32_16x16x32_bf16 v[88:91], v[138:141], v[184:187], 0
	v_mfma_f32_16x16x32_bf16 v[76:79], v[130:133], v[192:195], 0
	v_mfma_f32_16x16x32_bf16 v[72:75], v[138:141], v[192:195], 0
	v_mfma_f32_16x16x32_bf16 v[126:129], v[134:137], v[172:175], v[126:129]
	v_mfma_f32_16x16x32_bf16 v[122:125], v[142:145], v[172:175], v[122:125]
	v_mfma_f32_16x16x32_bf16 v[108:111], v[134:137], v[180:183], v[108:111]
	v_mfma_f32_16x16x32_bf16 v[104:107], v[142:145], v[180:183], v[104:107]
	v_mfma_f32_16x16x32_bf16 v[92:95], v[134:137], v[188:191], v[92:95]
	v_mfma_f32_16x16x32_bf16 v[88:91], v[142:145], v[188:191], v[88:91]
	v_mfma_f32_16x16x32_bf16 v[76:79], v[134:137], v[196:199], v[76:79]
	v_mfma_f32_16x16x32_bf16 v[72:75], v[142:145], v[196:199], v[72:75]
	s_setprio 0
	s_setprio 1
	v_mfma_f32_16x16x32_bf16 v[118:121], v[146:149], v[168:171], 0
	v_mfma_f32_16x16x32_bf16 v[114:117], v[156:159], v[168:171], 0
	v_mfma_f32_16x16x32_bf16 v[100:103], v[146:149], v[176:179], 0
	v_mfma_f32_16x16x32_bf16 v[96:99], v[156:159], v[176:179], 0
	v_mfma_f32_16x16x32_bf16 v[84:87], v[146:149], v[184:187], 0
	v_mfma_f32_16x16x32_bf16 v[80:83], v[156:159], v[184:187], 0
	v_mfma_f32_16x16x32_bf16 v[68:71], v[146:149], v[192:195], 0
	v_mfma_f32_16x16x32_bf16 v[64:67], v[156:159], v[192:195], 0
	v_mfma_f32_16x16x32_bf16 v[118:121], v[150:153], v[172:175], v[118:121]
	v_mfma_f32_16x16x32_bf16 v[114:117], v[160:163], v[172:175], v[114:117]
	v_mfma_f32_16x16x32_bf16 v[100:103], v[150:153], v[180:183], v[100:103]
	v_mfma_f32_16x16x32_bf16 v[96:99], v[160:163], v[180:183], v[96:99]
	v_mfma_f32_16x16x32_bf16 v[84:87], v[150:153], v[188:191], v[84:87]
	v_mfma_f32_16x16x32_bf16 v[80:83], v[160:163], v[188:191], v[80:83]
	v_mfma_f32_16x16x32_bf16 v[68:71], v[150:153], v[196:199], v[68:71]
	v_mfma_f32_16x16x32_bf16 v[64:67], v[160:163], v[196:199], v[64:67]
	s_setprio 0
	s_branch .Lzwo_r0
.Lzwo_s1:
	v_mfma_f32_16x16x32_bf16 v[60:63], v[130:133], v[168:171], 0
	v_mfma_f32_16x16x32_bf16 v[56:59], v[138:141], v[168:171], 0
	v_mfma_f32_16x16x32_bf16 v[44:47], v[130:133], v[176:179], 0
	v_mfma_f32_16x16x32_bf16 v[40:43], v[138:141], v[176:179], 0
	v_mfma_f32_16x16x32_bf16 v[28:31], v[130:133], v[184:187], 0
	v_mfma_f32_16x16x32_bf16 v[24:27], v[138:141], v[184:187], 0
	v_mfma_f32_16x16x32_bf16 v[12:15], v[130:133], v[192:195], 0
	v_mfma_f32_16x16x32_bf16 v[8:11], v[138:141], v[192:195], 0
	v_mfma_f32_16x16x32_bf16 v[60:63], v[134:137], v[172:175], v[60:63]
	v_mfma_f32_16x16x32_bf16 v[56:59], v[142:145], v[172:175], v[56:59]
	v_mfma_f32_16x16x32_bf16 v[44:47], v[134:137], v[180:183], v[44:47]
	v_mfma_f32_16x16x32_bf16 v[40:43], v[142:145], v[180:183], v[40:43]
	v_mfma_f32_16x16x32_bf16 v[28:31], v[134:137], v[188:191], v[28:31]
	v_mfma_f32_16x16x32_bf16 v[24:27], v[142:145], v[188:191], v[24:27]
	v_mfma_f32_16x16x32_bf16 v[12:15], v[134:137], v[196:199], v[12:15]
	v_mfma_f32_16x16x32_bf16 v[8:11], v[142:145], v[196:199], v[8:11]
	s_setprio 0
	s_setprio 1
	v_mfma_f32_16x16x32_bf16 v[52:55], v[146:149], v[168:171], 0
	v_mfma_f32_16x16x32_bf16 v[48:51], v[156:159], v[168:171], 0
	v_mfma_f32_16x16x32_bf16 v[36:39], v[146:149], v[176:179], 0
	v_mfma_f32_16x16x32_bf16 v[32:35], v[156:159], v[176:179], 0
	v_mfma_f32_16x16x32_bf16 v[20:23], v[146:149], v[184:187], 0
	v_mfma_f32_16x16x32_bf16 v[16:19], v[156:159], v[184:187], 0
	v_mfma_f32_16x16x32_bf16 v[4:7], v[146:149], v[192:195], 0
	v_mfma_f32_16x16x32_bf16 v[0:3], v[156:159], v[192:195], 0
	v_mfma_f32_16x16x32_bf16 v[52:55], v[150:153], v[172:175], v[52:55]
	v_mfma_f32_16x16x32_bf16 v[48:51], v[160:163], v[172:175], v[48:51]
	v_mfma_f32_16x16x32_bf16 v[36:39], v[150:153], v[180:183], v[36:39]
	v_mfma_f32_16x16x32_bf16 v[32:35], v[160:163], v[180:183], v[32:35]
	v_mfma_f32_16x16x32_bf16 v[20:23], v[150:153], v[188:191], v[20:23]
	v_mfma_f32_16x16x32_bf16 v[16:19], v[160:163], v[188:191], v[16:19]
	v_mfma_f32_16x16x32_bf16 v[4:7], v[150:153], v[196:199], v[4:7]
	v_mfma_f32_16x16x32_bf16 v[0:3], v[160:163], v[196:199], v[0:3]
	s_setprio 0
	s_branch .Lzwo_r1

; #define PG8_STAGE(bufoff, gbase, voff) do { _Pragma("unroll") for (int _i = 0; _i < 2; ++_i) { const char* gb_ = (const char*)(gbase) + _i * rstep; asm volatile("" : "+s"(gb_));   \
;         __builtin_amdgcn_global_load_lds((const unsigned*)(gb_ + (voff)), (LAS unsigned*)(lds + (bufoff) + ldsw + _i * 8192), 16, 0, 0); } } while (0)
; #define PG8_LDA(dst, b, h) do { _Pragma("unroll") for (int m = 0; m < 4; ++m) _Pragma("unroll") for (int k = 0; k < 2; ++k) dst[m][k] = *(const LAS bf16x8*)(lds + PG8_SA(b, h) + aoff + m * 2048 + k * 1024); } while (0)
; #define PG8_WAIT_V(n) asm volatile("s_waitcnt vmcnt(" #n ")" ::: "memory")
; #define PG8_WAIT_L(n) asm volatile("s_waitcnt lgkmcnt(" #n ")" ::: "memory")
; #define PG8_BAR __builtin_amdgcn_s_barrier()
; template <class Epi, class Sched, bool ALIGN_EPI = true, bool SP2 = true, bool I8 = false, bool F8 = false>
; __device__ __forceinline__ void gemm_phase(LAS unsigned char* lds, const int K, const Sched& S, const Epi& E, const int wave) {
;     ...
;         const bool has_next = S.next(ui + 1, nxt);
;         const char* nA = has_next ? nxt.a : cA; const char* nB = has_next ? nxt.b : cB;
;         for (int t = 0; t < nt; t += 2) {
;             const bool last = (t == nt - 2);
;             const char* a1 = cA + (size_t)(t + 1) * kstep;
;             const char* a2 = last ? nA : cA + (size_t)(t + 2) * kstep; const char* b2 = last ? nB : cB + (size_t)(t + 2) * kstep;
;             const char* a3 = a2 + kstep; const char* b3 = b2 + kstep;
;             if constexpr (SP2) {
;             PG8_LDB(B0, 0, 0); PG8_LDB(B1, 0, 1); PG8_SCHED; PG8_LDA(At, 0, 0); PG8_STAGE(PG8_SA(1, 1), a1 + hstep, voffA);
;             PG8_WAIT_V(8); PG8_WAIT_L(0); PG8_BAR; PG8_MMA(0, 0, At, B0); PG8_MMA(0, 1, At, B1); PG8_BAR; PG8_SCHED;
;             PG8_LDA(At, 0, 1); PG8_STAGE(PG8_SB(0, 0), b2, voffB); PG8_STAGE(PG8_SB(0, 1), b2 + hstep, voffB); PG8_STAGE(PG8_SA(0, 0), a2, voffA);
;             PG8_WAIT_V(8); PG8_WAIT_L(0); PG8_BAR; PG8_MMA(1, 0, At, B0); PG8_MMA(1, 1, At, B1); PG8_BAR; PG8_SCHED;
;     ...
;         if (!(Epi::KEEPS && cur.sub < 2)) {
; #pragma unroll
;         for (int a = 0; a < 2; ++a)
; #pragma unroll
;             for (int b = 0; b < 2; ++b)
; #pragma unroll
;                 for (int m = 0; m < 4; ++m)
; #pragma unroll
;                     for (int n = 0; n < 2; ++n) acc[a][b][m][n] = (acc_t){0, 0, 0, 0};
;         }
.LBB0_1085:
	s_add_u32 s11, s22, 0x100
	s_addc_u32 s13, s23, 0
	s_add_u32 s20, s20, 0x60080
	s_addc_u32 s21, s21, 0
	s_mov_b32 s19, -2
.LBB0_1086:
	s_add_u32 s22, s20, 0xfffa0080
	s_addc_u32 s23, s21, -1
	s_cmp_eq_u32 s19, 12
	s_cselect_b32 s22, s14, s22
	s_cselect_b32 s23, s15, s23
	s_cselect_b32 s26, s16, s11
	s_cselect_b32 s27, s17, s13
	s_add_u32 s24, s22, 0x80
	s_addc_u32 s25, s23, 0
	s_add_i32 s48, 0, 0x10000
	s_add_i32 s49, 0, 0x14000
	v_add_u32_e32 v142, s48, v165
	v_add_u32_e32 v160, s49, v165
	ds_read_b128 v[130:133], v142
	ds_read_b128 v[134:137], v142 offset:1024
	ds_read_b128 v[138:141], v142 offset:2048
	ds_read_b128 v[142:145], v142 offset:3072
	ds_read_b128 v[146:149], v160
	ds_read_b128 v[150:153], v160 offset:1024
	ds_read_b128 v[156:159], v160 offset:2048
	ds_read_b128 v[160:163], v160 offset:3072
	s_add_u32 s46, s20, 0xfffe0000
	s_addc_u32 s47, s21, -1
	ds_read_b128 v[168:171], v166
	ds_read_b128 v[172:175], v166 offset:1024
	ds_read_b128 v[176:179], v166 offset:2048
	ds_read_b128 v[180:183], v166 offset:3072
	ds_read_b128 v[184:187], v166 offset:4096
	ds_read_b128 v[188:191], v166 offset:5120
	ds_read_b128 v[192:195], v166 offset:6144
	ds_read_b128 v[196:199], v166 offset:7168
	s_add_i32 m0, s35, 0xc000
	v_lshl_add_u64 v[200:201], s[46:47], 0, v[154:155]
	s_mov_b64 s[46:47], s[20:21]
	global_load_lds_dwordx4 v[200:201], off
	s_add_i32 m0, s35, 0xe000
	v_lshl_add_u64 v[200:201], s[46:47], 0, v[154:155]
	global_load_lds_dwordx4 v[200:201], off
	s_waitcnt vmcnt(8)
	s_waitcnt lgkmcnt(0)
	s_barrier
	s_setprio 1
	s_waitcnt lgkmcnt(0)
	s_cmp_eq_u32 s19, -2
	s_cbranch_scc1 .Lzwo_s0
	v_mfma_f32_16x16x32_bf16 v[126:129], v[130:133], v[168:171], v[126:129]
	v_mfma_f32_16x16x32_bf16 v[122:125], v[138:141], v[168:171], v[122:125]
	v_mfma_f32_16x16x32_bf16 v[108:111], v[130:133], v[176:179], v[108:111]
	v_mfma_f32_16x16x32_bf16 v[104:107], v[138:141], v[176:179], v[104:107]
	v_mfma_f32_16x16x32_bf16 v[92:95], v[130:133], v[184:187], v[92:95]
	v_mfma_f32_16x16x32_bf16 v[88:91], v[138:141], v[184:187], v[88:91]
	v_mfma_f32_16x16x32_bf16 v[76:79], v[130:133], v[192:195], v[76:79]
	v_mfma_f32_16x16x32_bf16 v[72:75], v[138:141], v[192:195], v[72:75]
	v_mfma_f32_16x16x32_bf16 v[126:129], v[134:137], v[172:175], v[126:129]
	v_mfma_f32_16x16x32_bf16 v[122:125], v[142:145], v[172:175], v[122:125]
	v_mfma_f32_16x16x32_bf16 v[108:111], v[134:137], v[180:183], v[108:111]
	v_mfma_f32_16x16x32_bf16 v[104:107], v[142:145], v[180:183], v[104:107]
	v_mfma_f32_16x16x32_bf16 v[92:95], v[134:137], v[188:191], v[92:95]
	v_mfma_f32_16x16x32_bf16 v[88:91], v[142:145], v[188:191], v[88:91]
	v_mfma_f32_16x16x32_bf16 v[76:79], v[134:137], v[196:199], v[76:79]
	v_mfma_f32_16x16x32_bf16 v[72:75], v[142:145], v[196:199], v[72:75]
	s_setprio 0
	s_setprio 1
	v_mfma_f32_16x16x32_bf16 v[118:121], v[146:149], v[168:171], v[118:121]
	v_mfma_f32_16x16x32_bf16 v[114:117], v[156:159], v[168:171], v[114:117]
	v_mfma_f32_16x16x32_bf16 v[100:103], v[146:149], v[176:179], v[100:103]
	v_mfma_f32_16x16x32_bf16 v[96:99], v[156:159], v[176:179], v[96:99]
	v_mfma_f32_16x16x32_bf16 v[84:87], v[146:149], v[184:187], v[84:87]
	v_mfma_f32_16x16x32_bf16 v[80:83], v[156:159], v[184:187], v[80:83]
	v_mfma_f32_16x16x32_bf16 v[68:71], v[146:149], v[192:195], v[68:71]
	v_mfma_f32_16x16x32_bf16 v[64:67], v[156:159], v[192:195], v[64:67]
	v_mfma_f32_16x16x32_bf16 v[118:121], v[150:153], v[172:175], v[118:121]
	v_mfma_f32_16x16x32_bf16 v[114:117], v[160:163], v[172:175], v[114:117]
	v_mfma_f32_16x16x32_bf16 v[100:103], v[150:153], v[180:183], v[100:103]
	v_mfma_f32_16x16x32_bf16 v[96:99], v[160:163], v[180:183], v[96:99]
	v_mfma_f32_16x16x32_bf16 v[84:87], v[150:153], v[188:191], v[84:87]
	v_mfma_f32_16x16x32_bf16 v[80:83], v[160:163], v[188:191], v[80:83]
	v_mfma_f32_16x16x32_bf16 v[68:71], v[150:153], v[196:199], v[68:71]
	v_mfma_f32_16x16x32_bf16 v[64:67], v[160:163], v[196:199], v[64:67]
	s_setprio 0
.Lzwo_r0:
	s_barrier
	s_mov_b64 s[46:47], s[26:27]
	ds_read_b128 v[168:171], v166 offset:16384
	ds_read_b128 v[172:175], v166 offset:17408
	ds_read_b128 v[176:179], v166 offset:18432
	ds_read_b128 v[180:183], v166 offset:19456
	ds_read_b128 v[184:187], v166 offset:20480
	ds_read_b128 v[188:191], v166 offset:21504
	ds_read_b128 v[192:195], v166 offset:22528
	ds_read_b128 v[196:199], v166 offset:23552
	s_add_i32 s48, s48, s34
	v_lshl_add_u64 v[200:201], s[46:47], 0, v[112:113]
	s_add_u32 s46, s26, 0x20000
	s_mov_b32 m0, s48
	s_addc_u32 s47, s27, 0
	global_load_lds_dwordx4 v[200:201], off
	s_add_i32 m0, s48, 0x2000
	v_lshl_add_u64 v[200:201], s[46:47], 0, v[112:113]
	s_add_u32 s46, s26, 0x40000
	s_addc_u32 s47, s27, 0
	global_load_lds_dwordx4 v[200:201], off
	s_add_i32 s48, s49, s34
	v_lshl_add_u64 v[200:201], s[46:47], 0, v[112:113]
	s_add_u32 s46, s26, 0x60000
	s_mov_b32 m0, s48
	s_addc_u32 s47, s27, 0
	global_load_lds_dwordx4 v[200:201], off
	s_add_i32 m0, s48, 0x2000
	v_lshl_add_u64 v[200:201], s[46:47], 0, v[112:113]
	s_mov_b64 s[46:47], s[22:23]
	global_load_lds_dwordx4 v[200:201], off
	s_mov_b32 m0, s35
	v_lshl_add_u64 v[200:201], s[46:47], 0, v[154:155]
	s_add_u32 s46, s22, 0x20000
	s_addc_u32 s47, s23, 0
	global_load_lds_dwordx4 v[200:201], off
	s_mov_b32 m0, s36
	v_lshl_add_u64 v[200:201], s[46:47], 0, v[154:155]
	global_load_lds_dwordx4 v[200:201], off
	s_waitcnt vmcnt(8)
	s_waitcnt lgkmcnt(0)
	s_barrier
	s_setprio 1
	s_waitcnt lgkmcnt(0)
	s_cmp_eq_u32 s19, -2
	s_cbranch_scc1 .Lzwo_s1
; #define PG8_STAGE(bufoff, gbase, voff) do { _Pragma("unroll") for (int _i = 0; _i < 2; ++_i) { const char* gb_ = (const char*)(gbase) + _i * rstep; asm volatile("" : "+s"(gb_));   \
;         __builtin_amdgcn_global_load_lds((const unsigned*)(gb_ + (voff)), (LAS unsigned*)(lds + (bufoff) + ldsw + _i * 8192), 16, 0, 0); } } while (0)
; #define PG8_LDA(dst, b, h) do { _Pragma("unroll") for (int m = 0; m < 4; ++m) _Pragma("unroll") for (int k = 0; k < 2; ++k) dst[m][k] = *(const LAS bf16x8*)(lds + PG8_SA(b, h) + aoff + m * 2048 + k * 1024); } while (0)
; #define PG8_LDB(dst, b, h) do { _Pragma("unroll") for (int n = 0; n < 2; ++n) _Pragma("unroll") for (int k = 0; k < 2; ++k) dst[n][k] = *(const LAS bf16x8*)(lds + PG8_SB(b, h) + boff + n * 2048 + k * 1024); } while (0)
; #define PG8_WAIT_V(n) asm volatile("s_waitcnt vmcnt(" #n ")" ::: "memory")
; #define PG8_WAIT_L(n) asm volatile("s_waitcnt lgkmcnt(" #n ")" ::: "memory")
; #define PG8_BAR __builtin_amdgcn_s_barrier()
; #define PG8_SCHED __builtin_amdgcn_sched_barrier(0)
; template <class Epi, class Sched, bool ALIGN_EPI = true, bool SP2 = true, bool I8 = false, bool F8 = false>
; __device__ __forceinline__ void gemm_phase(LAS unsigned char* lds, const int K, const Sched& S, const Epi& E, const int wave) {
;     ...
;             PG8_WAIT_V(8); PG8_WAIT_L(0); PG8_BAR; PG8_MMA(1, 0, At, B0); PG8_MMA(1, 1, At, B1); PG8_BAR; PG8_SCHED;
;             PG8_LDB(B0, 1, 0); PG8_LDB(B1, 1, 1); PG8_SCHED; PG8_LDA(At, 1, 0); PG8_STAGE(PG8_SA(0, 1), a2 + hstep, voffA);
;             PG8_WAIT_V(8); PG8_WAIT_L(0); PG8_BAR; PG8_MMA(0, 0, At, B0); PG8_MMA(0, 1, At, B1); PG8_BAR; PG8_SCHED;
	v_mfma_f32_16x16x32_bf16 v[60:63], v[130:133], v[168:171], v[60:63]
	v_mfma_f32_16x16x32_bf16 v[56:59], v[138:141], v[168:171], v[56:59]
	v_mfma_f32_16x16x32_bf16 v[44:47], v[130:133], v[176:179], v[44:47]
	v_mfma_f32_16x16x32_bf16 v[40:43], v[138:141], v[176:179], v[40:43]
	v_mfma_f32_16x16x32_bf16 v[28:31], v[130:133], v[184:187], v[28:31]
	v_mfma_f32_16x16x32_bf16 v[24:27], v[138:141], v[184:187], v[24:27]
	v_mfma_f32_16x16x32_bf16 v[12:15], v[130:133], v[192:195], v[12:15]
	v_mfma_f32_16x16x32_bf16 v[8:11], v[138:141], v[192:195], v[8:11]
	v_mfma_f32_16x16x32_bf16 v[60:63], v[134:137], v[172:175], v[60:63]
	v_mfma_f32_16x16x32_bf16 v[56:59], v[142:145], v[172:175], v[56:59]
	v_mfma_f32_16x16x32_bf16 v[44:47], v[134:137], v[180:183], v[44:47]
	v_mfma_f32_16x16x32_bf16 v[40:43], v[142:145], v[180:183], v[40:43]
	v_mfma_f32_16x16x32_bf16 v[28:31], v[134:137], v[188:191], v[28:31]
	v_mfma_f32_16x16x32_bf16 v[24:27], v[142:145], v[188:191], v[24:27]
	v_mfma_f32_16x16x32_bf16 v[12:15], v[134:137], v[196:199], v[12:15]
	v_mfma_f32_16x16x32_bf16 v[8:11], v[142:145], v[196:199], v[8:11]
	s_setprio 0
	s_setprio 1
	v_mfma_f32_16x16x32_bf16 v[52:55], v[146:149], v[168:171], v[52:55]
	v_mfma_f32_16x16x32_bf16 v[48:51], v[156:159], v[168:171], v[48:51]
	v_mfma_f32_16x16x32_bf16 v[36:39], v[146:149], v[176:179], v[36:39]
	v_mfma_f32_16x16x32_bf16 v[32:35], v[156:159], v[176:179], v[32:35]
	v_mfma_f32_16x16x32_bf16 v[20:23], v[146:149], v[184:187], v[20:23]
	v_mfma_f32_16x16x32_bf16 v[16:19], v[156:159], v[184:187], v[16:19]
	v_mfma_f32_16x16x32_bf16 v[4:7], v[146:149], v[192:195], v[4:7]
	v_mfma_f32_16x16x32_bf16 v[0:3], v[156:159], v[192:195], v[0:3]
	v_mfma_f32_16x16x32_bf16 v[52:55], v[150:153], v[172:175], v[52:55]
	v_mfma_f32_16x16x32_bf16 v[48:51], v[160:163], v[172:175], v[48:51]
	v_mfma_f32_16x16x32_bf16 v[36:39], v[150:153], v[180:183], v[36:39]
	v_mfma_f32_16x16x32_bf16 v[32:35], v[160:163], v[180:183], v[32:35]
	v_mfma_f32_16x16x32_bf16 v[20:23], v[150:153], v[188:191], v[20:23]
	v_mfma_f32_16x16x32_bf16 v[16:19], v[160:163], v[188:191], v[16:19]
	v_mfma_f32_16x16x32_bf16 v[4:7], v[150:153], v[196:199], v[4:7]
	v_mfma_f32_16x16x32_bf16 v[0:3], v[160:163], v[196:199], v[0:3]
	s_setprio 0
.Lzwo_r1:
	s_barrier
	s_add_i32 s48, 0, 0x18000
	s_add_i32 s49, 0, 0x1c000
	v_add_u32_e32 v142, s48, v165
	v_add_u32_e32 v160, s49, v165
	ds_read_b128 v[130:133], v142
	ds_read_b128 v[134:137], v142 offset:1024
	ds_read_b128 v[138:141], v142 offset:2048
	ds_read_b128 v[142:145], v142 offset:3072
	ds_read_b128 v[146:149], v160
	ds_read_b128 v[150:153], v160 offset:1024
	ds_read_b128 v[156:159], v160 offset:2048
	ds_read_b128 v[160:163], v160 offset:3072
	s_add_u32 s46, s22, 0x40000
	s_addc_u32 s47, s23, 0
	ds_read_b128 v[168:171], v166 offset:32768
	ds_read_b128 v[172:175], v166 offset:33792
	ds_read_b128 v[176:179], v166 offset:34816
	ds_read_b128 v[180:183], v166 offset:35840
	ds_read_b128 v[184:187], v166 offset:36864
	ds_read_b128 v[188:191], v166 offset:37888
	ds_read_b128 v[192:195], v166 offset:38912
	ds_read_b128 v[196:199], v166 offset:39936
	s_mov_b32 m0, s37
	v_lshl_add_u64 v[200:201], s[46:47], 0, v[154:155]
	s_add_u32 s46, s22, 0x60000
	s_addc_u32 s47, s23, 0
	global_load_lds_dwordx4 v[200:201], off
	s_mov_b32 m0, s38
	v_lshl_add_u64 v[200:201], s[46:47], 0, v[154:155]
	global_load_lds_dwordx4 v[200:201], off
	s_waitcnt vmcnt(8)
	s_waitcnt lgkmcnt(0)
	s_barrier
	s_setprio 1
	s_waitcnt lgkmcnt(0)
	v_mfma_f32_16x16x32_bf16 v[126:129], v[130:133], v[168:171], v[126:129]
	v_mfma_f32_16x16x32_bf16 v[122:125], v[138:141], v[168:171], v[122:125]
	v_mfma_f32_16x16x32_bf16 v[108:111], v[130:133], v[176:179], v[108:111]
	v_mfma_f32_16x16x32_bf16 v[104:107], v[138:141], v[176:179], v[104:107]
	v_mfma_f32_16x16x32_bf16 v[92:95], v[130:133], v[184:187], v[92:95]
	v_mfma_f32_16x16x32_bf16 v[88:91], v[138:141], v[184:187], v[88:91]
	v_mfma_f32_16x16x32_bf16 v[76:79], v[130:133], v[192:195], v[76:79]
	v_mfma_f32_16x16x32_bf16 v[72:75], v[138:141], v[192:195], v[72:75]
	v_mfma_f32_16x16x32_bf16 v[126:129], v[134:137], v[172:175], v[126:129]
	v_mfma_f32_16x16x32_bf16 v[122:125], v[142:145], v[172:175], v[122:125]
	v_mfma_f32_16x16x32_bf16 v[108:111], v[134:137], v[180:183], v[108:111]
	v_mfma_f32_16x16x32_bf16 v[104:107], v[142:145], v[180:183], v[104:107]
	v_mfma_f32_16x16x32_bf16 v[92:95], v[134:137], v[188:191], v[92:95]
	v_mfma_f32_16x16x32_bf16 v[88:91], v[142:145], v[188:191], v[88:91]
	v_mfma_f32_16x16x32_bf16 v[76:79], v[134:137], v[196:199], v[76:79]
	v_mfma_f32_16x16x32_bf16 v[72:75], v[142:145], v[196:199], v[72:75]
	s_setprio 0
	s_setprio 1
	v_mfma_f32_16x16x32_bf16 v[118:121], v[146:149], v[168:171], v[118:121]
	v_mfma_f32_16x16x32_bf16 v[114:117], v[156:159], v[168:171], v[114:117]
	v_mfma_f32_16x16x32_bf16 v[100:103], v[146:149], v[176:179], v[100:103]
	v_mfma_f32_16x16x32_bf16 v[96:99], v[156:159], v[176:179], v[96:99]
	v_mfma_f32_16x16x32_bf16 v[84:87], v[146:149], v[184:187], v[84:87]
	v_mfma_f32_16x16x32_bf16 v[80:83], v[156:159], v[184:187], v[80:83]
	v_mfma_f32_16x16x32_bf16 v[68:71], v[146:149], v[192:195], v[68:71]
	v_mfma_f32_16x16x32_bf16 v[64:67], v[156:159], v[192:195], v[64:67]
	v_mfma_f32_16x16x32_bf16 v[118:121], v[150:153], v[172:175], v[118:121]
	v_mfma_f32_16x16x32_bf16 v[114:117], v[160:163], v[172:175], v[114:117]
	v_mfma_f32_16x16x32_bf16 v[100:103], v[150:153], v[180:183], v[100:103]
	v_mfma_f32_16x16x32_bf16 v[96:99], v[160:163], v[180:183], v[96:99]
	v_mfma_f32_16x16x32_bf16 v[84:87], v[150:153], v[188:191], v[84:87]
	v_mfma_f32_16x16x32_bf16 v[80:83], v[160:163], v[188:191], v[80:83]
	v_mfma_f32_16x16x32_bf16 v[68:71], v[150:153], v[196:199], v[68:71]
	v_mfma_f32_16x16x32_bf16 v[64:67], v[160:163], v[196:199], v[64:67]
	s_setprio 0
	s_barrier
; #define PG8_STAGE(bufoff, gbase, voff) do { _Pragma("unroll") for (int _i = 0; _i < 2; ++_i) { const char* gb_ = (const char*)(gbase) + _i * rstep; asm volatile("" : "+s"(gb_));   \
;         __builtin_amdgcn_global_load_lds((const unsigned*)(gb_ + (voff)), (LAS unsigned*)(lds + (bufoff) + ldsw + _i * 8192), 16, 0, 0); } } while (0)
; #define PG8_LDA(dst, b, h) do { _Pragma("unroll") for (int m = 0; m < 4; ++m) _Pragma("unroll") for (int k = 0; k < 2; ++k) dst[m][k] = *(const LAS bf16x8*)(lds + PG8_SA(b, h) + aoff + m * 2048 + k * 1024); } while (0)
; #define PG8_WAIT_V(n) asm volatile("s_waitcnt vmcnt(" #n ")" ::: "memory")
; #define PG8_WAIT_L(n) asm volatile("s_waitcnt lgkmcnt(" #n ")" ::: "memory")
; template <class Epi, class Sched, bool ALIGN_EPI = true, bool SP2 = true, bool I8 = false, bool F8 = false>
; __device__ __forceinline__ void gemm_phase(LAS unsigned char* lds, const int K, const Sched& S, const Epi& E, const int wave) {
;     ...
;         for (int t = 0; t < nt; t += 2) {
;             const bool last = (t == nt - 2);
;             const char* a1 = cA + (size_t)(t + 1) * kstep;
;             const char* a2 = last ? nA : cA + (size_t)(t + 2) * kstep; const char* b2 = last ? nB : cB + (size_t)(t + 2) * kstep;
;             const char* a3 = a2 + kstep; const char* b3 = b2 + kstep;
;             if constexpr (SP2) {
;             PG8_LDB(B0, 0, 0); PG8_LDB(B1, 0, 1); PG8_SCHED; PG8_LDA(At, 0, 0); PG8_STAGE(PG8_SA(1, 1), a1 + hstep, voffA);
;             PG8_WAIT_V(8); PG8_WAIT_L(0); PG8_BAR; PG8_MMA(0, 0, At, B0); PG8_MMA(0, 1, At, B1); PG8_BAR; PG8_SCHED;
;             PG8_LDA(At, 0, 1); PG8_STAGE(PG8_SB(0, 0), b2, voffB); PG8_STAGE(PG8_SB(0, 1), b2 + hstep, voffB); PG8_STAGE(PG8_SA(0, 0), a2, voffA);
;             PG8_WAIT_V(8); PG8_WAIT_L(0); PG8_BAR; PG8_MMA(1, 0, At, B0); PG8_MMA(1, 1, At, B1); PG8_BAR; PG8_SCHED;
;             PG8_LDB(B0, 1, 0); PG8_LDB(B1, 1, 1); PG8_SCHED; PG8_LDA(At, 1, 0); PG8_STAGE(PG8_SA(0, 1), a2 + hstep, voffA);
;             PG8_WAIT_V(8); PG8_WAIT_L(0); PG8_BAR; PG8_MMA(0, 0, At, B0); PG8_MMA(0, 1, At, B1); PG8_BAR; PG8_SCHED;
;             PG8_LDA(At, 1, 1); PG8_STAGE(PG8_SB(1, 0), b3, voffB); PG8_STAGE(PG8_SB(1, 1), b3 + hstep, voffB); PG8_STAGE(PG8_SA(1, 0), a3, voffA);
;             PG8_WAIT_V(8); PG8_WAIT_L(0); PG8_BAR; PG8_MMA(1, 0, At, B0); PG8_MMA(1, 1, At, B1); PG8_BAR; PG8_SCHED;
	s_add_u32 s46, s26, 0x80
	s_addc_u32 s47, s27, 0
	ds_read_b128 v[168:171], v166 offset:49152
	ds_read_b128 v[172:175], v166 offset:50176
	ds_read_b128 v[176:179], v166 offset:51200
	ds_read_b128 v[180:183], v166 offset:52224
	ds_read_b128 v[184:187], v166 offset:53248
	ds_read_b128 v[188:191], v166 offset:54272
	ds_read_b128 v[192:195], v166 offset:55296
	ds_read_b128 v[196:199], v166 offset:56320
	s_add_i32 s48, s48, s34
	v_lshl_add_u64 v[200:201], s[46:47], 0, v[112:113]
	s_add_u32 s46, s26, 0x20080
	s_mov_b32 m0, s48
	s_addc_u32 s47, s27, 0
	global_load_lds_dwordx4 v[200:201], off
	s_add_i32 m0, s48, 0x2000
	v_lshl_add_u64 v[200:201], s[46:47], 0, v[112:113]
	s_add_u32 s46, s26, 0x40080
	s_addc_u32 s47, s27, 0
	global_load_lds_dwordx4 v[200:201], off
	s_nop 0
	v_lshl_add_u64 v[200:201], s[46:47], 0, v[112:113]
	s_add_i32 s46, s49, s34
	s_mov_b32 m0, s46
	s_add_u32 s26, s26, 0x60080
	global_load_lds_dwordx4 v[200:201], off
	s_addc_u32 s27, s27, 0
	s_add_i32 m0, s46, 0x2000
	s_add_u32 s22, s22, 0x20080
	v_lshl_add_u64 v[200:201], s[26:27], 0, v[112:113]
	global_load_lds_dwordx4 v[200:201], off
	s_mov_b32 m0, s41
	v_lshl_add_u64 v[200:201], s[24:25], 0, v[154:155]
	s_addc_u32 s23, s23, 0
	global_load_lds_dwordx4 v[200:201], off
	s_mov_b32 m0, s42
	v_lshl_add_u64 v[200:201], s[22:23], 0, v[154:155]
	global_load_lds_dwordx4 v[200:201], off
	s_waitcnt vmcnt(8)
	s_waitcnt lgkmcnt(0)
	s_barrier
	s_setprio 1
	s_waitcnt lgkmcnt(0)
	v_mfma_f32_16x16x32_bf16 v[60:63], v[130:133], v[168:171], v[60:63]
	v_mfma_f32_16x16x32_bf16 v[56:59], v[138:141], v[168:171], v[56:59]
	v_mfma_f32_16x16x32_bf16 v[44:47], v[130:133], v[176:179], v[44:47]
	v_mfma_f32_16x16x32_bf16 v[40:43], v[138:141], v[176:179], v[40:43]
	v_mfma_f32_16x16x32_bf16 v[28:31], v[130:133], v[184:187], v[28:31]
	v_mfma_f32_16x16x32_bf16 v[24:27], v[138:141], v[184:187], v[24:27]
	v_mfma_f32_16x16x32_bf16 v[12:15], v[130:133], v[192:195], v[12:15]
	v_mfma_f32_16x16x32_bf16 v[8:11], v[138:141], v[192:195], v[8:11]
	v_mfma_f32_16x16x32_bf16 v[60:63], v[134:137], v[172:175], v[60:63]
	v_mfma_f32_16x16x32_bf16 v[56:59], v[142:145], v[172:175], v[56:59]
	v_mfma_f32_16x16x32_bf16 v[44:47], v[134:137], v[180:183], v[44:47]
	v_mfma_f32_16x16x32_bf16 v[40:43], v[142:145], v[180:183], v[40:43]
	v_mfma_f32_16x16x32_bf16 v[28:31], v[134:137], v[188:191], v[28:31]
	v_mfma_f32_16x16x32_bf16 v[24:27], v[142:145], v[188:191], v[24:27]
	v_mfma_f32_16x16x32_bf16 v[12:15], v[134:137], v[196:199], v[12:15]
	v_mfma_f32_16x16x32_bf16 v[8:11], v[142:145], v[196:199], v[8:11]
	s_setprio 0
	s_setprio 1
	v_mfma_f32_16x16x32_bf16 v[52:55], v[146:149], v[168:171], v[52:55]
	v_mfma_f32_16x16x32_bf16 v[48:51], v[156:159], v[168:171], v[48:51]
	v_mfma_f32_16x16x32_bf16 v[36:39], v[146:149], v[176:179], v[36:39]
	v_mfma_f32_16x16x32_bf16 v[32:35], v[156:159], v[176:179], v[32:35]
	v_mfma_f32_16x16x32_bf16 v[20:23], v[146:149], v[184:187], v[20:23]
	v_mfma_f32_16x16x32_bf16 v[16:19], v[156:159], v[184:187], v[16:19]
	v_mfma_f32_16x16x32_bf16 v[4:7], v[146:149], v[192:195], v[4:7]
	v_mfma_f32_16x16x32_bf16 v[0:3], v[156:159], v[192:195], v[0:3]
	v_mfma_f32_16x16x32_bf16 v[52:55], v[150:153], v[172:175], v[52:55]
	v_mfma_f32_16x16x32_bf16 v[48:51], v[160:163], v[172:175], v[48:51]
	v_mfma_f32_16x16x32_bf16 v[36:39], v[150:153], v[180:183], v[36:39]
	v_mfma_f32_16x16x32_bf16 v[32:35], v[160:163], v[180:183], v[32:35]
	v_mfma_f32_16x16x32_bf16 v[20:23], v[150:153], v[188:191], v[20:23]
	v_mfma_f32_16x16x32_bf16 v[16:19], v[160:163], v[188:191], v[16:19]
	v_mfma_f32_16x16x32_bf16 v[4:7], v[150:153], v[196:199], v[4:7]
	v_mfma_f32_16x16x32_bf16 v[0:3], v[160:163], v[196:199], v[0:3]
	s_setprio 0
	s_barrier
	s_add_i32 s19, s19, 2
	s_add_u32 s11, s11, 0x100
	s_addc_u32 s13, s13, 0
	s_add_u32 s20, s20, 0x100
	s_addc_u32 s21, s21, 0
	s_cmp_gt_u32 s19, 13
	s_cbranch_scc0 .LBB0_1086
	s_and_b64 vcc, exec, s[2:3]
	s_cbranch_vccz .LBB0_1089
	s_barrier

; #define PG8_STAGE(bufoff, gbase, voff) do { _Pragma("unroll") for (int _i = 0; _i < 2; ++_i) { const char* gb_ = (const char*)(gbase) + _i * rstep; asm volatile("" : "+s"(gb_));   \
;         __builtin_amdgcn_global_load_lds((const unsigned*)(gb_ + (voff)), (LAS unsigned*)(lds + (bufoff) + ldsw + _i * 8192), 16, 0, 0); } } while (0)
; #define PG8_LDA(dst, b, h) do { _Pragma("unroll") for (int m = 0; m < 4; ++m) _Pragma("unroll") for (int k = 0; k < 2; ++k) dst[m][k] = *(const LAS bf16x8*)(lds + PG8_SA(b, h) + aoff + m * 2048 + k * 1024); } while (0)
; #define PG8_WAIT_V(n) asm volatile("s_waitcnt vmcnt(" #n ")" ::: "memory")
; #define PG8_WAIT_L(n) asm volatile("s_waitcnt lgkmcnt(" #n ")" ::: "memory")
; #define PG8_BAR __builtin_amdgcn_s_barrier()
; #define PG8_SCHED __builtin_amdgcn_sched_barrier(0)
; template <class Epi, class Sched, bool ALIGN_EPI = true, bool SP2 = true, bool I8 = false, bool F8 = false>
; __device__ __forceinline__ void gemm_phase(LAS unsigned char* lds, const int K, const Sched& S, const Epi& E, const int wave) {
;     ...
;             PG8_WAIT_V(8); PG8_WAIT_L(0); PG8_BAR; PG8_MMA(0, 0, At, B0); PG8_MMA(0, 1, At, B1); PG8_BAR; PG8_SCHED;
;             PG8_LDA(At, 0, 1); PG8_STAGE(PG8_SB(0, 0), b2, voffB); PG8_STAGE(PG8_SB(0, 1), b2 + hstep, voffB); PG8_STAGE(PG8_SA(0, 0), a2, voffA);
;             PG8_WAIT_V(8); PG8_WAIT_L(0); PG8_BAR; PG8_MMA(1, 0, At, B0); PG8_MMA(1, 1, At, B1); PG8_BAR; PG8_SCHED;
.Lzqx_s0:
	v_mfma_f32_16x16x32_bf16 v[126:129], v[136:139], v[174:177], 0
	v_mfma_f32_16x16x32_bf16 v[122:125], v[146:149], v[174:177], 0
	v_mfma_f32_16x16x32_bf16 v[118:121], v[136:139], v[182:185], 0
	v_mfma_f32_16x16x32_bf16 v[108:111], v[146:149], v[182:185], 0
	v_mfma_f32_16x16x32_bf16 v[100:103], v[136:139], v[190:193], 0
	v_mfma_f32_16x16x32_bf16 v[92:95], v[146:149], v[190:193], 0
	v_mfma_f32_16x16x32_bf16 v[84:87], v[136:139], v[198:201], 0
	v_mfma_f32_16x16x32_bf16 v[76:79], v[146:149], v[198:201], 0
	v_mfma_f32_16x16x32_bf16 v[126:129], v[142:145], v[178:181], v[126:129]
	v_mfma_f32_16x16x32_bf16 v[122:125], v[150:153], v[178:181], v[122:125]
	v_mfma_f32_16x16x32_bf16 v[118:121], v[142:145], v[186:189], v[118:121]
	v_mfma_f32_16x16x32_bf16 v[108:111], v[150:153], v[186:189], v[108:111]
	v_mfma_f32_16x16x32_bf16 v[100:103], v[142:145], v[194:197], v[100:103]
	v_mfma_f32_16x16x32_bf16 v[92:95], v[150:153], v[194:197], v[92:95]
	v_mfma_f32_16x16x32_bf16 v[84:87], v[142:145], v[202:205], v[84:87]
	v_mfma_f32_16x16x32_bf16 v[76:79], v[150:153], v[202:205], v[76:79]
	s_setprio 0
	s_setprio 1
	v_mfma_f32_16x16x32_bf16 v[114:117], v[154:157], v[174:177], 0
	v_mfma_f32_16x16x32_bf16 v[104:107], v[166:169], v[174:177], 0
	v_mfma_f32_16x16x32_bf16 v[96:99], v[154:157], v[182:185], 0
	v_mfma_f32_16x16x32_bf16 v[88:91], v[166:169], v[182:185], 0
	v_mfma_f32_16x16x32_bf16 v[80:83], v[154:157], v[190:193], 0
	v_mfma_f32_16x16x32_bf16 v[72:75], v[166:169], v[190:193], 0
	v_mfma_f32_16x16x32_bf16 v[68:71], v[154:157], v[198:201], 0
	v_mfma_f32_16x16x32_bf16 v[64:67], v[166:169], v[198:201], 0
	v_mfma_f32_16x16x32_bf16 v[114:117], v[158:161], v[178:181], v[114:117]
	v_mfma_f32_16x16x32_bf16 v[104:107], v[170:173], v[178:181], v[104:107]
	v_mfma_f32_16x16x32_bf16 v[96:99], v[158:161], v[186:189], v[96:99]
	v_mfma_f32_16x16x32_bf16 v[88:91], v[170:173], v[186:189], v[88:91]
	v_mfma_f32_16x16x32_bf16 v[80:83], v[158:161], v[194:197], v[80:83]
	v_mfma_f32_16x16x32_bf16 v[72:75], v[170:173], v[194:197], v[72:75]
	v_mfma_f32_16x16x32_bf16 v[68:71], v[158:161], v[202:205], v[68:71]
	v_mfma_f32_16x16x32_bf16 v[64:67], v[170:173], v[202:205], v[64:67]
	s_setprio 0
	s_branch .Lzqx_r0
.Lzqx_s1:
	v_mfma_f32_16x16x32_bf16 v[60:63], v[136:139], v[174:177], 0
	v_mfma_f32_16x16x32_bf16 v[56:59], v[146:149], v[174:177], 0
	v_mfma_f32_16x16x32_bf16 v[52:55], v[136:139], v[182:185], 0
	v_mfma_f32_16x16x32_bf16 v[44:47], v[146:149], v[182:185], 0
	v_mfma_f32_16x16x32_bf16 v[36:39], v[136:139], v[190:193], 0
	v_mfma_f32_16x16x32_bf16 v[28:31], v[146:149], v[190:193], 0
	v_mfma_f32_16x16x32_bf16 v[20:23], v[136:139], v[198:201], 0
	v_mfma_f32_16x16x32_bf16 v[12:15], v[146:149], v[198:201], 0
	v_mfma_f32_16x16x32_bf16 v[60:63], v[142:145], v[178:181], v[60:63]
	v_mfma_f32_16x16x32_bf16 v[56:59], v[150:153], v[178:181], v[56:59]
	v_mfma_f32_16x16x32_bf16 v[52:55], v[142:145], v[186:189], v[52:55]
	v_mfma_f32_16x16x32_bf16 v[44:47], v[150:153], v[186:189], v[44:47]
	v_mfma_f32_16x16x32_bf16 v[36:39], v[142:145], v[194:197], v[36:39]
	v_mfma_f32_16x16x32_bf16 v[28:31], v[150:153], v[194:197], v[28:31]
	v_mfma_f32_16x16x32_bf16 v[20:23], v[142:145], v[202:205], v[20:23]
	v_mfma_f32_16x16x32_bf16 v[12:15], v[150:153], v[202:205], v[12:15]
	s_setprio 0
	s_setprio 1
	v_mfma_f32_16x16x32_bf16 v[48:51], v[154:157], v[174:177], 0
	v_mfma_f32_16x16x32_bf16 v[40:43], v[166:169], v[174:177], 0
	v_mfma_f32_16x16x32_bf16 v[32:35], v[154:157], v[182:185], 0
	v_mfma_f32_16x16x32_bf16 v[24:27], v[166:169], v[182:185], 0
	v_mfma_f32_16x16x32_bf16 v[16:19], v[154:157], v[190:193], 0
	v_mfma_f32_16x16x32_bf16 v[8:11], v[166:169], v[190:193], 0
	v_mfma_f32_16x16x32_bf16 v[4:7], v[154:157], v[198:201], 0
	v_mfma_f32_16x16x32_bf16 v[0:3], v[166:169], v[198:201], 0
	v_mfma_f32_16x16x32_bf16 v[48:51], v[158:161], v[178:181], v[48:51]
	v_mfma_f32_16x16x32_bf16 v[40:43], v[170:173], v[178:181], v[40:43]
	v_mfma_f32_16x16x32_bf16 v[32:35], v[158:161], v[186:189], v[32:35]
	v_mfma_f32_16x16x32_bf16 v[24:27], v[170:173], v[186:189], v[24:27]
	v_mfma_f32_16x16x32_bf16 v[16:19], v[158:161], v[194:197], v[16:19]
	v_mfma_f32_16x16x32_bf16 v[8:11], v[170:173], v[194:197], v[8:11]
	v_mfma_f32_16x16x32_bf16 v[4:7], v[158:161], v[202:205], v[4:7]
	v_mfma_f32_16x16x32_bf16 v[0:3], v[170:173], v[202:205], v[0:3]
	s_setprio 0
	s_branch .Lzqx_r1

; #define PG8_STAGE(bufoff, gbase, voff) do { _Pragma("unroll") for (int _i = 0; _i < 2; ++_i) { const char* gb_ = (const char*)(gbase) + _i * rstep; asm volatile("" : "+s"(gb_));   \
;         __builtin_amdgcn_global_load_lds((const unsigned*)(gb_ + (voff)), (LAS unsigned*)(lds + (bufoff) + ldsw + _i * 8192), 16, 0, 0); } } while (0)
; #define PG8_LDA(dst, b, h) do { _Pragma("unroll") for (int m = 0; m < 4; ++m) _Pragma("unroll") for (int k = 0; k < 2; ++k) dst[m][k] = *(const LAS bf16x8*)(lds + PG8_SA(b, h) + aoff + m * 2048 + k * 1024); } while (0)
; #define PG8_LDB(dst, b, h) do { _Pragma("unroll") for (int n = 0; n < 2; ++n) _Pragma("unroll") for (int k = 0; k < 2; ++k) dst[n][k] = *(const LAS bf16x8*)(lds + PG8_SB(b, h) + boff + n * 2048 + k * 1024); } while (0)
; #define PG8_WAIT_V(n) asm volatile("s_waitcnt vmcnt(" #n ")" ::: "memory")
; #define PG8_WAIT_L(n) asm volatile("s_waitcnt lgkmcnt(" #n ")" ::: "memory")
; #define PG8_BAR __builtin_amdgcn_s_barrier()
; template <class Epi, class Sched, bool ALIGN_EPI = true, bool SP2 = true, bool I8 = false, bool F8 = false>
; __device__ __forceinline__ void gemm_phase(LAS unsigned char* lds, const int K, const Sched& S, const Epi& E, const int wave) {
;     ...
;         for (int t = 0; t < nt; t += 2) {
;             const bool last = (t == nt - 2);
;             const char* a1 = cA + (size_t)(t + 1) * kstep;
;             const char* a2 = last ? nA : cA + (size_t)(t + 2) * kstep; const char* b2 = last ? nB : cB + (size_t)(t + 2) * kstep;
;             const char* a3 = a2 + kstep; const char* b3 = b2 + kstep;
;             if constexpr (SP2) {
;             PG8_LDB(B0, 0, 0); PG8_LDB(B1, 0, 1); PG8_SCHED; PG8_LDA(At, 0, 0); PG8_STAGE(PG8_SA(1, 1), a1 + hstep, voffA);
;             PG8_WAIT_V(8); PG8_WAIT_L(0); PG8_BAR; PG8_MMA(0, 0, At, B0); PG8_MMA(0, 1, At, B1); PG8_BAR; PG8_SCHED;
;             PG8_LDA(At, 0, 1); PG8_STAGE(PG8_SB(0, 0), b2, voffB); PG8_STAGE(PG8_SB(0, 1), b2 + hstep, voffB); PG8_STAGE(PG8_SA(0, 0), a2, voffA);
;             PG8_WAIT_V(8); PG8_WAIT_L(0); PG8_BAR; PG8_MMA(1, 0, At, B0); PG8_MMA(1, 1, At, B1); PG8_BAR; PG8_SCHED;
;     ...
;         for (int a = 0; a < 2; ++a)
; #pragma unroll
;             for (int b = 0; b < 2; ++b)
; #pragma unroll
;                 for (int m = 0; m < 4; ++m)
; #pragma unroll
;                     for (int n = 0; n < 2; ++n) acc[a][b][m][n] = (acc_t){0, 0, 0, 0};
.LBB0_1169:
	s_add_u32 s11, s22, 0x100
	s_addc_u32 s13, s23, 0
	s_add_u32 s20, s20, 0x60080
	s_addc_u32 s21, s21, 0
	s_mov_b32 s44, -2
.LBB0_1170:
	s_add_u32 s22, s20, 0xfffa0080
	s_addc_u32 s23, s21, -1
	s_cmp_eq_u32 s44, 12
	s_cselect_b32 s22, s14, s22
	s_cselect_b32 s23, s15, s23
	s_cselect_b32 s26, s16, s11
	s_cselect_b32 s27, s17, s13
	s_add_u32 s24, s22, 0x80
	s_addc_u32 s25, s23, 0
	s_add_i32 s45, 0, 0x10000
	v_add_u32_e32 v132, s45, v135
	s_add_i32 s48, 0, 0x14000
	ds_read_b128 v[136:139], v132
	ds_read_b128 v[142:145], v132 offset:1024
	ds_read_b128 v[146:149], v132 offset:2048
	ds_read_b128 v[150:153], v132 offset:3072
	v_add_u32_e32 v132, s48, v135
	ds_read_b128 v[154:157], v132
	ds_read_b128 v[158:161], v132 offset:1024
	ds_read_b128 v[166:169], v132 offset:2048
	ds_read_b128 v[170:173], v132 offset:3072
	s_add_u32 s46, s20, 0xfffe0000
	s_addc_u32 s47, s21, -1
	ds_read_b128 v[174:177], v141
	ds_read_b128 v[178:181], v141 offset:1024
	ds_read_b128 v[182:185], v141 offset:2048
	ds_read_b128 v[186:189], v141 offset:3072
	ds_read_b128 v[190:193], v141 offset:4096
	ds_read_b128 v[194:197], v141 offset:5120
	ds_read_b128 v[198:201], v141 offset:6144
	ds_read_b128 v[202:205], v141 offset:7168
	s_add_i32 m0, s36, 0xc000
	v_lshl_add_u64 v[132:133], s[46:47], 0, v[130:131]
	s_mov_b64 s[46:47], s[20:21]
	global_load_lds_dwordx4 v[132:133], off
	s_add_i32 m0, s36, 0xe000
	v_lshl_add_u64 v[132:133], s[46:47], 0, v[130:131]
	global_load_lds_dwordx4 v[132:133], off
	s_waitcnt vmcnt(8)
	s_waitcnt lgkmcnt(0)
	s_barrier
	s_setprio 1
	s_waitcnt lgkmcnt(0)
	s_cmp_eq_u32 s44, -2
	s_cbranch_scc1 .Lzqx_s0
	v_mfma_f32_16x16x32_bf16 v[126:129], v[136:139], v[174:177], v[126:129]
	v_mfma_f32_16x16x32_bf16 v[122:125], v[146:149], v[174:177], v[122:125]
	v_mfma_f32_16x16x32_bf16 v[118:121], v[136:139], v[182:185], v[118:121]
	v_mfma_f32_16x16x32_bf16 v[108:111], v[146:149], v[182:185], v[108:111]
	v_mfma_f32_16x16x32_bf16 v[100:103], v[136:139], v[190:193], v[100:103]
	v_mfma_f32_16x16x32_bf16 v[92:95], v[146:149], v[190:193], v[92:95]
	v_mfma_f32_16x16x32_bf16 v[84:87], v[136:139], v[198:201], v[84:87]
	v_mfma_f32_16x16x32_bf16 v[76:79], v[146:149], v[198:201], v[76:79]
	v_mfma_f32_16x16x32_bf16 v[126:129], v[142:145], v[178:181], v[126:129]
	v_mfma_f32_16x16x32_bf16 v[122:125], v[150:153], v[178:181], v[122:125]
	v_mfma_f32_16x16x32_bf16 v[118:121], v[142:145], v[186:189], v[118:121]
	v_mfma_f32_16x16x32_bf16 v[108:111], v[150:153], v[186:189], v[108:111]
	v_mfma_f32_16x16x32_bf16 v[100:103], v[142:145], v[194:197], v[100:103]
	v_mfma_f32_16x16x32_bf16 v[92:95], v[150:153], v[194:197], v[92:95]
	v_mfma_f32_16x16x32_bf16 v[84:87], v[142:145], v[202:205], v[84:87]
	v_mfma_f32_16x16x32_bf16 v[76:79], v[150:153], v[202:205], v[76:79]
	s_setprio 0
	s_setprio 1
	v_mfma_f32_16x16x32_bf16 v[114:117], v[154:157], v[174:177], v[114:117]
	v_mfma_f32_16x16x32_bf16 v[104:107], v[166:169], v[174:177], v[104:107]
	v_mfma_f32_16x16x32_bf16 v[96:99], v[154:157], v[182:185], v[96:99]
	v_mfma_f32_16x16x32_bf16 v[88:91], v[166:169], v[182:185], v[88:91]
	v_mfma_f32_16x16x32_bf16 v[80:83], v[154:157], v[190:193], v[80:83]
	v_mfma_f32_16x16x32_bf16 v[72:75], v[166:169], v[190:193], v[72:75]
	v_mfma_f32_16x16x32_bf16 v[68:71], v[154:157], v[198:201], v[68:71]
	v_mfma_f32_16x16x32_bf16 v[64:67], v[166:169], v[198:201], v[64:67]
	v_mfma_f32_16x16x32_bf16 v[114:117], v[158:161], v[178:181], v[114:117]
	v_mfma_f32_16x16x32_bf16 v[104:107], v[170:173], v[178:181], v[104:107]
	v_mfma_f32_16x16x32_bf16 v[96:99], v[158:161], v[186:189], v[96:99]
	v_mfma_f32_16x16x32_bf16 v[88:91], v[170:173], v[186:189], v[88:91]
	v_mfma_f32_16x16x32_bf16 v[80:83], v[158:161], v[194:197], v[80:83]
	v_mfma_f32_16x16x32_bf16 v[72:75], v[170:173], v[194:197], v[72:75]
	v_mfma_f32_16x16x32_bf16 v[68:71], v[158:161], v[202:205], v[68:71]
	v_mfma_f32_16x16x32_bf16 v[64:67], v[170:173], v[202:205], v[64:67]
	s_setprio 0
.Lzqx_r0:
	s_barrier
	s_mov_b64 s[46:47], s[26:27]
	ds_read_b128 v[174:177], v141 offset:16384
	ds_read_b128 v[178:181], v141 offset:17408
	ds_read_b128 v[182:185], v141 offset:18432
	ds_read_b128 v[186:189], v141 offset:19456
	ds_read_b128 v[190:193], v141 offset:20480
	ds_read_b128 v[194:197], v141 offset:21504
	ds_read_b128 v[198:201], v141 offset:22528
	ds_read_b128 v[202:205], v141 offset:23552
	s_add_i32 s45, s45, s35
	v_lshl_add_u64 v[132:133], s[46:47], 0, v[112:113]
	s_add_u32 s46, s26, 0x20000
	s_mov_b32 m0, s45
	s_addc_u32 s47, s27, 0
	global_load_lds_dwordx4 v[132:133], off
	s_add_i32 m0, s45, 0x2000
	v_lshl_add_u64 v[132:133], s[46:47], 0, v[112:113]
	s_add_u32 s46, s26, 0x40000
	s_addc_u32 s47, s27, 0
	global_load_lds_dwordx4 v[132:133], off
	s_add_i32 s45, s48, s35
	v_lshl_add_u64 v[132:133], s[46:47], 0, v[112:113]
	s_add_u32 s46, s26, 0x60000
	s_mov_b32 m0, s45
	s_addc_u32 s47, s27, 0
	global_load_lds_dwordx4 v[132:133], off
	s_add_i32 m0, s45, 0x2000
	v_lshl_add_u64 v[132:133], s[46:47], 0, v[112:113]
	s_mov_b64 s[46:47], s[22:23]
	global_load_lds_dwordx4 v[132:133], off
	s_mov_b32 m0, s36
	v_lshl_add_u64 v[132:133], s[46:47], 0, v[130:131]
	s_add_u32 s46, s22, 0x20000
	s_addc_u32 s47, s23, 0
	global_load_lds_dwordx4 v[132:133], off
	s_mov_b32 m0, s37
	v_lshl_add_u64 v[132:133], s[46:47], 0, v[130:131]
	global_load_lds_dwordx4 v[132:133], off
	s_waitcnt vmcnt(8)
	s_waitcnt lgkmcnt(0)
	s_barrier
	s_setprio 1
	s_waitcnt lgkmcnt(0)
	s_cmp_eq_u32 s44, -2
	s_cbranch_scc1 .Lzqx_s1
; #define PG8_STAGE(bufoff, gbase, voff) do { _Pragma("unroll") for (int _i = 0; _i < 2; ++_i) { const char* gb_ = (const char*)(gbase) + _i * rstep; asm volatile("" : "+s"(gb_));   \
;         __builtin_amdgcn_global_load_lds((const unsigned*)(gb_ + (voff)), (LAS unsigned*)(lds + (bufoff) + ldsw + _i * 8192), 16, 0, 0); } } while (0)
; #define PG8_LDA(dst, b, h) do { _Pragma("unroll") for (int m = 0; m < 4; ++m) _Pragma("unroll") for (int k = 0; k < 2; ++k) dst[m][k] = *(const LAS bf16x8*)(lds + PG8_SA(b, h) + aoff + m * 2048 + k * 1024); } while (0)
; #define PG8_LDB(dst, b, h) do { _Pragma("unroll") for (int n = 0; n < 2; ++n) _Pragma("unroll") for (int k = 0; k < 2; ++k) dst[n][k] = *(const LAS bf16x8*)(lds + PG8_SB(b, h) + boff + n * 2048 + k * 1024); } while (0)
; #define PG8_WAIT_V(n) asm volatile("s_waitcnt vmcnt(" #n ")" ::: "memory")
; #define PG8_WAIT_L(n) asm volatile("s_waitcnt lgkmcnt(" #n ")" ::: "memory")
; #define PG8_BAR __builtin_amdgcn_s_barrier()
; #define PG8_SCHED __builtin_amdgcn_sched_barrier(0)
; template <class Epi, class Sched, bool ALIGN_EPI = true, bool SP2 = true, bool I8 = false, bool F8 = false>
; __device__ __forceinline__ void gemm_phase(LAS unsigned char* lds, const int K, const Sched& S, const Epi& E, const int wave) {
;     ...
;             PG8_WAIT_V(8); PG8_WAIT_L(0); PG8_BAR; PG8_MMA(1, 0, At, B0); PG8_MMA(1, 1, At, B1); PG8_BAR; PG8_SCHED;
;             PG8_LDB(B0, 1, 0); PG8_LDB(B1, 1, 1); PG8_SCHED; PG8_LDA(At, 1, 0); PG8_STAGE(PG8_SA(0, 1), a2 + hstep, voffA);
;             PG8_WAIT_V(8); PG8_WAIT_L(0); PG8_BAR; PG8_MMA(0, 0, At, B0); PG8_MMA(0, 1, At, B1); PG8_BAR; PG8_SCHED;
	v_mfma_f32_16x16x32_bf16 v[60:63], v[136:139], v[174:177], v[60:63]
	v_mfma_f32_16x16x32_bf16 v[56:59], v[146:149], v[174:177], v[56:59]
	v_mfma_f32_16x16x32_bf16 v[52:55], v[136:139], v[182:185], v[52:55]
	v_mfma_f32_16x16x32_bf16 v[44:47], v[146:149], v[182:185], v[44:47]
	v_mfma_f32_16x16x32_bf16 v[36:39], v[136:139], v[190:193], v[36:39]
	v_mfma_f32_16x16x32_bf16 v[28:31], v[146:149], v[190:193], v[28:31]
	v_mfma_f32_16x16x32_bf16 v[20:23], v[136:139], v[198:201], v[20:23]
	v_mfma_f32_16x16x32_bf16 v[12:15], v[146:149], v[198:201], v[12:15]
	v_mfma_f32_16x16x32_bf16 v[60:63], v[142:145], v[178:181], v[60:63]
	v_mfma_f32_16x16x32_bf16 v[56:59], v[150:153], v[178:181], v[56:59]
	v_mfma_f32_16x16x32_bf16 v[52:55], v[142:145], v[186:189], v[52:55]
	v_mfma_f32_16x16x32_bf16 v[44:47], v[150:153], v[186:189], v[44:47]
	v_mfma_f32_16x16x32_bf16 v[36:39], v[142:145], v[194:197], v[36:39]
	v_mfma_f32_16x16x32_bf16 v[28:31], v[150:153], v[194:197], v[28:31]
	v_mfma_f32_16x16x32_bf16 v[20:23], v[142:145], v[202:205], v[20:23]
	v_mfma_f32_16x16x32_bf16 v[12:15], v[150:153], v[202:205], v[12:15]
	s_setprio 0
	s_setprio 1
	v_mfma_f32_16x16x32_bf16 v[48:51], v[154:157], v[174:177], v[48:51]
	v_mfma_f32_16x16x32_bf16 v[40:43], v[166:169], v[174:177], v[40:43]
	v_mfma_f32_16x16x32_bf16 v[32:35], v[154:157], v[182:185], v[32:35]
	v_mfma_f32_16x16x32_bf16 v[24:27], v[166:169], v[182:185], v[24:27]
	v_mfma_f32_16x16x32_bf16 v[16:19], v[154:157], v[190:193], v[16:19]
	v_mfma_f32_16x16x32_bf16 v[8:11], v[166:169], v[190:193], v[8:11]
	v_mfma_f32_16x16x32_bf16 v[4:7], v[154:157], v[198:201], v[4:7]
	v_mfma_f32_16x16x32_bf16 v[0:3], v[166:169], v[198:201], v[0:3]
	v_mfma_f32_16x16x32_bf16 v[48:51], v[158:161], v[178:181], v[48:51]
	v_mfma_f32_16x16x32_bf16 v[40:43], v[170:173], v[178:181], v[40:43]
	v_mfma_f32_16x16x32_bf16 v[32:35], v[158:161], v[186:189], v[32:35]
	v_mfma_f32_16x16x32_bf16 v[24:27], v[170:173], v[186:189], v[24:27]
	v_mfma_f32_16x16x32_bf16 v[16:19], v[158:161], v[194:197], v[16:19]
	v_mfma_f32_16x16x32_bf16 v[8:11], v[170:173], v[194:197], v[8:11]
	v_mfma_f32_16x16x32_bf16 v[4:7], v[158:161], v[202:205], v[4:7]
	v_mfma_f32_16x16x32_bf16 v[0:3], v[170:173], v[202:205], v[0:3]
	s_setprio 0
.Lzqx_r1:
	s_barrier
	s_add_i32 s45, 0, 0x18000
	v_add_u32_e32 v132, s45, v135
	s_add_i32 s48, 0, 0x1c000
	ds_read_b128 v[136:139], v132
	ds_read_b128 v[142:145], v132 offset:1024
	ds_read_b128 v[146:149], v132 offset:2048
	ds_read_b128 v[150:153], v132 offset:3072
	v_add_u32_e32 v132, s48, v135
	ds_read_b128 v[154:157], v132
	ds_read_b128 v[158:161], v132 offset:1024
	ds_read_b128 v[166:169], v132 offset:2048
	ds_read_b128 v[170:173], v132 offset:3072
	s_add_u32 s46, s22, 0x40000
	s_addc_u32 s47, s23, 0
	ds_read_b128 v[174:177], v141 offset:32768
	ds_read_b128 v[178:181], v141 offset:33792
	ds_read_b128 v[182:185], v141 offset:34816
	ds_read_b128 v[186:189], v141 offset:35840
	ds_read_b128 v[190:193], v141 offset:36864
	ds_read_b128 v[194:197], v141 offset:37888
	ds_read_b128 v[198:201], v141 offset:38912
	ds_read_b128 v[202:205], v141 offset:39936
	s_mov_b32 m0, s38
	v_lshl_add_u64 v[132:133], s[46:47], 0, v[130:131]
	s_add_u32 s46, s22, 0x60000
	s_addc_u32 s47, s23, 0
	global_load_lds_dwordx4 v[132:133], off
	s_mov_b32 m0, s39
	v_lshl_add_u64 v[132:133], s[46:47], 0, v[130:131]
	global_load_lds_dwordx4 v[132:133], off
	s_waitcnt vmcnt(8)
	s_waitcnt lgkmcnt(0)
	s_barrier
	s_setprio 1
	s_waitcnt lgkmcnt(0)
	v_mfma_f32_16x16x32_bf16 v[126:129], v[136:139], v[174:177], v[126:129]
	v_mfma_f32_16x16x32_bf16 v[122:125], v[146:149], v[174:177], v[122:125]
	v_mfma_f32_16x16x32_bf16 v[118:121], v[136:139], v[182:185], v[118:121]
	v_mfma_f32_16x16x32_bf16 v[108:111], v[146:149], v[182:185], v[108:111]
	v_mfma_f32_16x16x32_bf16 v[100:103], v[136:139], v[190:193], v[100:103]
	v_mfma_f32_16x16x32_bf16 v[92:95], v[146:149], v[190:193], v[92:95]
	v_mfma_f32_16x16x32_bf16 v[84:87], v[136:139], v[198:201], v[84:87]
	v_mfma_f32_16x16x32_bf16 v[76:79], v[146:149], v[198:201], v[76:79]
	v_mfma_f32_16x16x32_bf16 v[126:129], v[142:145], v[178:181], v[126:129]
	v_mfma_f32_16x16x32_bf16 v[122:125], v[150:153], v[178:181], v[122:125]
	v_mfma_f32_16x16x32_bf16 v[118:121], v[142:145], v[186:189], v[118:121]
	v_mfma_f32_16x16x32_bf16 v[108:111], v[150:153], v[186:189], v[108:111]
	v_mfma_f32_16x16x32_bf16 v[100:103], v[142:145], v[194:197], v[100:103]
	v_mfma_f32_16x16x32_bf16 v[92:95], v[150:153], v[194:197], v[92:95]
	v_mfma_f32_16x16x32_bf16 v[84:87], v[142:145], v[202:205], v[84:87]
	v_mfma_f32_16x16x32_bf16 v[76:79], v[150:153], v[202:205], v[76:79]
	s_setprio 0
	s_setprio 1
	v_mfma_f32_16x16x32_bf16 v[114:117], v[154:157], v[174:177], v[114:117]
	v_mfma_f32_16x16x32_bf16 v[104:107], v[166:169], v[174:177], v[104:107]
	v_mfma_f32_16x16x32_bf16 v[96:99], v[154:157], v[182:185], v[96:99]
	v_mfma_f32_16x16x32_bf16 v[88:91], v[166:169], v[182:185], v[88:91]
	v_mfma_f32_16x16x32_bf16 v[80:83], v[154:157], v[190:193], v[80:83]
	v_mfma_f32_16x16x32_bf16 v[72:75], v[166:169], v[190:193], v[72:75]
	v_mfma_f32_16x16x32_bf16 v[68:71], v[154:157], v[198:201], v[68:71]
	v_mfma_f32_16x16x32_bf16 v[64:67], v[166:169], v[198:201], v[64:67]
	v_mfma_f32_16x16x32_bf16 v[114:117], v[158:161], v[178:181], v[114:117]
	v_mfma_f32_16x16x32_bf16 v[104:107], v[170:173], v[178:181], v[104:107]
	v_mfma_f32_16x16x32_bf16 v[96:99], v[158:161], v[186:189], v[96:99]
	v_mfma_f32_16x16x32_bf16 v[88:91], v[170:173], v[186:189], v[88:91]
	v_mfma_f32_16x16x32_bf16 v[80:83], v[158:161], v[194:197], v[80:83]
	v_mfma_f32_16x16x32_bf16 v[72:75], v[170:173], v[194:197], v[72:75]
	v_mfma_f32_16x16x32_bf16 v[68:71], v[158:161], v[202:205], v[68:71]
	v_mfma_f32_16x16x32_bf16 v[64:67], v[170:173], v[202:205], v[64:67]
	s_setprio 0
	s_barrier
; #define PG8_STAGE(bufoff, gbase, voff) do { _Pragma("unroll") for (int _i = 0; _i < 2; ++_i) { const char* gb_ = (const char*)(gbase) + _i * rstep; asm volatile("" : "+s"(gb_));   \
;         __builtin_amdgcn_global_load_lds((const unsigned*)(gb_ + (voff)), (LAS unsigned*)(lds + (bufoff) + ldsw + _i * 8192), 16, 0, 0); } } while (0)
; #define PG8_LDA(dst, b, h) do { _Pragma("unroll") for (int m = 0; m < 4; ++m) _Pragma("unroll") for (int k = 0; k < 2; ++k) dst[m][k] = *(const LAS bf16x8*)(lds + PG8_SA(b, h) + aoff + m * 2048 + k * 1024); } while (0)
; #define PG8_WAIT_V(n) asm volatile("s_waitcnt vmcnt(" #n ")" ::: "memory")
; #define PG8_WAIT_L(n) asm volatile("s_waitcnt lgkmcnt(" #n ")" ::: "memory")
; template <class Epi, class Sched, bool ALIGN_EPI = true, bool SP2 = true, bool I8 = false, bool F8 = false>
; __device__ __forceinline__ void gemm_phase(LAS unsigned char* lds, const int K, const Sched& S, const Epi& E, const int wave) {
;     ...
;         for (int t = 0; t < nt; t += 2) {
;             const bool last = (t == nt - 2);
;             const char* a1 = cA + (size_t)(t + 1) * kstep;
;             const char* a2 = last ? nA : cA + (size_t)(t + 2) * kstep; const char* b2 = last ? nB : cB + (size_t)(t + 2) * kstep;
;             const char* a3 = a2 + kstep; const char* b3 = b2 + kstep;
;             if constexpr (SP2) {
;             PG8_LDB(B0, 0, 0); PG8_LDB(B1, 0, 1); PG8_SCHED; PG8_LDA(At, 0, 0); PG8_STAGE(PG8_SA(1, 1), a1 + hstep, voffA);
;             PG8_WAIT_V(8); PG8_WAIT_L(0); PG8_BAR; PG8_MMA(0, 0, At, B0); PG8_MMA(0, 1, At, B1); PG8_BAR; PG8_SCHED;
;             PG8_LDA(At, 0, 1); PG8_STAGE(PG8_SB(0, 0), b2, voffB); PG8_STAGE(PG8_SB(0, 1), b2 + hstep, voffB); PG8_STAGE(PG8_SA(0, 0), a2, voffA);
;             PG8_WAIT_V(8); PG8_WAIT_L(0); PG8_BAR; PG8_MMA(1, 0, At, B0); PG8_MMA(1, 1, At, B1); PG8_BAR; PG8_SCHED;
;             PG8_LDB(B0, 1, 0); PG8_LDB(B1, 1, 1); PG8_SCHED; PG8_LDA(At, 1, 0); PG8_STAGE(PG8_SA(0, 1), a2 + hstep, voffA);
;             PG8_WAIT_V(8); PG8_WAIT_L(0); PG8_BAR; PG8_MMA(0, 0, At, B0); PG8_MMA(0, 1, At, B1); PG8_BAR; PG8_SCHED;
;             PG8_LDA(At, 1, 1); PG8_STAGE(PG8_SB(1, 0), b3, voffB); PG8_STAGE(PG8_SB(1, 1), b3 + hstep, voffB); PG8_STAGE(PG8_SA(1, 0), a3, voffA);
;             PG8_WAIT_V(8); PG8_WAIT_L(0); PG8_BAR; PG8_MMA(1, 0, At, B0); PG8_MMA(1, 1, At, B1); PG8_BAR; PG8_SCHED;
	s_add_u32 s46, s26, 0x80
	s_addc_u32 s47, s27, 0
	ds_read_b128 v[174:177], v141 offset:49152
	ds_read_b128 v[178:181], v141 offset:50176
	ds_read_b128 v[182:185], v141 offset:51200
	ds_read_b128 v[186:189], v141 offset:52224
	ds_read_b128 v[190:193], v141 offset:53248
	ds_read_b128 v[194:197], v141 offset:54272
	ds_read_b128 v[198:201], v141 offset:55296
	ds_read_b128 v[202:205], v141 offset:56320
	s_add_i32 s45, s45, s35
	v_lshl_add_u64 v[132:133], s[46:47], 0, v[112:113]
	s_add_u32 s46, s26, 0x20080
	s_mov_b32 m0, s45
	s_addc_u32 s47, s27, 0
	global_load_lds_dwordx4 v[132:133], off
	s_add_i32 m0, s45, 0x2000
	v_lshl_add_u64 v[132:133], s[46:47], 0, v[112:113]
	s_add_u32 s46, s26, 0x40080
	s_addc_u32 s47, s27, 0
	s_add_i32 s45, s48, s35
	global_load_lds_dwordx4 v[132:133], off
	s_mov_b32 m0, s45
	v_lshl_add_u64 v[132:133], s[46:47], 0, v[112:113]
	s_add_u32 s26, s26, 0x60080
	global_load_lds_dwordx4 v[132:133], off
	s_addc_u32 s27, s27, 0
	s_add_i32 m0, s45, 0x2000
	s_add_u32 s22, s22, 0x20080
	v_lshl_add_u64 v[132:133], s[26:27], 0, v[112:113]
	global_load_lds_dwordx4 v[132:133], off
	s_mov_b32 m0, s41
	v_lshl_add_u64 v[132:133], s[24:25], 0, v[130:131]
	s_addc_u32 s23, s23, 0
	global_load_lds_dwordx4 v[132:133], off
	s_mov_b32 m0, s42
	v_lshl_add_u64 v[132:133], s[22:23], 0, v[130:131]
	global_load_lds_dwordx4 v[132:133], off
	s_waitcnt vmcnt(8)
	s_waitcnt lgkmcnt(0)
	s_barrier
	s_setprio 1
	s_waitcnt lgkmcnt(0)
	v_mfma_f32_16x16x32_bf16 v[60:63], v[136:139], v[174:177], v[60:63]
	v_mfma_f32_16x16x32_bf16 v[56:59], v[146:149], v[174:177], v[56:59]
	v_mfma_f32_16x16x32_bf16 v[52:55], v[136:139], v[182:185], v[52:55]
	v_mfma_f32_16x16x32_bf16 v[44:47], v[146:149], v[182:185], v[44:47]
	v_mfma_f32_16x16x32_bf16 v[36:39], v[136:139], v[190:193], v[36:39]
	v_mfma_f32_16x16x32_bf16 v[28:31], v[146:149], v[190:193], v[28:31]
	v_mfma_f32_16x16x32_bf16 v[20:23], v[136:139], v[198:201], v[20:23]
	v_mfma_f32_16x16x32_bf16 v[12:15], v[146:149], v[198:201], v[12:15]
	v_mfma_f32_16x16x32_bf16 v[60:63], v[142:145], v[178:181], v[60:63]
	v_mfma_f32_16x16x32_bf16 v[56:59], v[150:153], v[178:181], v[56:59]
	v_mfma_f32_16x16x32_bf16 v[52:55], v[142:145], v[186:189], v[52:55]
	v_mfma_f32_16x16x32_bf16 v[44:47], v[150:153], v[186:189], v[44:47]
	v_mfma_f32_16x16x32_bf16 v[36:39], v[142:145], v[194:197], v[36:39]
	v_mfma_f32_16x16x32_bf16 v[28:31], v[150:153], v[194:197], v[28:31]
	v_mfma_f32_16x16x32_bf16 v[20:23], v[142:145], v[202:205], v[20:23]
	v_mfma_f32_16x16x32_bf16 v[12:15], v[150:153], v[202:205], v[12:15]
	s_setprio 0
	s_setprio 1
	v_mfma_f32_16x16x32_bf16 v[48:51], v[154:157], v[174:177], v[48:51]
	v_mfma_f32_16x16x32_bf16 v[40:43], v[166:169], v[174:177], v[40:43]
	v_mfma_f32_16x16x32_bf16 v[32:35], v[154:157], v[182:185], v[32:35]
	v_mfma_f32_16x16x32_bf16 v[24:27], v[166:169], v[182:185], v[24:27]
	v_mfma_f32_16x16x32_bf16 v[16:19], v[154:157], v[190:193], v[16:19]
	v_mfma_f32_16x16x32_bf16 v[8:11], v[166:169], v[190:193], v[8:11]
	v_mfma_f32_16x16x32_bf16 v[4:7], v[154:157], v[198:201], v[4:7]
	v_mfma_f32_16x16x32_bf16 v[0:3], v[166:169], v[198:201], v[0:3]
	v_mfma_f32_16x16x32_bf16 v[48:51], v[158:161], v[178:181], v[48:51]
	v_mfma_f32_16x16x32_bf16 v[40:43], v[170:173], v[178:181], v[40:43]
	v_mfma_f32_16x16x32_bf16 v[32:35], v[158:161], v[186:189], v[32:35]
	v_mfma_f32_16x16x32_bf16 v[24:27], v[170:173], v[186:189], v[24:27]
	v_mfma_f32_16x16x32_bf16 v[16:19], v[158:161], v[194:197], v[16:19]
	v_mfma_f32_16x16x32_bf16 v[8:11], v[170:173], v[194:197], v[8:11]
	v_mfma_f32_16x16x32_bf16 v[4:7], v[158:161], v[202:205], v[4:7]
	v_mfma_f32_16x16x32_bf16 v[0:3], v[170:173], v[202:205], v[0:3]
	s_setprio 0
	s_barrier
	s_add_i32 s44, s44, 2
	s_add_u32 s11, s11, 0x100
	s_addc_u32 s13, s13, 0
	s_add_u32 s20, s20, 0x100
	s_addc_u32 s21, s21, 0
	s_cmp_gt_u32 s44, 13
	s_cbranch_scc0 .LBB0_1170
	s_and_b64 vcc, exec, s[8:9]
	s_cbranch_vccz .LBB0_1173
	s_barrier

; __device__ __forceinline__ int fresh_tid(int wave) { return wave * 64 + fresh_lane(); }
; __device__ __forceinline__ unsigned xb_xcc_id() { return (unsigned)__builtin_amdgcn_s_getreg((3 << 11) | 20) & 0xFu; }
; __device__ __forceinline__ void xcd_barrier(const XcdBarrier& b) {
;     asm volatile("s_waitcnt vmcnt(0)" ::: "memory");
;     __syncthreads();
;     if (fresh_tid(b.wave) == 0) {
;         unsigned* bar = b.bar; asm volatile("" : "+s"(bar));
;         __builtin_amdgcn_s_waitcnt(0);
;         const unsigned bx = xb_xcc_id();
;         unsigned nloc = b.st[0], nx = b.st[1];
;         if (nloc == 0u) { xcd_barrier_complete(bar, bx, nloc, nx); b.st[0] = nloc; b.st[1] = nx; }
.LBB0_1177:
	s_mov_b32 s0, s93
	s_waitcnt vmcnt(0)
	s_waitcnt lgkmcnt(0)
	s_barrier
	s_nop 0
	v_mbcnt_lo_u32_b32 v0, -1, s0
	v_mbcnt_hi_u32_b32 v0, -1, v0
	v_readlane_b32 s0, v254, 17
	s_nop 1
	v_cmp_eq_u32_e32 vcc, s0, v0
	s_and_saveexec_b64 s[0:1], vcc
	s_branch .LBB0_1221
	v_readlane_b32 s2, v253, 53
	v_readlane_b32 s5, v254, 8
	v_readlane_b32 s3, v253, 54
	s_waitcnt vmcnt(0) expcnt(0) lgkmcnt(0)
	v_mov_b32_e32 v0, s5
	s_getreg_b32 s4, hwreg(HW_REG_XCC_ID, 0, 4)
	ds_read_b32 v2, v0
	v_readlane_b32 s5, v254, 9
	s_and_b32 s33, s4, 15
	s_waitcnt lgkmcnt(0)
	v_cmp_ne_u32_e32 vcc, 0, v2
	v_mov_b32_e32 v0, s5
	ds_read_b32 v0, v0
	s_cbranch_vccnz .LBB0_1192
	v_readlane_b32 s4, v253, 3
	v_readlane_b32 s5, v253, 4
	s_load_dwordx2 s[8:9], s[4:5], 0x4
	s_add_u32 s4, s2, 0x1000
	s_addc_u32 s5, s3, 0
	s_add_u32 s6, s2, 0x1100
	s_addc_u32 s7, s3, 0
	s_waitcnt lgkmcnt(0)
	s_mul_i32 s30, s8, s78
	s_add_u32 s8, s2, 0x1200
	s_mul_i32 s30, s30, s9
	s_addc_u32 s9, s3, 0
	s_add_u32 s10, s2, 0x1300
	s_addc_u32 s11, s3, 0
	s_mov_b32 s31, 1
	s_mov_b64 s[12:13], 0
	s_branch .LBB0_1182

; __global__ void __launch_bounds__(NTHREADS, 2) mk_fwd(Params P) {
;     ...
;             for (int u = c, rnd = 0; u < B * XH * (S / 256); u += G, ++rnd) { int qt = u & 15, h = (u >> 4) & 3, b = u >> 6;
;                 if (G == 256) { const int idx = rnd * 32 + (c >> 3), bh = (c & 7) * 4 + (idx >> 4); qt = idx & 15; h = bh & 3; b = bh >> 2; }
.LBB0_1224:
	v_readlane_b32 s4, v254, 10
	v_readlane_b32 s5, v254, 11
	s_andn2_b64 vcc, exec, s[4:5]
	s_cbranch_vccnz .LBB0_1226
	s_bfe_u32 s36, s25, 0x10003
	s_lshl_b32 s36, s36, 1
	s_add_i32 s36, s36, s27
	s_lshr_b32 s4, s26, 2
	s_and_b32 s5, s25, 7
	s_lshr_b32 s8, s25, 4
	s_lshl_b32 s8, s8, 3
	s_or_b32 s5, s5, s8
	s_branch .LBB0_1227

; #define PG8_STAGE(bufoff, gbase, voff) do { _Pragma("unroll") for (int _i = 0; _i < 2; ++_i) { const char* gb_ = (const char*)(gbase) + _i * rstep; asm volatile("" : "+s"(gb_));   \
;         __builtin_amdgcn_global_load_lds((const unsigned*)(gb_ + (voff)), (LAS unsigned*)(lds + (bufoff) + ldsw + _i * 8192), 16, 0, 0); } } while (0)
; #define PG8_LDA(dst, b, h) do { _Pragma("unroll") for (int m = 0; m < 4; ++m) _Pragma("unroll") for (int k = 0; k < 2; ++k) dst[m][k] = *(const LAS bf16x8*)(lds + PG8_SA(b, h) + aoff + m * 2048 + k * 1024); } while (0)
; #define PG8_LDB(dst, b, h) do { _Pragma("unroll") for (int n = 0; n < 2; ++n) _Pragma("unroll") for (int k = 0; k < 2; ++k) dst[n][k] = *(const LAS bf16x8*)(lds + PG8_SB(b, h) + boff + n * 2048 + k * 1024); } while (0)
; #define PG8_WAIT_V(n) asm volatile("s_waitcnt vmcnt(" #n ")" ::: "memory")
; #define PG8_WAIT_L(n) asm volatile("s_waitcnt lgkmcnt(" #n ")" ::: "memory")
; #define PG8_BAR __builtin_amdgcn_s_barrier()
; template <class Epi, class Sched, bool ALIGN_EPI = true, bool SP2 = true, bool I8 = false, bool F8 = false>
; __device__ __forceinline__ void gemm_phase(LAS unsigned char* lds, const int K, const Sched& S, const Epi& E, const int wave) {
;     ...
;         for (int t = 0; t < nt; t += 2) {
;             const bool last = (t == nt - 2);
;             const char* a1 = cA + (size_t)(t + 1) * kstep;
;             const char* a2 = last ? nA : cA + (size_t)(t + 2) * kstep; const char* b2 = last ? nB : cB + (size_t)(t + 2) * kstep;
;             const char* a3 = a2 + kstep; const char* b3 = b2 + kstep;
;             if constexpr (SP2) {
;             PG8_LDB(B0, 0, 0); PG8_LDB(B1, 0, 1); PG8_SCHED; PG8_LDA(At, 0, 0); PG8_STAGE(PG8_SA(1, 1), a1 + hstep, voffA);
;             PG8_WAIT_V(8); PG8_WAIT_L(0); PG8_BAR; PG8_MMA(0, 0, At, B0); PG8_MMA(0, 1, At, B1); PG8_BAR; PG8_SCHED;
;             PG8_LDA(At, 0, 1); PG8_STAGE(PG8_SB(0, 0), b2, voffB); PG8_STAGE(PG8_SB(0, 1), b2 + hstep, voffB); PG8_STAGE(PG8_SA(0, 0), a2, voffA);
;             PG8_WAIT_V(8); PG8_WAIT_L(0); PG8_BAR; PG8_MMA(1, 0, At, B0); PG8_MMA(1, 1, At, B1); PG8_BAR; PG8_SCHED;
;     ...
;         for (int a = 0; a < 2; ++a)
; #pragma unroll
;             for (int b = 0; b < 2; ++b)
; #pragma unroll
;                 for (int m = 0; m < 4; ++m)
; #pragma unroll
;                     for (int n = 0; n < 2; ++n) acc[a][b][m][n] = (acc_t){0, 0, 0, 0};
.LBB0_1299:
	s_add_u32 s11, s22, 0x100
	s_addc_u32 s13, s23, 0
	s_add_u32 s20, s20, 0x30080
	s_addc_u32 s21, s21, 0
	s_mov_b32 s19, -2
.LBB0_1300:
	s_add_u32 s22, s20, 0xfffd0080
	s_addc_u32 s23, s21, -1
	s_cmp_eq_u32 s19, 4
	s_cselect_b32 s22, s14, s22
	s_cselect_b32 s23, s15, s23
	s_cselect_b32 s26, s16, s11
	s_cselect_b32 s27, s17, s13
	s_add_u32 s24, s22, 0x80
	s_addc_u32 s25, s23, 0
	s_add_i32 s48, 0, 0x10000
	s_add_i32 s49, 0, 0x14000
	v_add_u32_e32 v142, s48, v165
	v_add_u32_e32 v160, s49, v165
	ds_read_b128 v[130:133], v142
	ds_read_b128 v[134:137], v142 offset:1024
	ds_read_b128 v[138:141], v142 offset:2048
	ds_read_b128 v[142:145], v142 offset:3072
	ds_read_b128 v[146:149], v160
	ds_read_b128 v[150:153], v160 offset:1024
	ds_read_b128 v[156:159], v160 offset:2048
	ds_read_b128 v[160:163], v160 offset:3072
	s_add_u32 s46, s20, 0xffff0000
	s_addc_u32 s47, s21, -1
	ds_read_b128 v[168:171], v166
	ds_read_b128 v[172:175], v166 offset:1024
	ds_read_b128 v[176:179], v166 offset:2048
	ds_read_b128 v[180:183], v166 offset:3072
	ds_read_b128 v[184:187], v166 offset:4096
	ds_read_b128 v[188:191], v166 offset:5120
	ds_read_b128 v[192:195], v166 offset:6144
	ds_read_b128 v[196:199], v166 offset:7168
	s_add_i32 m0, s35, 0xc000
	v_lshl_add_u64 v[200:201], s[46:47], 0, v[154:155]
	s_mov_b64 s[46:47], s[20:21]
	global_load_lds_dwordx4 v[200:201], off
	s_add_i32 m0, s35, 0xe000
	v_lshl_add_u64 v[200:201], s[46:47], 0, v[154:155]
	global_load_lds_dwordx4 v[200:201], off
	s_waitcnt vmcnt(8)
	s_waitcnt lgkmcnt(0)
	s_barrier
	s_setprio 1
	s_waitcnt lgkmcnt(0)
	s_cmp_eq_u32 s19, -2
	s_cbranch_scc1 .Lzxo_s0
	v_mfma_f32_16x16x32_bf16 v[126:129], v[130:133], v[168:171], v[126:129]
	v_mfma_f32_16x16x32_bf16 v[122:125], v[138:141], v[168:171], v[122:125]
	v_mfma_f32_16x16x32_bf16 v[108:111], v[130:133], v[176:179], v[108:111]
	v_mfma_f32_16x16x32_bf16 v[104:107], v[138:141], v[176:179], v[104:107]
	v_mfma_f32_16x16x32_bf16 v[92:95], v[130:133], v[184:187], v[92:95]
	v_mfma_f32_16x16x32_bf16 v[88:91], v[138:141], v[184:187], v[88:91]
	v_mfma_f32_16x16x32_bf16 v[76:79], v[130:133], v[192:195], v[76:79]
	v_mfma_f32_16x16x32_bf16 v[72:75], v[138:141], v[192:195], v[72:75]
	v_mfma_f32_16x16x32_bf16 v[126:129], v[134:137], v[172:175], v[126:129]
	v_mfma_f32_16x16x32_bf16 v[122:125], v[142:145], v[172:175], v[122:125]
	v_mfma_f32_16x16x32_bf16 v[108:111], v[134:137], v[180:183], v[108:111]
	v_mfma_f32_16x16x32_bf16 v[104:107], v[142:145], v[180:183], v[104:107]
	v_mfma_f32_16x16x32_bf16 v[92:95], v[134:137], v[188:191], v[92:95]
	v_mfma_f32_16x16x32_bf16 v[88:91], v[142:145], v[188:191], v[88:91]
	v_mfma_f32_16x16x32_bf16 v[76:79], v[134:137], v[196:199], v[76:79]
	v_mfma_f32_16x16x32_bf16 v[72:75], v[142:145], v[196:199], v[72:75]
	s_setprio 0
	s_setprio 1
	v_mfma_f32_16x16x32_bf16 v[118:121], v[146:149], v[168:171], v[118:121]
	v_mfma_f32_16x16x32_bf16 v[114:117], v[156:159], v[168:171], v[114:117]
	v_mfma_f32_16x16x32_bf16 v[100:103], v[146:149], v[176:179], v[100:103]
	v_mfma_f32_16x16x32_bf16 v[96:99], v[156:159], v[176:179], v[96:99]
	v_mfma_f32_16x16x32_bf16 v[84:87], v[146:149], v[184:187], v[84:87]
	v_mfma_f32_16x16x32_bf16 v[80:83], v[156:159], v[184:187], v[80:83]
	v_mfma_f32_16x16x32_bf16 v[68:71], v[146:149], v[192:195], v[68:71]
	v_mfma_f32_16x16x32_bf16 v[64:67], v[156:159], v[192:195], v[64:67]
	v_mfma_f32_16x16x32_bf16 v[118:121], v[150:153], v[172:175], v[118:121]
	v_mfma_f32_16x16x32_bf16 v[114:117], v[160:163], v[172:175], v[114:117]
	v_mfma_f32_16x16x32_bf16 v[100:103], v[150:153], v[180:183], v[100:103]
	v_mfma_f32_16x16x32_bf16 v[96:99], v[160:163], v[180:183], v[96:99]
	v_mfma_f32_16x16x32_bf16 v[84:87], v[150:153], v[188:191], v[84:87]
	v_mfma_f32_16x16x32_bf16 v[80:83], v[160:163], v[188:191], v[80:83]
	v_mfma_f32_16x16x32_bf16 v[68:71], v[150:153], v[196:199], v[68:71]
	v_mfma_f32_16x16x32_bf16 v[64:67], v[160:163], v[196:199], v[64:67]
	s_setprio 0
.Lzxo_r0:
	s_barrier
	s_mov_b64 s[46:47], s[26:27]
	ds_read_b128 v[168:171], v166 offset:16384
	ds_read_b128 v[172:175], v166 offset:17408
	ds_read_b128 v[176:179], v166 offset:18432
	ds_read_b128 v[180:183], v166 offset:19456
	ds_read_b128 v[184:187], v166 offset:20480
	ds_read_b128 v[188:191], v166 offset:21504
	ds_read_b128 v[192:195], v166 offset:22528
	ds_read_b128 v[196:199], v166 offset:23552
	s_add_i32 s48, s48, s34
	v_lshl_add_u64 v[200:201], s[46:47], 0, v[112:113]
	s_add_u32 s46, s26, 0x10000
	s_mov_b32 m0, s48
	s_addc_u32 s47, s27, 0
	global_load_lds_dwordx4 v[200:201], off
	s_add_i32 m0, s48, 0x2000
	v_lshl_add_u64 v[200:201], s[46:47], 0, v[112:113]
	s_add_u32 s46, s26, 0x20000
	s_addc_u32 s47, s27, 0
	global_load_lds_dwordx4 v[200:201], off
	s_add_i32 s48, s49, s34
	v_lshl_add_u64 v[200:201], s[46:47], 0, v[112:113]
	s_add_u32 s46, s26, 0x30000
	s_mov_b32 m0, s48
	s_addc_u32 s47, s27, 0
	global_load_lds_dwordx4 v[200:201], off
	s_add_i32 m0, s48, 0x2000
	v_lshl_add_u64 v[200:201], s[46:47], 0, v[112:113]
	s_mov_b64 s[46:47], s[22:23]
	global_load_lds_dwordx4 v[200:201], off
	s_mov_b32 m0, s35
	v_lshl_add_u64 v[200:201], s[46:47], 0, v[154:155]
	s_add_u32 s46, s22, 0x10000
	s_addc_u32 s47, s23, 0
	global_load_lds_dwordx4 v[200:201], off
	s_mov_b32 m0, s36
	v_lshl_add_u64 v[200:201], s[46:47], 0, v[154:155]
	global_load_lds_dwordx4 v[200:201], off
	s_waitcnt vmcnt(8)
	s_waitcnt lgkmcnt(0)
	s_barrier
	s_setprio 1
	s_waitcnt lgkmcnt(0)
	s_cmp_eq_u32 s19, -2
	s_cbranch_scc1 .Lzxo_s1
; #define PG8_STAGE(bufoff, gbase, voff) do { _Pragma("unroll") for (int _i = 0; _i < 2; ++_i) { const char* gb_ = (const char*)(gbase) + _i * rstep; asm volatile("" : "+s"(gb_));   \
;         __builtin_amdgcn_global_load_lds((const unsigned*)(gb_ + (voff)), (LAS unsigned*)(lds + (bufoff) + ldsw + _i * 8192), 16, 0, 0); } } while (0)
; #define PG8_LDA(dst, b, h) do { _Pragma("unroll") for (int m = 0; m < 4; ++m) _Pragma("unroll") for (int k = 0; k < 2; ++k) dst[m][k] = *(const LAS bf16x8*)(lds + PG8_SA(b, h) + aoff + m * 2048 + k * 1024); } while (0)
; #define PG8_LDB(dst, b, h) do { _Pragma("unroll") for (int n = 0; n < 2; ++n) _Pragma("unroll") for (int k = 0; k < 2; ++k) dst[n][k] = *(const LAS bf16x8*)(lds + PG8_SB(b, h) + boff + n * 2048 + k * 1024); } while (0)
; #define PG8_WAIT_V(n) asm volatile("s_waitcnt vmcnt(" #n ")" ::: "memory")
; #define PG8_WAIT_L(n) asm volatile("s_waitcnt lgkmcnt(" #n ")" ::: "memory")
; #define PG8_BAR __builtin_amdgcn_s_barrier()
; #define PG8_SCHED __builtin_amdgcn_sched_barrier(0)
; template <class Epi, class Sched, bool ALIGN_EPI = true, bool SP2 = true, bool I8 = false, bool F8 = false>
; __device__ __forceinline__ void gemm_phase(LAS unsigned char* lds, const int K, const Sched& S, const Epi& E, const int wave) {
;     ...
;             PG8_WAIT_V(8); PG8_WAIT_L(0); PG8_BAR; PG8_MMA(1, 0, At, B0); PG8_MMA(1, 1, At, B1); PG8_BAR; PG8_SCHED;
;             PG8_LDB(B0, 1, 0); PG8_LDB(B1, 1, 1); PG8_SCHED; PG8_LDA(At, 1, 0); PG8_STAGE(PG8_SA(0, 1), a2 + hstep, voffA);
;             PG8_WAIT_V(8); PG8_WAIT_L(0); PG8_BAR; PG8_MMA(0, 0, At, B0); PG8_MMA(0, 1, At, B1); PG8_BAR; PG8_SCHED;
	v_mfma_f32_16x16x32_bf16 v[60:63], v[130:133], v[168:171], v[60:63]
	v_mfma_f32_16x16x32_bf16 v[56:59], v[138:141], v[168:171], v[56:59]
	v_mfma_f32_16x16x32_bf16 v[44:47], v[130:133], v[176:179], v[44:47]
	v_mfma_f32_16x16x32_bf16 v[40:43], v[138:141], v[176:179], v[40:43]
	v_mfma_f32_16x16x32_bf16 v[28:31], v[130:133], v[184:187], v[28:31]
	v_mfma_f32_16x16x32_bf16 v[24:27], v[138:141], v[184:187], v[24:27]
	v_mfma_f32_16x16x32_bf16 v[12:15], v[130:133], v[192:195], v[12:15]
	v_mfma_f32_16x16x32_bf16 v[8:11], v[138:141], v[192:195], v[8:11]
	v_mfma_f32_16x16x32_bf16 v[60:63], v[134:137], v[172:175], v[60:63]
	v_mfma_f32_16x16x32_bf16 v[56:59], v[142:145], v[172:175], v[56:59]
	v_mfma_f32_16x16x32_bf16 v[44:47], v[134:137], v[180:183], v[44:47]
	v_mfma_f32_16x16x32_bf16 v[40:43], v[142:145], v[180:183], v[40:43]
	v_mfma_f32_16x16x32_bf16 v[28:31], v[134:137], v[188:191], v[28:31]
	v_mfma_f32_16x16x32_bf16 v[24:27], v[142:145], v[188:191], v[24:27]
	v_mfma_f32_16x16x32_bf16 v[12:15], v[134:137], v[196:199], v[12:15]
	v_mfma_f32_16x16x32_bf16 v[8:11], v[142:145], v[196:199], v[8:11]
	s_setprio 0
	s_setprio 1
	v_mfma_f32_16x16x32_bf16 v[52:55], v[146:149], v[168:171], v[52:55]
	v_mfma_f32_16x16x32_bf16 v[48:51], v[156:159], v[168:171], v[48:51]
	v_mfma_f32_16x16x32_bf16 v[36:39], v[146:149], v[176:179], v[36:39]
	v_mfma_f32_16x16x32_bf16 v[32:35], v[156:159], v[176:179], v[32:35]
	v_mfma_f32_16x16x32_bf16 v[20:23], v[146:149], v[184:187], v[20:23]
	v_mfma_f32_16x16x32_bf16 v[16:19], v[156:159], v[184:187], v[16:19]
	v_mfma_f32_16x16x32_bf16 v[4:7], v[146:149], v[192:195], v[4:7]
	v_mfma_f32_16x16x32_bf16 v[0:3], v[156:159], v[192:195], v[0:3]
	v_mfma_f32_16x16x32_bf16 v[52:55], v[150:153], v[172:175], v[52:55]
	v_mfma_f32_16x16x32_bf16 v[48:51], v[160:163], v[172:175], v[48:51]
	v_mfma_f32_16x16x32_bf16 v[36:39], v[150:153], v[180:183], v[36:39]
	v_mfma_f32_16x16x32_bf16 v[32:35], v[160:163], v[180:183], v[32:35]
	v_mfma_f32_16x16x32_bf16 v[20:23], v[150:153], v[188:191], v[20:23]
	v_mfma_f32_16x16x32_bf16 v[16:19], v[160:163], v[188:191], v[16:19]
	v_mfma_f32_16x16x32_bf16 v[4:7], v[150:153], v[196:199], v[4:7]
	v_mfma_f32_16x16x32_bf16 v[0:3], v[160:163], v[196:199], v[0:3]
	s_setprio 0
.Lzxo_r1:
	s_barrier
	s_add_i32 s48, 0, 0x18000
	s_add_i32 s49, 0, 0x1c000
	v_add_u32_e32 v142, s48, v165
	v_add_u32_e32 v160, s49, v165
	ds_read_b128 v[130:133], v142
	ds_read_b128 v[134:137], v142 offset:1024
	ds_read_b128 v[138:141], v142 offset:2048
	ds_read_b128 v[142:145], v142 offset:3072
	ds_read_b128 v[146:149], v160
	ds_read_b128 v[150:153], v160 offset:1024
	ds_read_b128 v[156:159], v160 offset:2048
	ds_read_b128 v[160:163], v160 offset:3072
	s_add_u32 s46, s22, 0x20000
	s_addc_u32 s47, s23, 0
	ds_read_b128 v[168:171], v166 offset:32768
	ds_read_b128 v[172:175], v166 offset:33792
	ds_read_b128 v[176:179], v166 offset:34816
	ds_read_b128 v[180:183], v166 offset:35840
	ds_read_b128 v[184:187], v166 offset:36864
	ds_read_b128 v[188:191], v166 offset:37888
	ds_read_b128 v[192:195], v166 offset:38912
	ds_read_b128 v[196:199], v166 offset:39936
	s_mov_b32 m0, s37
	v_lshl_add_u64 v[200:201], s[46:47], 0, v[154:155]
	s_add_u32 s46, s22, 0x30000
	s_addc_u32 s47, s23, 0
	global_load_lds_dwordx4 v[200:201], off
	s_mov_b32 m0, s38
	v_lshl_add_u64 v[200:201], s[46:47], 0, v[154:155]
	global_load_lds_dwordx4 v[200:201], off
	s_waitcnt vmcnt(8)
	s_waitcnt lgkmcnt(0)
	s_barrier
	s_setprio 1
	s_waitcnt lgkmcnt(0)
	v_mfma_f32_16x16x32_bf16 v[126:129], v[130:133], v[168:171], v[126:129]
	v_mfma_f32_16x16x32_bf16 v[122:125], v[138:141], v[168:171], v[122:125]
	v_mfma_f32_16x16x32_bf16 v[108:111], v[130:133], v[176:179], v[108:111]
	v_mfma_f32_16x16x32_bf16 v[104:107], v[138:141], v[176:179], v[104:107]
	v_mfma_f32_16x16x32_bf16 v[92:95], v[130:133], v[184:187], v[92:95]
	v_mfma_f32_16x16x32_bf16 v[88:91], v[138:141], v[184:187], v[88:91]
	v_mfma_f32_16x16x32_bf16 v[76:79], v[130:133], v[192:195], v[76:79]
	v_mfma_f32_16x16x32_bf16 v[72:75], v[138:141], v[192:195], v[72:75]
	v_mfma_f32_16x16x32_bf16 v[126:129], v[134:137], v[172:175], v[126:129]
	v_mfma_f32_16x16x32_bf16 v[122:125], v[142:145], v[172:175], v[122:125]
	v_mfma_f32_16x16x32_bf16 v[108:111], v[134:137], v[180:183], v[108:111]
	v_mfma_f32_16x16x32_bf16 v[104:107], v[142:145], v[180:183], v[104:107]
	v_mfma_f32_16x16x32_bf16 v[92:95], v[134:137], v[188:191], v[92:95]
	v_mfma_f32_16x16x32_bf16 v[88:91], v[142:145], v[188:191], v[88:91]
	v_mfma_f32_16x16x32_bf16 v[76:79], v[134:137], v[196:199], v[76:79]
	v_mfma_f32_16x16x32_bf16 v[72:75], v[142:145], v[196:199], v[72:75]
	s_setprio 0
	s_setprio 1
	v_mfma_f32_16x16x32_bf16 v[118:121], v[146:149], v[168:171], v[118:121]
	v_mfma_f32_16x16x32_bf16 v[114:117], v[156:159], v[168:171], v[114:117]
	v_mfma_f32_16x16x32_bf16 v[100:103], v[146:149], v[176:179], v[100:103]
	v_mfma_f32_16x16x32_bf16 v[96:99], v[156:159], v[176:179], v[96:99]
	v_mfma_f32_16x16x32_bf16 v[84:87], v[146:149], v[184:187], v[84:87]
	v_mfma_f32_16x16x32_bf16 v[80:83], v[156:159], v[184:187], v[80:83]
	v_mfma_f32_16x16x32_bf16 v[68:71], v[146:149], v[192:195], v[68:71]
	v_mfma_f32_16x16x32_bf16 v[64:67], v[156:159], v[192:195], v[64:67]
	v_mfma_f32_16x16x32_bf16 v[118:121], v[150:153], v[172:175], v[118:121]
	v_mfma_f32_16x16x32_bf16 v[114:117], v[160:163], v[172:175], v[114:117]
	v_mfma_f32_16x16x32_bf16 v[100:103], v[150:153], v[180:183], v[100:103]
	v_mfma_f32_16x16x32_bf16 v[96:99], v[160:163], v[180:183], v[96:99]
	v_mfma_f32_16x16x32_bf16 v[84:87], v[150:153], v[188:191], v[84:87]
	v_mfma_f32_16x16x32_bf16 v[80:83], v[160:163], v[188:191], v[80:83]
	v_mfma_f32_16x16x32_bf16 v[68:71], v[150:153], v[196:199], v[68:71]
	v_mfma_f32_16x16x32_bf16 v[64:67], v[160:163], v[196:199], v[64:67]
	s_setprio 0
	s_barrier
; #define PG8_STAGE(bufoff, gbase, voff) do { _Pragma("unroll") for (int _i = 0; _i < 2; ++_i) { const char* gb_ = (const char*)(gbase) + _i * rstep; asm volatile("" : "+s"(gb_));   \
;         __builtin_amdgcn_global_load_lds((const unsigned*)(gb_ + (voff)), (LAS unsigned*)(lds + (bufoff) + ldsw + _i * 8192), 16, 0, 0); } } while (0)
; #define PG8_LDA(dst, b, h) do { _Pragma("unroll") for (int m = 0; m < 4; ++m) _Pragma("unroll") for (int k = 0; k < 2; ++k) dst[m][k] = *(const LAS bf16x8*)(lds + PG8_SA(b, h) + aoff + m * 2048 + k * 1024); } while (0)
; #define PG8_WAIT_V(n) asm volatile("s_waitcnt vmcnt(" #n ")" ::: "memory")
; #define PG8_WAIT_L(n) asm volatile("s_waitcnt lgkmcnt(" #n ")" ::: "memory")
; template <class Epi, class Sched, bool ALIGN_EPI = true, bool SP2 = true, bool I8 = false, bool F8 = false>
; __device__ __forceinline__ void gemm_phase(LAS unsigned char* lds, const int K, const Sched& S, const Epi& E, const int wave) {
;     ...
;         for (int t = 0; t < nt; t += 2) {
;             const bool last = (t == nt - 2);
;             const char* a1 = cA + (size_t)(t + 1) * kstep;
;             const char* a2 = last ? nA : cA + (size_t)(t + 2) * kstep; const char* b2 = last ? nB : cB + (size_t)(t + 2) * kstep;
;             const char* a3 = a2 + kstep; const char* b3 = b2 + kstep;
;             if constexpr (SP2) {
;             PG8_LDB(B0, 0, 0); PG8_LDB(B1, 0, 1); PG8_SCHED; PG8_LDA(At, 0, 0); PG8_STAGE(PG8_SA(1, 1), a1 + hstep, voffA);
;             PG8_WAIT_V(8); PG8_WAIT_L(0); PG8_BAR; PG8_MMA(0, 0, At, B0); PG8_MMA(0, 1, At, B1); PG8_BAR; PG8_SCHED;
;             PG8_LDA(At, 0, 1); PG8_STAGE(PG8_SB(0, 0), b2, voffB); PG8_STAGE(PG8_SB(0, 1), b2 + hstep, voffB); PG8_STAGE(PG8_SA(0, 0), a2, voffA);
;             PG8_WAIT_V(8); PG8_WAIT_L(0); PG8_BAR; PG8_MMA(1, 0, At, B0); PG8_MMA(1, 1, At, B1); PG8_BAR; PG8_SCHED;
;             PG8_LDB(B0, 1, 0); PG8_LDB(B1, 1, 1); PG8_SCHED; PG8_LDA(At, 1, 0); PG8_STAGE(PG8_SA(0, 1), a2 + hstep, voffA);
;             PG8_WAIT_V(8); PG8_WAIT_L(0); PG8_BAR; PG8_MMA(0, 0, At, B0); PG8_MMA(0, 1, At, B1); PG8_BAR; PG8_SCHED;
;             PG8_LDA(At, 1, 1); PG8_STAGE(PG8_SB(1, 0), b3, voffB); PG8_STAGE(PG8_SB(1, 1), b3 + hstep, voffB); PG8_STAGE(PG8_SA(1, 0), a3, voffA);
;             PG8_WAIT_V(8); PG8_WAIT_L(0); PG8_BAR; PG8_MMA(1, 0, At, B0); PG8_MMA(1, 1, At, B1); PG8_BAR; PG8_SCHED;
	s_add_u32 s46, s26, 0x80
	s_addc_u32 s47, s27, 0
	ds_read_b128 v[168:171], v166 offset:49152
	ds_read_b128 v[172:175], v166 offset:50176
	ds_read_b128 v[176:179], v166 offset:51200
	ds_read_b128 v[180:183], v166 offset:52224
	ds_read_b128 v[184:187], v166 offset:53248
	ds_read_b128 v[188:191], v166 offset:54272
	ds_read_b128 v[192:195], v166 offset:55296
	ds_read_b128 v[196:199], v166 offset:56320
	s_add_i32 s48, s48, s34
	v_lshl_add_u64 v[200:201], s[46:47], 0, v[112:113]
	s_add_u32 s46, s26, 0x10080
	s_mov_b32 m0, s48
	s_addc_u32 s47, s27, 0
	global_load_lds_dwordx4 v[200:201], off
	s_add_i32 m0, s48, 0x2000
	v_lshl_add_u64 v[200:201], s[46:47], 0, v[112:113]
	s_add_u32 s46, s26, 0x20080
	s_addc_u32 s47, s27, 0
	global_load_lds_dwordx4 v[200:201], off
	s_nop 0
	v_lshl_add_u64 v[200:201], s[46:47], 0, v[112:113]
	s_add_i32 s46, s49, s34
	s_mov_b32 m0, s46
	s_add_u32 s26, s26, 0x30080
	global_load_lds_dwordx4 v[200:201], off
	s_addc_u32 s27, s27, 0
	s_add_i32 m0, s46, 0x2000
	s_add_u32 s22, s22, 0x10080
	v_lshl_add_u64 v[200:201], s[26:27], 0, v[112:113]
	global_load_lds_dwordx4 v[200:201], off
	s_mov_b32 m0, s41
	v_lshl_add_u64 v[200:201], s[24:25], 0, v[154:155]
	s_addc_u32 s23, s23, 0
	global_load_lds_dwordx4 v[200:201], off
	s_mov_b32 m0, s42
	v_lshl_add_u64 v[200:201], s[22:23], 0, v[154:155]
	global_load_lds_dwordx4 v[200:201], off
	s_waitcnt vmcnt(8)
	s_waitcnt lgkmcnt(0)
	s_barrier
	s_setprio 1
	s_waitcnt lgkmcnt(0)
	v_mfma_f32_16x16x32_bf16 v[60:63], v[130:133], v[168:171], v[60:63]
	v_mfma_f32_16x16x32_bf16 v[56:59], v[138:141], v[168:171], v[56:59]
	v_mfma_f32_16x16x32_bf16 v[44:47], v[130:133], v[176:179], v[44:47]
	v_mfma_f32_16x16x32_bf16 v[40:43], v[138:141], v[176:179], v[40:43]
	v_mfma_f32_16x16x32_bf16 v[28:31], v[130:133], v[184:187], v[28:31]
	v_mfma_f32_16x16x32_bf16 v[24:27], v[138:141], v[184:187], v[24:27]
	v_mfma_f32_16x16x32_bf16 v[12:15], v[130:133], v[192:195], v[12:15]
	v_mfma_f32_16x16x32_bf16 v[8:11], v[138:141], v[192:195], v[8:11]
	v_mfma_f32_16x16x32_bf16 v[60:63], v[134:137], v[172:175], v[60:63]
	v_mfma_f32_16x16x32_bf16 v[56:59], v[142:145], v[172:175], v[56:59]
	v_mfma_f32_16x16x32_bf16 v[44:47], v[134:137], v[180:183], v[44:47]
	v_mfma_f32_16x16x32_bf16 v[40:43], v[142:145], v[180:183], v[40:43]
	v_mfma_f32_16x16x32_bf16 v[28:31], v[134:137], v[188:191], v[28:31]
	v_mfma_f32_16x16x32_bf16 v[24:27], v[142:145], v[188:191], v[24:27]
	v_mfma_f32_16x16x32_bf16 v[12:15], v[134:137], v[196:199], v[12:15]
	v_mfma_f32_16x16x32_bf16 v[8:11], v[142:145], v[196:199], v[8:11]
	s_setprio 0
	s_setprio 1
	v_mfma_f32_16x16x32_bf16 v[52:55], v[146:149], v[168:171], v[52:55]
	v_mfma_f32_16x16x32_bf16 v[48:51], v[156:159], v[168:171], v[48:51]
	v_mfma_f32_16x16x32_bf16 v[36:39], v[146:149], v[176:179], v[36:39]
	v_mfma_f32_16x16x32_bf16 v[32:35], v[156:159], v[176:179], v[32:35]
	v_mfma_f32_16x16x32_bf16 v[20:23], v[146:149], v[184:187], v[20:23]
	v_mfma_f32_16x16x32_bf16 v[16:19], v[156:159], v[184:187], v[16:19]
	v_mfma_f32_16x16x32_bf16 v[4:7], v[146:149], v[192:195], v[4:7]
	v_mfma_f32_16x16x32_bf16 v[0:3], v[156:159], v[192:195], v[0:3]
	v_mfma_f32_16x16x32_bf16 v[52:55], v[150:153], v[172:175], v[52:55]
	v_mfma_f32_16x16x32_bf16 v[48:51], v[160:163], v[172:175], v[48:51]
	v_mfma_f32_16x16x32_bf16 v[36:39], v[150:153], v[180:183], v[36:39]
	v_mfma_f32_16x16x32_bf16 v[32:35], v[160:163], v[180:183], v[32:35]
	v_mfma_f32_16x16x32_bf16 v[20:23], v[150:153], v[188:191], v[20:23]
	v_mfma_f32_16x16x32_bf16 v[16:19], v[160:163], v[188:191], v[16:19]
	v_mfma_f32_16x16x32_bf16 v[4:7], v[150:153], v[196:199], v[4:7]
	v_mfma_f32_16x16x32_bf16 v[0:3], v[160:163], v[196:199], v[0:3]
	s_setprio 0
	s_barrier
	s_add_i32 s19, s19, 2
	s_add_u32 s11, s11, 0x100
	s_addc_u32 s13, s13, 0
	s_add_u32 s20, s20, 0x100
	s_addc_u32 s21, s21, 0
	s_cmp_gt_u32 s19, 5
	s_cbranch_scc0 .LBB0_1300
	s_and_b64 vcc, exec, s[2:3]
	s_cbranch_vccz .LBB0_1303
	s_barrier

; #define PG8_STAGE(bufoff, gbase, voff) do { _Pragma("unroll") for (int _i = 0; _i < 2; ++_i) { const char* gb_ = (const char*)(gbase) + _i * rstep; asm volatile("" : "+s"(gb_));   \
;         __builtin_amdgcn_global_load_lds((const unsigned*)(gb_ + (voff)), (LAS unsigned*)(lds + (bufoff) + ldsw + _i * 8192), 16, 0, 0); } } while (0)
; #define PG8_LDA(dst, b, h) do { _Pragma("unroll") for (int m = 0; m < 4; ++m) _Pragma("unroll") for (int k = 0; k < 2; ++k) dst[m][k] = *(const LAS bf16x8*)(lds + PG8_SA(b, h) + aoff + m * 2048 + k * 1024); } while (0)
; #define PG8_WAIT_V(n) asm volatile("s_waitcnt vmcnt(" #n ")" ::: "memory")
; #define PG8_WAIT_L(n) asm volatile("s_waitcnt lgkmcnt(" #n ")" ::: "memory")
; #define PG8_BAR __builtin_amdgcn_s_barrier()
; #define PG8_SCHED __builtin_amdgcn_sched_barrier(0)
; __device__ __forceinline__ void mma8(f32x4& c, const bf16x8& a0, const bf16x8& a1, const bf16x8& b0, const bf16x8& b1) {
;     typedef int i32x4_ __attribute__((ext_vector_type(4)));
;     const i32x8 A = __builtin_shufflevector(__builtin_bit_cast(i32x4_, a0), __builtin_bit_cast(i32x4_, a1), 0, 1, 2, 3, 4, 5, 6, 7), Bv = __builtin_shufflevector(__builtin_bit_cast(i32x4_, b0), __builtin_bit_cast(i32x4_, b1), 0, 1, 2, 3, 4, 5, 6, 7);
;     c = __builtin_amdgcn_mfma_scale_f32_16x16x128_f8f6f4(A, Bv, c, 0, 0, 0, 0, 0, 0);
; }
; template <class Epi, class Sched, bool ALIGN_EPI = true, bool SP2 = true, bool I8 = false, bool F8 = false>
; __device__ __forceinline__ void gemm_phase(LAS unsigned char* lds, const int K, const Sched& S, const Epi& E, const int wave) {
;     ...
;             PG8_WAIT_V(8); PG8_WAIT_L(0); PG8_BAR; PG8_MMA(0, 0, At, B0); PG8_MMA(0, 1, At, B1); PG8_BAR; PG8_SCHED;
;             PG8_LDA(At, 0, 1); PG8_STAGE(PG8_SB(0, 0), b2, voffB); PG8_STAGE(PG8_SB(0, 1), b2 + hstep, voffB); PG8_STAGE(PG8_SA(0, 0), a2, voffA);
;             PG8_WAIT_V(8); PG8_WAIT_L(0); PG8_BAR; PG8_MMA(1, 0, At, B0); PG8_MMA(1, 1, At, B1); PG8_BAR; PG8_SCHED;
.Lztd_s0:
	v_mfma_f32_16x16x128_f8f6f4 v[126:129], v[140:147], v[174:181], 0
	v_mfma_f32_16x16x128_f8f6f4 v[122:125], v[148:155], v[174:181], 0
	v_mfma_f32_16x16x128_f8f6f4 v[108:111], v[140:147], v[182:189], 0
	v_mfma_f32_16x16x128_f8f6f4 v[104:107], v[148:155], v[182:189], 0
	v_mfma_f32_16x16x128_f8f6f4 v[92:95], v[140:147], v[190:197], 0
	v_mfma_f32_16x16x128_f8f6f4 v[88:91], v[148:155], v[190:197], 0
	v_mfma_f32_16x16x128_f8f6f4 v[76:79], v[140:147], v[198:205], 0
	v_mfma_f32_16x16x128_f8f6f4 v[72:75], v[148:155], v[198:205], 0
	s_setprio 0
	s_setprio 1
	v_mfma_f32_16x16x128_f8f6f4 v[118:121], v[156:163], v[174:181], 0
	v_mfma_f32_16x16x128_f8f6f4 v[114:117], v[166:173], v[174:181], 0
	v_mfma_f32_16x16x128_f8f6f4 v[100:103], v[156:163], v[182:189], 0
	v_mfma_f32_16x16x128_f8f6f4 v[96:99], v[166:173], v[182:189], 0
	v_mfma_f32_16x16x128_f8f6f4 v[84:87], v[156:163], v[190:197], 0
	v_mfma_f32_16x16x128_f8f6f4 v[80:83], v[166:173], v[190:197], 0
	v_mfma_f32_16x16x128_f8f6f4 v[68:71], v[156:163], v[198:205], 0
	v_mfma_f32_16x16x128_f8f6f4 v[64:67], v[166:173], v[198:205], 0
	s_setprio 0
	s_branch .Lztd_r0
.Lztd_s1:
	v_mfma_f32_16x16x128_f8f6f4 v[60:63], v[140:147], v[174:181], 0
	v_mfma_f32_16x16x128_f8f6f4 v[56:59], v[148:155], v[174:181], 0
	v_mfma_f32_16x16x128_f8f6f4 v[48:51], v[140:147], v[182:189], 0
	v_mfma_f32_16x16x128_f8f6f4 v[40:43], v[148:155], v[182:189], 0
	v_mfma_f32_16x16x128_f8f6f4 v[32:35], v[140:147], v[190:197], 0
	v_mfma_f32_16x16x128_f8f6f4 v[24:27], v[148:155], v[190:197], 0
	v_mfma_f32_16x16x128_f8f6f4 v[16:19], v[140:147], v[198:205], 0
	v_mfma_f32_16x16x128_f8f6f4 v[8:11], v[148:155], v[198:205], 0
	s_setprio 0
	s_setprio 1
	v_mfma_f32_16x16x128_f8f6f4 v[52:55], v[156:163], v[174:181], 0
	v_mfma_f32_16x16x128_f8f6f4 v[44:47], v[166:173], v[174:181], 0
	v_mfma_f32_16x16x128_f8f6f4 v[36:39], v[156:163], v[182:189], 0
	v_mfma_f32_16x16x128_f8f6f4 v[28:31], v[166:173], v[182:189], 0
	v_mfma_f32_16x16x128_f8f6f4 v[20:23], v[156:163], v[190:197], 0
	v_mfma_f32_16x16x128_f8f6f4 v[12:15], v[166:173], v[190:197], 0
	v_mfma_f32_16x16x128_f8f6f4 v[4:7], v[156:163], v[198:205], 0
	v_mfma_f32_16x16x128_f8f6f4 v[0:3], v[166:173], v[198:205], 0
	s_setprio 0
	s_branch .Lztd_r1

; #define PG8_STAGE(bufoff, gbase, voff) do { _Pragma("unroll") for (int _i = 0; _i < 2; ++_i) { const char* gb_ = (const char*)(gbase) + _i * rstep; asm volatile("" : "+s"(gb_));   \
;         __builtin_amdgcn_global_load_lds((const unsigned*)(gb_ + (voff)), (LAS unsigned*)(lds + (bufoff) + ldsw + _i * 8192), 16, 0, 0); } } while (0)
; #define PG8_LDA(dst, b, h) do { _Pragma("unroll") for (int m = 0; m < 4; ++m) _Pragma("unroll") for (int k = 0; k < 2; ++k) dst[m][k] = *(const LAS bf16x8*)(lds + PG8_SA(b, h) + aoff + m * 2048 + k * 1024); } while (0)
; #define PG8_LDB(dst, b, h) do { _Pragma("unroll") for (int n = 0; n < 2; ++n) _Pragma("unroll") for (int k = 0; k < 2; ++k) dst[n][k] = *(const LAS bf16x8*)(lds + PG8_SB(b, h) + boff + n * 2048 + k * 1024); } while (0)
; #define PG8_WAIT_V(n) asm volatile("s_waitcnt vmcnt(" #n ")" ::: "memory")
; #define PG8_WAIT_L(n) asm volatile("s_waitcnt lgkmcnt(" #n ")" ::: "memory")
; #define PG8_BAR __builtin_amdgcn_s_barrier()
; template <class Epi, class Sched, bool ALIGN_EPI = true, bool SP2 = true, bool I8 = false, bool F8 = false>
; __device__ __forceinline__ void gemm_phase(LAS unsigned char* lds, const int K, const Sched& S, const Epi& E, const int wave) {
;     ...
;         for (int t = 0; t < nt; t += 2) {
;             const bool last = (t == nt - 2);
;             const char* a1 = cA + (size_t)(t + 1) * kstep;
;             const char* a2 = last ? nA : cA + (size_t)(t + 2) * kstep; const char* b2 = last ? nB : cB + (size_t)(t + 2) * kstep;
;             const char* a3 = a2 + kstep; const char* b3 = b2 + kstep;
;             if constexpr (SP2) {
;             PG8_LDB(B0, 0, 0); PG8_LDB(B1, 0, 1); PG8_SCHED; PG8_LDA(At, 0, 0); PG8_STAGE(PG8_SA(1, 1), a1 + hstep, voffA);
;             PG8_WAIT_V(8); PG8_WAIT_L(0); PG8_BAR; PG8_MMA(0, 0, At, B0); PG8_MMA(0, 1, At, B1); PG8_BAR; PG8_SCHED;
;             PG8_LDA(At, 0, 1); PG8_STAGE(PG8_SB(0, 0), b2, voffB); PG8_STAGE(PG8_SB(0, 1), b2 + hstep, voffB); PG8_STAGE(PG8_SA(0, 0), a2, voffA);
;             PG8_WAIT_V(8); PG8_WAIT_L(0); PG8_BAR; PG8_MMA(1, 0, At, B0); PG8_MMA(1, 1, At, B1); PG8_BAR; PG8_SCHED;
;     ...
;         for (int a = 0; a < 2; ++a)
; #pragma unroll
;             for (int b = 0; b < 2; ++b)
; #pragma unroll
;                 for (int m = 0; m < 4; ++m)
; #pragma unroll
;                     for (int n = 0; n < 2; ++n) acc[a][b][m][n] = (acc_t){0, 0, 0, 0};
.LBB0_1561:
	s_add_u32 s11, s12, 0x100
	s_addc_u32 s41, s13, 0
	s_add_u32 s12, s14, 0xa8080
	s_addc_u32 s13, s15, 0
	s_mov_b32 s58, -2
.LBB0_1562:
	s_add_u32 s14, s12, 0xfff58080
	s_addc_u32 s15, s13, -1
	s_cmp_eq_u32 s58, 24
	s_cselect_b32 s14, s6, s14
	s_cselect_b32 s15, s7, s15
	s_cselect_b32 s18, s8, s11
	s_cselect_b32 s19, s9, s41
	s_add_u32 s16, s14, 0x80
	s_addc_u32 s17, s15, 0
	s_add_i32 s59, 0, 0x10000
	v_add_u32_e32 v132, s59, v133
	s_add_i32 s64, 0, 0x14000
	ds_read_b128 v[140:143], v132
	ds_read_b128 v[144:147], v132 offset:1024
	ds_read_b128 v[148:151], v132 offset:2048
	ds_read_b128 v[152:155], v132 offset:3072
	v_add_u32_e32 v132, s64, v133
	ds_read_b128 v[156:159], v132
	ds_read_b128 v[160:163], v132 offset:1024
	ds_read_b128 v[166:169], v132 offset:2048
	ds_read_b128 v[170:173], v132 offset:3072
	s_add_u32 s62, s12, 0xfffc8000
	s_addc_u32 s63, s13, -1
	ds_read_b128 v[174:177], v138
	ds_read_b128 v[178:181], v138 offset:1024
	ds_read_b128 v[182:185], v138 offset:2048
	ds_read_b128 v[186:189], v138 offset:3072
	ds_read_b128 v[190:193], v138 offset:4096
	ds_read_b128 v[194:197], v138 offset:5120
	ds_read_b128 v[198:201], v138 offset:6144
	ds_read_b128 v[202:205], v138 offset:7168
	s_add_i32 m0, s21, 0xc000
	v_lshl_add_u64 v[134:135], s[62:63], 0, v[130:131]
	s_mov_b64 s[62:63], s[12:13]
	global_load_lds_dwordx4 v[134:135], off
	s_add_i32 m0, s21, 0xe000
	v_lshl_add_u64 v[134:135], s[62:63], 0, v[130:131]
	global_load_lds_dwordx4 v[134:135], off
	s_waitcnt vmcnt(8)
	s_waitcnt lgkmcnt(0)
	s_barrier
	s_setprio 1
	s_waitcnt lgkmcnt(0)
	s_cmp_eq_u32 s58, -2
	s_cbranch_scc1 .Lztd_s0
	v_mfma_f32_16x16x128_f8f6f4 v[126:129], v[140:147], v[174:181], v[126:129]
	v_mfma_f32_16x16x128_f8f6f4 v[122:125], v[148:155], v[174:181], v[122:125]
	v_mfma_f32_16x16x128_f8f6f4 v[108:111], v[140:147], v[182:189], v[108:111]
	v_mfma_f32_16x16x128_f8f6f4 v[104:107], v[148:155], v[182:189], v[104:107]
	v_mfma_f32_16x16x128_f8f6f4 v[92:95], v[140:147], v[190:197], v[92:95]
	v_mfma_f32_16x16x128_f8f6f4 v[88:91], v[148:155], v[190:197], v[88:91]
	v_mfma_f32_16x16x128_f8f6f4 v[76:79], v[140:147], v[198:205], v[76:79]
	v_mfma_f32_16x16x128_f8f6f4 v[72:75], v[148:155], v[198:205], v[72:75]
	s_setprio 0
	s_setprio 1
	v_mfma_f32_16x16x128_f8f6f4 v[118:121], v[156:163], v[174:181], v[118:121]
	v_mfma_f32_16x16x128_f8f6f4 v[114:117], v[166:173], v[174:181], v[114:117]
	v_mfma_f32_16x16x128_f8f6f4 v[100:103], v[156:163], v[182:189], v[100:103]
	v_mfma_f32_16x16x128_f8f6f4 v[96:99], v[166:173], v[182:189], v[96:99]
	v_mfma_f32_16x16x128_f8f6f4 v[84:87], v[156:163], v[190:197], v[84:87]
	v_mfma_f32_16x16x128_f8f6f4 v[80:83], v[166:173], v[190:197], v[80:83]
	v_mfma_f32_16x16x128_f8f6f4 v[68:71], v[156:163], v[198:205], v[68:71]
	v_mfma_f32_16x16x128_f8f6f4 v[64:67], v[166:173], v[198:205], v[64:67]
	s_setprio 0
.Lztd_r0:
	s_barrier
	s_mov_b64 s[62:63], s[18:19]
	ds_read_b128 v[174:177], v138 offset:16384
	ds_read_b128 v[178:181], v138 offset:17408
	ds_read_b128 v[182:185], v138 offset:18432
	ds_read_b128 v[186:189], v138 offset:19456
	ds_read_b128 v[190:193], v138 offset:20480
	ds_read_b128 v[194:197], v138 offset:21504
	ds_read_b128 v[198:201], v138 offset:22528
	ds_read_b128 v[202:205], v138 offset:23552
	s_add_i32 s59, s59, s20
	v_lshl_add_u64 v[134:135], s[62:63], 0, v[112:113]
	s_add_u32 s62, s18, 0x38000
	s_mov_b32 m0, s59
	s_addc_u32 s63, s19, 0
	global_load_lds_dwordx4 v[134:135], off
	s_add_i32 m0, s59, 0x2000
	v_lshl_add_u64 v[134:135], s[62:63], 0, v[112:113]
	s_add_u32 s62, s18, 0x70000
	s_addc_u32 s63, s19, 0
	global_load_lds_dwordx4 v[134:135], off
	s_add_i32 s59, s64, s20
	v_lshl_add_u64 v[134:135], s[62:63], 0, v[112:113]
	s_add_u32 s62, s18, 0xa8000
	s_mov_b32 m0, s59
	s_addc_u32 s63, s19, 0
	global_load_lds_dwordx4 v[134:135], off
	s_add_i32 m0, s59, 0x2000
	v_lshl_add_u64 v[134:135], s[62:63], 0, v[112:113]
	s_mov_b64 s[62:63], s[14:15]
	global_load_lds_dwordx4 v[134:135], off
	s_mov_b32 m0, s21
	v_lshl_add_u64 v[134:135], s[62:63], 0, v[130:131]
	s_add_u32 s62, s14, 0x38000
	s_addc_u32 s63, s15, 0
	global_load_lds_dwordx4 v[134:135], off
	s_mov_b32 m0, s22
	v_lshl_add_u64 v[134:135], s[62:63], 0, v[130:131]
	global_load_lds_dwordx4 v[134:135], off
	s_waitcnt vmcnt(8)
	s_waitcnt lgkmcnt(0)
	s_barrier
	s_setprio 1
	s_waitcnt lgkmcnt(0)
	s_cmp_eq_u32 s58, -2
	s_cbranch_scc1 .Lztd_s1
	v_mfma_f32_16x16x128_f8f6f4 v[60:63], v[140:147], v[174:181], v[60:63]
	v_mfma_f32_16x16x128_f8f6f4 v[56:59], v[148:155], v[174:181], v[56:59]
	v_mfma_f32_16x16x128_f8f6f4 v[48:51], v[140:147], v[182:189], v[48:51]
	v_mfma_f32_16x16x128_f8f6f4 v[40:43], v[148:155], v[182:189], v[40:43]
	v_mfma_f32_16x16x128_f8f6f4 v[32:35], v[140:147], v[190:197], v[32:35]
	v_mfma_f32_16x16x128_f8f6f4 v[24:27], v[148:155], v[190:197], v[24:27]
	v_mfma_f32_16x16x128_f8f6f4 v[16:19], v[140:147], v[198:205], v[16:19]
	v_mfma_f32_16x16x128_f8f6f4 v[8:11], v[148:155], v[198:205], v[8:11]
	s_setprio 0
	s_setprio 1
	v_mfma_f32_16x16x128_f8f6f4 v[52:55], v[156:163], v[174:181], v[52:55]
	v_mfma_f32_16x16x128_f8f6f4 v[44:47], v[166:173], v[174:181], v[44:47]
	v_mfma_f32_16x16x128_f8f6f4 v[36:39], v[156:163], v[182:189], v[36:39]
	v_mfma_f32_16x16x128_f8f6f4 v[28:31], v[166:173], v[182:189], v[28:31]
	v_mfma_f32_16x16x128_f8f6f4 v[20:23], v[156:163], v[190:197], v[20:23]
	v_mfma_f32_16x16x128_f8f6f4 v[12:15], v[166:173], v[190:197], v[12:15]
	v_mfma_f32_16x16x128_f8f6f4 v[4:7], v[156:163], v[198:205], v[4:7]
	v_mfma_f32_16x16x128_f8f6f4 v[0:3], v[166:173], v[198:205], v[0:3]
	s_setprio 0
; #define PG8_STAGE(bufoff, gbase, voff) do { _Pragma("unroll") for (int _i = 0; _i < 2; ++_i) { const char* gb_ = (const char*)(gbase) + _i * rstep; asm volatile("" : "+s"(gb_));   \
;         __builtin_amdgcn_global_load_lds((const unsigned*)(gb_ + (voff)), (LAS unsigned*)(lds + (bufoff) + ldsw + _i * 8192), 16, 0, 0); } } while (0)
; #define PG8_LDA(dst, b, h) do { _Pragma("unroll") for (int m = 0; m < 4; ++m) _Pragma("unroll") for (int k = 0; k < 2; ++k) dst[m][k] = *(const LAS bf16x8*)(lds + PG8_SA(b, h) + aoff + m * 2048 + k * 1024); } while (0)
; #define PG8_LDB(dst, b, h) do { _Pragma("unroll") for (int n = 0; n < 2; ++n) _Pragma("unroll") for (int k = 0; k < 2; ++k) dst[n][k] = *(const LAS bf16x8*)(lds + PG8_SB(b, h) + boff + n * 2048 + k * 1024); } while (0)
; #define PG8_WAIT_V(n) asm volatile("s_waitcnt vmcnt(" #n ")" ::: "memory")
; #define PG8_WAIT_L(n) asm volatile("s_waitcnt lgkmcnt(" #n ")" ::: "memory")
; #define PG8_BAR __builtin_amdgcn_s_barrier()
; #define PG8_SCHED __builtin_amdgcn_sched_barrier(0)
; template <class Epi, class Sched, bool ALIGN_EPI = true, bool SP2 = true, bool I8 = false, bool F8 = false>
; __device__ __forceinline__ void gemm_phase(LAS unsigned char* lds, const int K, const Sched& S, const Epi& E, const int wave) {
;     ...
;             PG8_LDB(B0, 1, 0); PG8_LDB(B1, 1, 1); PG8_SCHED; PG8_LDA(At, 1, 0); PG8_STAGE(PG8_SA(0, 1), a2 + hstep, voffA);
;             PG8_WAIT_V(8); PG8_WAIT_L(0); PG8_BAR; PG8_MMA(0, 0, At, B0); PG8_MMA(0, 1, At, B1); PG8_BAR; PG8_SCHED;
;             PG8_LDA(At, 1, 1); PG8_STAGE(PG8_SB(1, 0), b3, voffB); PG8_STAGE(PG8_SB(1, 1), b3 + hstep, voffB); PG8_STAGE(PG8_SA(1, 0), a3, voffA);
;             PG8_WAIT_V(8); PG8_WAIT_L(0); PG8_BAR; PG8_MMA(1, 0, At, B0); PG8_MMA(1, 1, At, B1); PG8_BAR; PG8_SCHED;
.Lztd_r1:
	s_barrier
	s_add_i32 s59, 0, 0x18000
	v_add_u32_e32 v132, s59, v133
	s_add_i32 s64, 0, 0x1c000
	ds_read_b128 v[140:143], v132
	ds_read_b128 v[144:147], v132 offset:1024
	ds_read_b128 v[148:151], v132 offset:2048
	ds_read_b128 v[152:155], v132 offset:3072
	v_add_u32_e32 v132, s64, v133
	ds_read_b128 v[156:159], v132
	ds_read_b128 v[160:163], v132 offset:1024
	ds_read_b128 v[166:169], v132 offset:2048
	ds_read_b128 v[170:173], v132 offset:3072
	s_add_u32 s62, s14, 0x70000
	s_addc_u32 s63, s15, 0
	ds_read_b128 v[174:177], v138 offset:32768
	ds_read_b128 v[178:181], v138 offset:33792
	ds_read_b128 v[182:185], v138 offset:34816
	ds_read_b128 v[186:189], v138 offset:35840
	ds_read_b128 v[190:193], v138 offset:36864
	ds_read_b128 v[194:197], v138 offset:37888
	ds_read_b128 v[198:201], v138 offset:38912
	ds_read_b128 v[202:205], v138 offset:39936
	s_mov_b32 m0, s23
	v_lshl_add_u64 v[134:135], s[62:63], 0, v[130:131]
	s_add_u32 s62, s14, 0xa8000
	s_addc_u32 s63, s15, 0
	global_load_lds_dwordx4 v[134:135], off
	s_mov_b32 m0, s24
	v_lshl_add_u64 v[134:135], s[62:63], 0, v[130:131]
	global_load_lds_dwordx4 v[134:135], off
	s_waitcnt vmcnt(8)
	s_waitcnt lgkmcnt(0)
	s_barrier
	s_setprio 1
	s_waitcnt lgkmcnt(0)
	v_mfma_f32_16x16x128_f8f6f4 v[126:129], v[140:147], v[174:181], v[126:129]
	v_mfma_f32_16x16x128_f8f6f4 v[122:125], v[148:155], v[174:181], v[122:125]
	v_mfma_f32_16x16x128_f8f6f4 v[108:111], v[140:147], v[182:189], v[108:111]
	v_mfma_f32_16x16x128_f8f6f4 v[104:107], v[148:155], v[182:189], v[104:107]
	v_mfma_f32_16x16x128_f8f6f4 v[92:95], v[140:147], v[190:197], v[92:95]
	v_mfma_f32_16x16x128_f8f6f4 v[88:91], v[148:155], v[190:197], v[88:91]
	v_mfma_f32_16x16x128_f8f6f4 v[76:79], v[140:147], v[198:205], v[76:79]
	v_mfma_f32_16x16x128_f8f6f4 v[72:75], v[148:155], v[198:205], v[72:75]
	s_setprio 0
	s_setprio 1
	v_mfma_f32_16x16x128_f8f6f4 v[118:121], v[156:163], v[174:181], v[118:121]
	v_mfma_f32_16x16x128_f8f6f4 v[114:117], v[166:173], v[174:181], v[114:117]
	v_mfma_f32_16x16x128_f8f6f4 v[100:103], v[156:163], v[182:189], v[100:103]
	v_mfma_f32_16x16x128_f8f6f4 v[96:99], v[166:173], v[182:189], v[96:99]
	v_mfma_f32_16x16x128_f8f6f4 v[84:87], v[156:163], v[190:197], v[84:87]
	v_mfma_f32_16x16x128_f8f6f4 v[80:83], v[166:173], v[190:197], v[80:83]
	v_mfma_f32_16x16x128_f8f6f4 v[68:71], v[156:163], v[198:205], v[68:71]
	v_mfma_f32_16x16x128_f8f6f4 v[64:67], v[166:173], v[198:205], v[64:67]
	s_setprio 0
	s_barrier
	s_add_u32 s62, s18, 0x80
	s_addc_u32 s63, s19, 0
	ds_read_b128 v[174:177], v138 offset:49152
	ds_read_b128 v[178:181], v138 offset:50176
	ds_read_b128 v[182:185], v138 offset:51200
	ds_read_b128 v[186:189], v138 offset:52224
	ds_read_b128 v[190:193], v138 offset:53248
	ds_read_b128 v[194:197], v138 offset:54272
	ds_read_b128 v[198:201], v138 offset:55296
	ds_read_b128 v[202:205], v138 offset:56320
	s_add_i32 s59, s59, s20
	v_lshl_add_u64 v[134:135], s[62:63], 0, v[112:113]
	s_add_u32 s62, s18, 0x38080
	s_mov_b32 m0, s59
	s_addc_u32 s63, s19, 0
	global_load_lds_dwordx4 v[134:135], off
	s_add_i32 m0, s59, 0x2000
	v_lshl_add_u64 v[134:135], s[62:63], 0, v[112:113]
	s_add_u32 s62, s18, 0x70080
	s_addc_u32 s63, s19, 0
	s_add_i32 s59, s64, s20
	global_load_lds_dwordx4 v[134:135], off
	s_mov_b32 m0, s59
	v_lshl_add_u64 v[134:135], s[62:63], 0, v[112:113]
	s_add_u32 s18, s18, 0xa8080
	global_load_lds_dwordx4 v[134:135], off
	s_addc_u32 s19, s19, 0
	s_add_i32 m0, s59, 0x2000
	s_add_u32 s14, s14, 0x38080
	v_lshl_add_u64 v[134:135], s[18:19], 0, v[112:113]
	global_load_lds_dwordx4 v[134:135], off
	s_mov_b32 m0, s26
	v_lshl_add_u64 v[134:135], s[16:17], 0, v[130:131]
	s_addc_u32 s15, s15, 0
	global_load_lds_dwordx4 v[134:135], off
	s_mov_b32 m0, s27
	v_lshl_add_u64 v[134:135], s[14:15], 0, v[130:131]
	global_load_lds_dwordx4 v[134:135], off
	s_waitcnt vmcnt(8)
	s_waitcnt lgkmcnt(0)
	s_barrier
	s_setprio 1
	s_waitcnt lgkmcnt(0)
	v_mfma_f32_16x16x128_f8f6f4 v[60:63], v[140:147], v[174:181], v[60:63]
	v_mfma_f32_16x16x128_f8f6f4 v[56:59], v[148:155], v[174:181], v[56:59]
	v_mfma_f32_16x16x128_f8f6f4 v[48:51], v[140:147], v[182:189], v[48:51]
	v_mfma_f32_16x16x128_f8f6f4 v[40:43], v[148:155], v[182:189], v[40:43]
	v_mfma_f32_16x16x128_f8f6f4 v[32:35], v[140:147], v[190:197], v[32:35]
	v_mfma_f32_16x16x128_f8f6f4 v[24:27], v[148:155], v[190:197], v[24:27]
	v_mfma_f32_16x16x128_f8f6f4 v[16:19], v[140:147], v[198:205], v[16:19]
	v_mfma_f32_16x16x128_f8f6f4 v[8:11], v[148:155], v[198:205], v[8:11]
	s_setprio 0
	s_setprio 1
	v_mfma_f32_16x16x128_f8f6f4 v[52:55], v[156:163], v[174:181], v[52:55]
	v_mfma_f32_16x16x128_f8f6f4 v[44:47], v[166:173], v[174:181], v[44:47]
	v_mfma_f32_16x16x128_f8f6f4 v[36:39], v[156:163], v[182:189], v[36:39]
	v_mfma_f32_16x16x128_f8f6f4 v[28:31], v[166:173], v[182:189], v[28:31]
	v_mfma_f32_16x16x128_f8f6f4 v[20:23], v[156:163], v[190:197], v[20:23]
	v_mfma_f32_16x16x128_f8f6f4 v[12:15], v[166:173], v[190:197], v[12:15]
	v_mfma_f32_16x16x128_f8f6f4 v[4:7], v[156:163], v[198:205], v[4:7]
	v_mfma_f32_16x16x128_f8f6f4 v[0:3], v[166:173], v[198:205], v[0:3]
	s_setprio 0
	s_barrier
	s_add_i32 s58, s58, 2
	s_add_u32 s11, s11, 0x100
	s_addc_u32 s41, s41, 0
	s_add_u32 s12, s12, 0x100
	s_addc_u32 s13, s13, 0
	s_cmp_gt_u32 s58, 25
	s_cbranch_scc0 .LBB0_1562
	s_and_b64 vcc, exec, s[4:5]
	s_cbranch_vccz .LBB0_1565
	s_barrier

; #define PG8_STAGE(bufoff, gbase, voff) do { _Pragma("unroll") for (int _i = 0; _i < 2; ++_i) { const char* gb_ = (const char*)(gbase) + _i * rstep; asm volatile("" : "+s"(gb_));   \
;         __builtin_amdgcn_global_load_lds((const unsigned*)(gb_ + (voff)), (LAS unsigned*)(lds + (bufoff) + ldsw + _i * 8192), 16, 0, 0); } } while (0)
; #define PG8_LDA(dst, b, h) do { _Pragma("unroll") for (int m = 0; m < 4; ++m) _Pragma("unroll") for (int k = 0; k < 2; ++k) dst[m][k] = *(const LAS bf16x8*)(lds + PG8_SA(b, h) + aoff + m * 2048 + k * 1024); } while (0)
; #define PG8_LDB(dst, b, h) do { _Pragma("unroll") for (int n = 0; n < 2; ++n) _Pragma("unroll") for (int k = 0; k < 2; ++k) dst[n][k] = *(const LAS bf16x8*)(lds + PG8_SB(b, h) + boff + n * 2048 + k * 1024); } while (0)
; #define PG8_WAIT_V(n) asm volatile("s_waitcnt vmcnt(" #n ")" ::: "memory")
; #define PG8_WAIT_L(n) asm volatile("s_waitcnt lgkmcnt(" #n ")" ::: "memory")
; #define PG8_BAR __builtin_amdgcn_s_barrier()
; template <class Epi, class Sched, bool ALIGN_EPI = true, bool SP2 = true, bool I8 = false, bool F8 = false>
; __device__ __forceinline__ void gemm_phase(LAS unsigned char* lds, const int K, const Sched& S, const Epi& E, const int wave) {
;     ...
;         for (int t = 0; t < nt; t += 2) {
;             const bool last = (t == nt - 2);
;             const char* a1 = cA + (size_t)(t + 1) * kstep;
;             const char* a2 = last ? nA : cA + (size_t)(t + 2) * kstep; const char* b2 = last ? nB : cB + (size_t)(t + 2) * kstep;
;             const char* a3 = a2 + kstep; const char* b3 = b2 + kstep;
;             if constexpr (SP2) {
;             PG8_LDB(B0, 0, 0); PG8_LDB(B1, 0, 1); PG8_SCHED; PG8_LDA(At, 0, 0); PG8_STAGE(PG8_SA(1, 1), a1 + hstep, voffA);
;             PG8_WAIT_V(8); PG8_WAIT_L(0); PG8_BAR; PG8_MMA(0, 0, At, B0); PG8_MMA(0, 1, At, B1); PG8_BAR; PG8_SCHED;
;             PG8_LDA(At, 0, 1); PG8_STAGE(PG8_SB(0, 0), b2, voffB); PG8_STAGE(PG8_SB(0, 1), b2 + hstep, voffB); PG8_STAGE(PG8_SA(0, 0), a2, voffA);
;             PG8_WAIT_V(8); PG8_WAIT_L(0); PG8_BAR; PG8_MMA(1, 0, At, B0); PG8_MMA(1, 1, At, B1); PG8_BAR; PG8_SCHED;
;     ...
;         for (int a = 0; a < 2; ++a)
; #pragma unroll
;             for (int b = 0; b < 2; ++b)
; #pragma unroll
;                 for (int m = 0; m < 4; ++m)
; #pragma unroll
;                     for (int n = 0; n < 2; ++n) acc[a][b][m][n] = (acc_t){0, 0, 0, 0};
.LBB0_1629:
	s_add_u32 s15, s18, 0x100
	s_addc_u32 s65, s19, 0
	s_add_u32 s16, s16, 0xa8080
	s_addc_u32 s17, s17, 0
	s_mov_b32 s71, -2
.LBB0_1630:
	s_add_u32 s18, s16, 0xfff58080
	s_addc_u32 s19, s17, -1
	s_cmp_eq_u32 s71, 24
	s_cselect_b32 s18, s10, s18
	s_cselect_b32 s19, s11, s19
	s_cselect_b32 s22, s12, s15
	s_cselect_b32 s23, s13, s65
	s_add_u32 s20, s18, 0x80
	s_addc_u32 s21, s19, 0
	s_add_i32 s73, 0, 0x10000
	v_add_u32_e32 v132, s73, v133
	s_add_i32 s74, 0, 0x14000
	ds_read_b128 v[140:143], v132
	ds_read_b128 v[144:147], v132 offset:1024
	ds_read_b128 v[148:151], v132 offset:2048
	ds_read_b128 v[152:155], v132 offset:3072
	v_add_u32_e32 v132, s74, v133
	ds_read_b128 v[156:159], v132
	ds_read_b128 v[160:163], v132 offset:1024
	ds_read_b128 v[166:169], v132 offset:2048
	ds_read_b128 v[170:173], v132 offset:3072
	s_add_u32 s68, s16, 0xfffc8000
	s_addc_u32 s69, s17, -1
	ds_read_b128 v[174:177], v138
	ds_read_b128 v[178:181], v138 offset:1024
	ds_read_b128 v[182:185], v138 offset:2048
	ds_read_b128 v[186:189], v138 offset:3072
	ds_read_b128 v[190:193], v138 offset:4096
	ds_read_b128 v[194:197], v138 offset:5120
	ds_read_b128 v[198:201], v138 offset:6144
	ds_read_b128 v[202:205], v138 offset:7168
	s_add_i32 m0, s29, 0xc000
	v_lshl_add_u64 v[134:135], s[68:69], 0, v[130:131]
	s_mov_b64 s[68:69], s[16:17]
	global_load_lds_dwordx4 v[134:135], off
	s_add_i32 m0, s29, 0xe000
	v_lshl_add_u64 v[134:135], s[68:69], 0, v[130:131]
	global_load_lds_dwordx4 v[134:135], off
	s_waitcnt vmcnt(8)
	s_waitcnt lgkmcnt(0)
	s_barrier
	s_setprio 1
	s_waitcnt lgkmcnt(0)
	s_cmp_eq_u32 s71, -2
	s_cbranch_scc1 .Lzmd_s0
	v_mfma_f32_16x16x128_f8f6f4 v[126:129], v[140:147], v[174:181], v[126:129]
	v_mfma_f32_16x16x128_f8f6f4 v[122:125], v[148:155], v[174:181], v[122:125]
	v_mfma_f32_16x16x128_f8f6f4 v[108:111], v[140:147], v[182:189], v[108:111]
	v_mfma_f32_16x16x128_f8f6f4 v[104:107], v[148:155], v[182:189], v[104:107]
	v_mfma_f32_16x16x128_f8f6f4 v[92:95], v[140:147], v[190:197], v[92:95]
	v_mfma_f32_16x16x128_f8f6f4 v[88:91], v[148:155], v[190:197], v[88:91]
	v_mfma_f32_16x16x128_f8f6f4 v[76:79], v[140:147], v[198:205], v[76:79]
	v_mfma_f32_16x16x128_f8f6f4 v[72:75], v[148:155], v[198:205], v[72:75]
	s_setprio 0
	s_setprio 1
	v_mfma_f32_16x16x128_f8f6f4 v[118:121], v[156:163], v[174:181], v[118:121]
	v_mfma_f32_16x16x128_f8f6f4 v[114:117], v[166:173], v[174:181], v[114:117]
	v_mfma_f32_16x16x128_f8f6f4 v[100:103], v[156:163], v[182:189], v[100:103]
	v_mfma_f32_16x16x128_f8f6f4 v[96:99], v[166:173], v[182:189], v[96:99]
	v_mfma_f32_16x16x128_f8f6f4 v[84:87], v[156:163], v[190:197], v[84:87]
	v_mfma_f32_16x16x128_f8f6f4 v[80:83], v[166:173], v[190:197], v[80:83]
	v_mfma_f32_16x16x128_f8f6f4 v[68:71], v[156:163], v[198:205], v[68:71]
	v_mfma_f32_16x16x128_f8f6f4 v[64:67], v[166:173], v[198:205], v[64:67]
	s_setprio 0
.Lzmd_r0:
	s_barrier
	s_mov_b64 s[68:69], s[22:23]
	ds_read_b128 v[174:177], v138 offset:16384
	ds_read_b128 v[178:181], v138 offset:17408
	ds_read_b128 v[182:185], v138 offset:18432
	ds_read_b128 v[186:189], v138 offset:19456
	ds_read_b128 v[190:193], v138 offset:20480
	ds_read_b128 v[194:197], v138 offset:21504
	ds_read_b128 v[198:201], v138 offset:22528
	ds_read_b128 v[202:205], v138 offset:23552
	s_add_i32 s73, s73, s27
	v_lshl_add_u64 v[134:135], s[68:69], 0, v[112:113]
	s_add_u32 s68, s22, 0x38000
	s_mov_b32 m0, s73
	s_addc_u32 s69, s23, 0
	global_load_lds_dwordx4 v[134:135], off
	s_add_i32 m0, s73, 0x2000
	v_lshl_add_u64 v[134:135], s[68:69], 0, v[112:113]
	s_add_u32 s68, s22, 0x70000
	s_addc_u32 s69, s23, 0
	global_load_lds_dwordx4 v[134:135], off
	s_add_i32 s73, s74, s27
	v_lshl_add_u64 v[134:135], s[68:69], 0, v[112:113]
	s_add_u32 s68, s22, 0xa8000
	s_mov_b32 m0, s73
	s_addc_u32 s69, s23, 0
	global_load_lds_dwordx4 v[134:135], off
	s_add_i32 m0, s73, 0x2000
	v_lshl_add_u64 v[134:135], s[68:69], 0, v[112:113]
	s_mov_b64 s[68:69], s[18:19]
	global_load_lds_dwordx4 v[134:135], off
	s_mov_b32 m0, s29
	v_lshl_add_u64 v[134:135], s[68:69], 0, v[130:131]
	s_add_u32 s68, s18, 0x38000
	s_addc_u32 s69, s19, 0
	global_load_lds_dwordx4 v[134:135], off
	s_mov_b32 m0, s30
	v_lshl_add_u64 v[134:135], s[68:69], 0, v[130:131]
	global_load_lds_dwordx4 v[134:135], off
	s_waitcnt vmcnt(8)
	s_waitcnt lgkmcnt(0)
	s_barrier
	s_setprio 1
	s_waitcnt lgkmcnt(0)
	s_cmp_eq_u32 s71, -2
	s_cbranch_scc1 .Lzmd_s1
	v_mfma_f32_16x16x128_f8f6f4 v[60:63], v[140:147], v[174:181], v[60:63]
	v_mfma_f32_16x16x128_f8f6f4 v[56:59], v[148:155], v[174:181], v[56:59]
	v_mfma_f32_16x16x128_f8f6f4 v[48:51], v[140:147], v[182:189], v[48:51]
	v_mfma_f32_16x16x128_f8f6f4 v[40:43], v[148:155], v[182:189], v[40:43]
	v_mfma_f32_16x16x128_f8f6f4 v[32:35], v[140:147], v[190:197], v[32:35]
	v_mfma_f32_16x16x128_f8f6f4 v[24:27], v[148:155], v[190:197], v[24:27]
	v_mfma_f32_16x16x128_f8f6f4 v[16:19], v[140:147], v[198:205], v[16:19]
	v_mfma_f32_16x16x128_f8f6f4 v[8:11], v[148:155], v[198:205], v[8:11]
	s_setprio 0
	s_setprio 1
	v_mfma_f32_16x16x128_f8f6f4 v[52:55], v[156:163], v[174:181], v[52:55]
	v_mfma_f32_16x16x128_f8f6f4 v[44:47], v[166:173], v[174:181], v[44:47]
	v_mfma_f32_16x16x128_f8f6f4 v[36:39], v[156:163], v[182:189], v[36:39]
	v_mfma_f32_16x16x128_f8f6f4 v[28:31], v[166:173], v[182:189], v[28:31]
	v_mfma_f32_16x16x128_f8f6f4 v[20:23], v[156:163], v[190:197], v[20:23]
	v_mfma_f32_16x16x128_f8f6f4 v[12:15], v[166:173], v[190:197], v[12:15]
	v_mfma_f32_16x16x128_f8f6f4 v[4:7], v[156:163], v[198:205], v[4:7]
	v_mfma_f32_16x16x128_f8f6f4 v[0:3], v[166:173], v[198:205], v[0:3]
	s_setprio 0
; #define PG8_STAGE(bufoff, gbase, voff) do { _Pragma("unroll") for (int _i = 0; _i < 2; ++_i) { const char* gb_ = (const char*)(gbase) + _i * rstep; asm volatile("" : "+s"(gb_));   \
;         __builtin_amdgcn_global_load_lds((const unsigned*)(gb_ + (voff)), (LAS unsigned*)(lds + (bufoff) + ldsw + _i * 8192), 16, 0, 0); } } while (0)
; #define PG8_LDA(dst, b, h) do { _Pragma("unroll") for (int m = 0; m < 4; ++m) _Pragma("unroll") for (int k = 0; k < 2; ++k) dst[m][k] = *(const LAS bf16x8*)(lds + PG8_SA(b, h) + aoff + m * 2048 + k * 1024); } while (0)
; #define PG8_LDB(dst, b, h) do { _Pragma("unroll") for (int n = 0; n < 2; ++n) _Pragma("unroll") for (int k = 0; k < 2; ++k) dst[n][k] = *(const LAS bf16x8*)(lds + PG8_SB(b, h) + boff + n * 2048 + k * 1024); } while (0)
; #define PG8_WAIT_V(n) asm volatile("s_waitcnt vmcnt(" #n ")" ::: "memory")
; #define PG8_WAIT_L(n) asm volatile("s_waitcnt lgkmcnt(" #n ")" ::: "memory")
; #define PG8_BAR __builtin_amdgcn_s_barrier()
; #define PG8_SCHED __builtin_amdgcn_sched_barrier(0)
; template <class Epi, class Sched, bool ALIGN_EPI = true, bool SP2 = true, bool I8 = false, bool F8 = false>
; __device__ __forceinline__ void gemm_phase(LAS unsigned char* lds, const int K, const Sched& S, const Epi& E, const int wave) {
;     ...
;             PG8_LDB(B0, 1, 0); PG8_LDB(B1, 1, 1); PG8_SCHED; PG8_LDA(At, 1, 0); PG8_STAGE(PG8_SA(0, 1), a2 + hstep, voffA);
;             PG8_WAIT_V(8); PG8_WAIT_L(0); PG8_BAR; PG8_MMA(0, 0, At, B0); PG8_MMA(0, 1, At, B1); PG8_BAR; PG8_SCHED;
;             PG8_LDA(At, 1, 1); PG8_STAGE(PG8_SB(1, 0), b3, voffB); PG8_STAGE(PG8_SB(1, 1), b3 + hstep, voffB); PG8_STAGE(PG8_SA(1, 0), a3, voffA);
;             PG8_WAIT_V(8); PG8_WAIT_L(0); PG8_BAR; PG8_MMA(1, 0, At, B0); PG8_MMA(1, 1, At, B1); PG8_BAR; PG8_SCHED;
.Lzmd_r1:
	s_barrier
	s_add_i32 s73, 0, 0x18000
	v_add_u32_e32 v132, s73, v133
	s_add_i32 s74, 0, 0x1c000
	ds_read_b128 v[140:143], v132
	ds_read_b128 v[144:147], v132 offset:1024
	ds_read_b128 v[148:151], v132 offset:2048
	ds_read_b128 v[152:155], v132 offset:3072
	v_add_u32_e32 v132, s74, v133
	ds_read_b128 v[156:159], v132
	ds_read_b128 v[160:163], v132 offset:1024
	ds_read_b128 v[166:169], v132 offset:2048
	ds_read_b128 v[170:173], v132 offset:3072
	s_add_u32 s68, s18, 0x70000
	s_addc_u32 s69, s19, 0
	ds_read_b128 v[174:177], v138 offset:32768
	ds_read_b128 v[178:181], v138 offset:33792
	ds_read_b128 v[182:185], v138 offset:34816
	ds_read_b128 v[186:189], v138 offset:35840
	ds_read_b128 v[190:193], v138 offset:36864
	ds_read_b128 v[194:197], v138 offset:37888
	ds_read_b128 v[198:201], v138 offset:38912
	ds_read_b128 v[202:205], v138 offset:39936
	s_mov_b32 m0, s31
	v_lshl_add_u64 v[134:135], s[68:69], 0, v[130:131]
	s_add_u32 s68, s18, 0xa8000
	s_addc_u32 s69, s19, 0
	global_load_lds_dwordx4 v[134:135], off
	s_mov_b32 m0, s33
	v_lshl_add_u64 v[134:135], s[68:69], 0, v[130:131]
	global_load_lds_dwordx4 v[134:135], off
	s_waitcnt vmcnt(8)
	s_waitcnt lgkmcnt(0)
	s_barrier
	s_setprio 1
	s_waitcnt lgkmcnt(0)
	v_mfma_f32_16x16x128_f8f6f4 v[126:129], v[140:147], v[174:181], v[126:129]
	v_mfma_f32_16x16x128_f8f6f4 v[122:125], v[148:155], v[174:181], v[122:125]
	v_mfma_f32_16x16x128_f8f6f4 v[108:111], v[140:147], v[182:189], v[108:111]
	v_mfma_f32_16x16x128_f8f6f4 v[104:107], v[148:155], v[182:189], v[104:107]
	v_mfma_f32_16x16x128_f8f6f4 v[92:95], v[140:147], v[190:197], v[92:95]
	v_mfma_f32_16x16x128_f8f6f4 v[88:91], v[148:155], v[190:197], v[88:91]
	v_mfma_f32_16x16x128_f8f6f4 v[76:79], v[140:147], v[198:205], v[76:79]
	v_mfma_f32_16x16x128_f8f6f4 v[72:75], v[148:155], v[198:205], v[72:75]
	s_setprio 0
	s_setprio 1
	v_mfma_f32_16x16x128_f8f6f4 v[118:121], v[156:163], v[174:181], v[118:121]
	v_mfma_f32_16x16x128_f8f6f4 v[114:117], v[166:173], v[174:181], v[114:117]
	v_mfma_f32_16x16x128_f8f6f4 v[100:103], v[156:163], v[182:189], v[100:103]
	v_mfma_f32_16x16x128_f8f6f4 v[96:99], v[166:173], v[182:189], v[96:99]
	v_mfma_f32_16x16x128_f8f6f4 v[84:87], v[156:163], v[190:197], v[84:87]
	v_mfma_f32_16x16x128_f8f6f4 v[80:83], v[166:173], v[190:197], v[80:83]
	v_mfma_f32_16x16x128_f8f6f4 v[68:71], v[156:163], v[198:205], v[68:71]
	v_mfma_f32_16x16x128_f8f6f4 v[64:67], v[166:173], v[198:205], v[64:67]
	s_setprio 0
	s_barrier
	s_add_u32 s68, s22, 0x80
	s_addc_u32 s69, s23, 0
	ds_read_b128 v[174:177], v138 offset:49152
	ds_read_b128 v[178:181], v138 offset:50176
	ds_read_b128 v[182:185], v138 offset:51200
	ds_read_b128 v[186:189], v138 offset:52224
	ds_read_b128 v[190:193], v138 offset:53248
	ds_read_b128 v[194:197], v138 offset:54272
	ds_read_b128 v[198:201], v138 offset:55296
	ds_read_b128 v[202:205], v138 offset:56320
	s_add_i32 s73, s73, s27
	v_lshl_add_u64 v[134:135], s[68:69], 0, v[112:113]
	s_add_u32 s68, s22, 0x38080
	s_mov_b32 m0, s73
	s_addc_u32 s69, s23, 0
	global_load_lds_dwordx4 v[134:135], off
	s_add_i32 m0, s73, 0x2000
	v_lshl_add_u64 v[134:135], s[68:69], 0, v[112:113]
	s_add_u32 s68, s22, 0x70080
	s_addc_u32 s69, s23, 0
	global_load_lds_dwordx4 v[134:135], off
	s_nop 0
	v_lshl_add_u64 v[134:135], s[68:69], 0, v[112:113]
	s_add_i32 s68, s74, s27
	s_mov_b32 m0, s68
	s_add_u32 s22, s22, 0xa8080
	global_load_lds_dwordx4 v[134:135], off
	s_addc_u32 s23, s23, 0
	s_add_i32 m0, s68, 0x2000
	s_add_u32 s18, s18, 0x38080
	v_lshl_add_u64 v[134:135], s[22:23], 0, v[112:113]
	global_load_lds_dwordx4 v[134:135], off
	s_mov_b32 m0, s40
	v_lshl_add_u64 v[134:135], s[20:21], 0, v[130:131]
	s_addc_u32 s19, s19, 0
	global_load_lds_dwordx4 v[134:135], off
	s_mov_b32 m0, s41
	v_lshl_add_u64 v[134:135], s[18:19], 0, v[130:131]
	global_load_lds_dwordx4 v[134:135], off
	s_waitcnt vmcnt(8)
	s_waitcnt lgkmcnt(0)
	s_barrier
	s_setprio 1
	s_waitcnt lgkmcnt(0)
	v_mfma_f32_16x16x128_f8f6f4 v[60:63], v[140:147], v[174:181], v[60:63]
	v_mfma_f32_16x16x128_f8f6f4 v[56:59], v[148:155], v[174:181], v[56:59]
	v_mfma_f32_16x16x128_f8f6f4 v[48:51], v[140:147], v[182:189], v[48:51]
	v_mfma_f32_16x16x128_f8f6f4 v[40:43], v[148:155], v[182:189], v[40:43]
	v_mfma_f32_16x16x128_f8f6f4 v[32:35], v[140:147], v[190:197], v[32:35]
	v_mfma_f32_16x16x128_f8f6f4 v[24:27], v[148:155], v[190:197], v[24:27]
	v_mfma_f32_16x16x128_f8f6f4 v[16:19], v[140:147], v[198:205], v[16:19]
	v_mfma_f32_16x16x128_f8f6f4 v[8:11], v[148:155], v[198:205], v[8:11]
	s_setprio 0
	s_setprio 1
	v_mfma_f32_16x16x128_f8f6f4 v[52:55], v[156:163], v[174:181], v[52:55]
	v_mfma_f32_16x16x128_f8f6f4 v[44:47], v[166:173], v[174:181], v[44:47]
	v_mfma_f32_16x16x128_f8f6f4 v[36:39], v[156:163], v[182:189], v[36:39]
	v_mfma_f32_16x16x128_f8f6f4 v[28:31], v[166:173], v[182:189], v[28:31]
	v_mfma_f32_16x16x128_f8f6f4 v[20:23], v[156:163], v[190:197], v[20:23]
	v_mfma_f32_16x16x128_f8f6f4 v[12:15], v[166:173], v[190:197], v[12:15]
	v_mfma_f32_16x16x128_f8f6f4 v[4:7], v[156:163], v[198:205], v[4:7]
	v_mfma_f32_16x16x128_f8f6f4 v[0:3], v[166:173], v[198:205], v[0:3]
	s_setprio 0
	s_barrier
	s_add_i32 s71, s71, 2
	s_add_u32 s15, s15, 0x100
	s_addc_u32 s65, s65, 0
	s_add_u32 s16, s16, 0x100
	s_addc_u32 s17, s17, 0
	s_cmp_gt_u32 s71, 25
	s_cbranch_scc0 .LBB0_1630
	s_and_b64 vcc, exec, s[8:9]
	s_cbranch_vccz .LBB0_1633
	s_barrier

; #define PG8_STAGE(bufoff, gbase, voff) do { _Pragma("unroll") for (int _i = 0; _i < 2; ++_i) { const char* gb_ = (const char*)(gbase) + _i * rstep; asm volatile("" : "+s"(gb_));   \
;         __builtin_amdgcn_global_load_lds((const unsigned*)(gb_ + (voff)), (LAS unsigned*)(lds + (bufoff) + ldsw + _i * 8192), 16, 0, 0); } } while (0)
; #define PG8_LDA(dst, b, h) do { _Pragma("unroll") for (int m = 0; m < 4; ++m) _Pragma("unroll") for (int k = 0; k < 2; ++k) dst[m][k] = *(const LAS bf16x8*)(lds + PG8_SA(b, h) + aoff + m * 2048 + k * 1024); } while (0)
; #define PG8_WAIT_V(n) asm volatile("s_waitcnt vmcnt(" #n ")" ::: "memory")
; #define PG8_WAIT_L(n) asm volatile("s_waitcnt lgkmcnt(" #n ")" ::: "memory")
; #define PG8_BAR __builtin_amdgcn_s_barrier()
; #define PG8_SCHED __builtin_amdgcn_sched_barrier(0)
; __device__ __forceinline__ void mma8(f32x4& c, const bf16x8& a0, const bf16x8& a1, const bf16x8& b0, const bf16x8& b1) {
;     typedef int i32x4_ __attribute__((ext_vector_type(4)));
;     const i32x8 A = __builtin_shufflevector(__builtin_bit_cast(i32x4_, a0), __builtin_bit_cast(i32x4_, a1), 0, 1, 2, 3, 4, 5, 6, 7), Bv = __builtin_shufflevector(__builtin_bit_cast(i32x4_, b0), __builtin_bit_cast(i32x4_, b1), 0, 1, 2, 3, 4, 5, 6, 7);
;     c = __builtin_amdgcn_mfma_scale_f32_16x16x128_f8f6f4(A, Bv, c, 0, 0, 0, 0, 0, 0);
; }
; template <class Epi, class Sched, bool ALIGN_EPI = true, bool SP2 = true, bool I8 = false, bool F8 = false>
; __device__ __forceinline__ void gemm_phase(LAS unsigned char* lds, const int K, const Sched& S, const Epi& E, const int wave) {
;     ...
;             PG8_WAIT_V(8); PG8_WAIT_L(0); PG8_BAR; PG8_MMA(0, 0, At, B0); PG8_MMA(0, 1, At, B1); PG8_BAR; PG8_SCHED;
;             PG8_LDA(At, 0, 1); PG8_STAGE(PG8_SB(0, 0), b2, voffB); PG8_STAGE(PG8_SB(0, 1), b2 + hstep, voffB); PG8_STAGE(PG8_SA(0, 0), a2, voffA);
;             PG8_WAIT_V(8); PG8_WAIT_L(0); PG8_BAR; PG8_MMA(1, 0, At, B0); PG8_MMA(1, 1, At, B1); PG8_BAR; PG8_SCHED;
.Lzdd_s0:
	v_mfma_f32_16x16x128_f8f6f4 v[126:129], v[130:137], v[174:181], 0
	v_mfma_f32_16x16x128_f8f6f4 v[122:125], v[138:145], v[174:181], 0
	v_mfma_f32_16x16x128_f8f6f4 v[108:111], v[130:137], v[182:189], 0
	v_mfma_f32_16x16x128_f8f6f4 v[104:107], v[138:145], v[182:189], 0
	v_mfma_f32_16x16x128_f8f6f4 v[92:95], v[130:137], v[190:197], 0
	v_mfma_f32_16x16x128_f8f6f4 v[88:91], v[138:145], v[190:197], 0
	v_mfma_f32_16x16x128_f8f6f4 v[76:79], v[130:137], v[198:205], 0
	v_mfma_f32_16x16x128_f8f6f4 v[72:75], v[138:145], v[198:205], 0
	s_setprio 0
	s_setprio 1
	v_mfma_f32_16x16x128_f8f6f4 v[118:121], v[146:153], v[174:181], 0
	v_mfma_f32_16x16x128_f8f6f4 v[114:117], v[166:173], v[174:181], 0
	v_mfma_f32_16x16x128_f8f6f4 v[100:103], v[146:153], v[182:189], 0
	v_mfma_f32_16x16x128_f8f6f4 v[96:99], v[166:173], v[182:189], 0
	v_mfma_f32_16x16x128_f8f6f4 v[84:87], v[146:153], v[190:197], 0
	v_mfma_f32_16x16x128_f8f6f4 v[80:83], v[166:173], v[190:197], 0
	v_mfma_f32_16x16x128_f8f6f4 v[68:71], v[146:153], v[198:205], 0
	v_mfma_f32_16x16x128_f8f6f4 v[64:67], v[166:173], v[198:205], 0
	s_setprio 0
	s_branch .Lzdd_r0
.Lzdd_s1:
	v_mfma_f32_16x16x128_f8f6f4 v[60:63], v[130:137], v[174:181], 0
	v_mfma_f32_16x16x128_f8f6f4 v[56:59], v[138:145], v[174:181], 0
	v_mfma_f32_16x16x128_f8f6f4 v[44:47], v[130:137], v[182:189], 0
	v_mfma_f32_16x16x128_f8f6f4 v[40:43], v[138:145], v[182:189], 0
	v_mfma_f32_16x16x128_f8f6f4 v[28:31], v[130:137], v[190:197], 0
	v_mfma_f32_16x16x128_f8f6f4 v[24:27], v[138:145], v[190:197], 0
	v_mfma_f32_16x16x128_f8f6f4 v[12:15], v[130:137], v[198:205], 0
	v_mfma_f32_16x16x128_f8f6f4 v[8:11], v[138:145], v[198:205], 0
	s_setprio 0
	s_setprio 1
	v_mfma_f32_16x16x128_f8f6f4 v[52:55], v[146:153], v[174:181], 0
	v_mfma_f32_16x16x128_f8f6f4 v[48:51], v[166:173], v[174:181], 0
	v_mfma_f32_16x16x128_f8f6f4 v[36:39], v[146:153], v[182:189], 0
	v_mfma_f32_16x16x128_f8f6f4 v[32:35], v[166:173], v[182:189], 0
	v_mfma_f32_16x16x128_f8f6f4 v[20:23], v[146:153], v[190:197], 0
	v_mfma_f32_16x16x128_f8f6f4 v[16:19], v[166:173], v[190:197], 0
	v_mfma_f32_16x16x128_f8f6f4 v[4:7], v[146:153], v[198:205], 0
	v_mfma_f32_16x16x128_f8f6f4 v[0:3], v[166:173], v[198:205], 0
	s_setprio 0
	s_branch .Lzdd_r1

; #define PG8_STAGE(bufoff, gbase, voff) do { _Pragma("unroll") for (int _i = 0; _i < 2; ++_i) { const char* gb_ = (const char*)(gbase) + _i * rstep; asm volatile("" : "+s"(gb_));   \
;         __builtin_amdgcn_global_load_lds((const unsigned*)(gb_ + (voff)), (LAS unsigned*)(lds + (bufoff) + ldsw + _i * 8192), 16, 0, 0); } } while (0)
; #define PG8_LDA(dst, b, h) do { _Pragma("unroll") for (int m = 0; m < 4; ++m) _Pragma("unroll") for (int k = 0; k < 2; ++k) dst[m][k] = *(const LAS bf16x8*)(lds + PG8_SA(b, h) + aoff + m * 2048 + k * 1024); } while (0)
; #define PG8_LDB(dst, b, h) do { _Pragma("unroll") for (int n = 0; n < 2; ++n) _Pragma("unroll") for (int k = 0; k < 2; ++k) dst[n][k] = *(const LAS bf16x8*)(lds + PG8_SB(b, h) + boff + n * 2048 + k * 1024); } while (0)
; #define PG8_WAIT_V(n) asm volatile("s_waitcnt vmcnt(" #n ")" ::: "memory")
; #define PG8_WAIT_L(n) asm volatile("s_waitcnt lgkmcnt(" #n ")" ::: "memory")
; #define PG8_BAR __builtin_amdgcn_s_barrier()
; template <class Epi, class Sched, bool ALIGN_EPI = true, bool SP2 = true, bool I8 = false, bool F8 = false>
; __device__ __forceinline__ void gemm_phase(LAS unsigned char* lds, const int K, const Sched& S, const Epi& E, const int wave) {
;     ...
;         for (int t = 0; t < nt; t += 2) {
;             const bool last = (t == nt - 2);
;             const char* a1 = cA + (size_t)(t + 1) * kstep;
;             const char* a2 = last ? nA : cA + (size_t)(t + 2) * kstep; const char* b2 = last ? nB : cB + (size_t)(t + 2) * kstep;
;             const char* a3 = a2 + kstep; const char* b3 = b2 + kstep;
;             if constexpr (SP2) {
;             PG8_LDB(B0, 0, 0); PG8_LDB(B1, 0, 1); PG8_SCHED; PG8_LDA(At, 0, 0); PG8_STAGE(PG8_SA(1, 1), a1 + hstep, voffA);
;             PG8_WAIT_V(8); PG8_WAIT_L(0); PG8_BAR; PG8_MMA(0, 0, At, B0); PG8_MMA(0, 1, At, B1); PG8_BAR; PG8_SCHED;
;             PG8_LDA(At, 0, 1); PG8_STAGE(PG8_SB(0, 0), b2, voffB); PG8_STAGE(PG8_SB(0, 1), b2 + hstep, voffB); PG8_STAGE(PG8_SA(0, 0), a2, voffA);
;             PG8_WAIT_V(8); PG8_WAIT_L(0); PG8_BAR; PG8_MMA(1, 0, At, B0); PG8_MMA(1, 1, At, B1); PG8_BAR; PG8_SCHED;
;     ...
;         for (int a = 0; a < 2; ++a)
; #pragma unroll
;             for (int b = 0; b < 2; ++b)
; #pragma unroll
;                 for (int m = 0; m < 4; ++m)
; #pragma unroll
;                     for (int n = 0; n < 2; ++n) acc[a][b][m][n] = (acc_t){0, 0, 0, 0};
.LBB0_1836:
	s_add_u32 s45, s18, 0x100
	s_addc_u32 s46, s19, 0
	s_add_u32 s2, s2, 0xa8080
	s_addc_u32 s3, s3, 0
	s_mov_b32 s47, -2
.LBB0_1837:
	s_add_u32 s18, s2, 0xfff58080
	s_addc_u32 s19, s3, -1
	s_cmp_eq_u32 s47, 24
	s_cselect_b32 s18, s14, s18
	s_cselect_b32 s19, s15, s19
	s_cselect_b32 s22, s16, s45
	s_cselect_b32 s23, s17, s46
	s_add_u32 s20, s18, 0x80
	s_addc_u32 s21, s19, 0
	s_add_i32 s50, 0, 0x10000
	s_add_i32 s51, 0, 0x14000
	v_add_u32_e32 v142, s50, v159
	v_add_u32_e32 v156, s51, v159
	ds_read_b128 v[130:133], v142
	ds_read_b128 v[134:137], v142 offset:1024
	ds_read_b128 v[138:141], v142 offset:2048
	ds_read_b128 v[142:145], v142 offset:3072
	ds_read_b128 v[146:149], v156
	ds_read_b128 v[150:153], v156 offset:1024
	ds_read_b128 v[166:169], v156 offset:2048
	ds_read_b128 v[170:173], v156 offset:3072
	s_add_u32 s48, s2, 0xfffc8000
	s_addc_u32 s49, s3, -1
	ds_read_b128 v[174:177], v165
	ds_read_b128 v[178:181], v165 offset:1024
	ds_read_b128 v[182:185], v165 offset:2048
	ds_read_b128 v[186:189], v165 offset:3072
	ds_read_b128 v[190:193], v165 offset:4096
	ds_read_b128 v[194:197], v165 offset:5120
	ds_read_b128 v[198:201], v165 offset:6144
	ds_read_b128 v[202:205], v165 offset:7168
	s_add_i32 m0, s30, 0xc000
	v_lshl_add_u64 v[156:157], s[48:49], 0, v[154:155]
	s_mov_b64 s[48:49], s[2:3]
	global_load_lds_dwordx4 v[156:157], off
	s_add_i32 m0, s30, 0xe000
	v_lshl_add_u64 v[156:157], s[48:49], 0, v[154:155]
	global_load_lds_dwordx4 v[156:157], off
	s_waitcnt vmcnt(8)
	s_waitcnt lgkmcnt(0)
	s_barrier
	s_setprio 1
	s_waitcnt lgkmcnt(0)
	s_cmp_eq_u32 s47, -2
	s_cbranch_scc1 .Lzdd_s0
	v_mfma_f32_16x16x128_f8f6f4 v[126:129], v[130:137], v[174:181], v[126:129]
	v_mfma_f32_16x16x128_f8f6f4 v[122:125], v[138:145], v[174:181], v[122:125]
	v_mfma_f32_16x16x128_f8f6f4 v[108:111], v[130:137], v[182:189], v[108:111]
	v_mfma_f32_16x16x128_f8f6f4 v[104:107], v[138:145], v[182:189], v[104:107]
	v_mfma_f32_16x16x128_f8f6f4 v[92:95], v[130:137], v[190:197], v[92:95]
	v_mfma_f32_16x16x128_f8f6f4 v[88:91], v[138:145], v[190:197], v[88:91]
	v_mfma_f32_16x16x128_f8f6f4 v[76:79], v[130:137], v[198:205], v[76:79]
	v_mfma_f32_16x16x128_f8f6f4 v[72:75], v[138:145], v[198:205], v[72:75]
	s_setprio 0
	s_setprio 1
	v_mfma_f32_16x16x128_f8f6f4 v[118:121], v[146:153], v[174:181], v[118:121]
	v_mfma_f32_16x16x128_f8f6f4 v[114:117], v[166:173], v[174:181], v[114:117]
	v_mfma_f32_16x16x128_f8f6f4 v[100:103], v[146:153], v[182:189], v[100:103]
	v_mfma_f32_16x16x128_f8f6f4 v[96:99], v[166:173], v[182:189], v[96:99]
	v_mfma_f32_16x16x128_f8f6f4 v[84:87], v[146:153], v[190:197], v[84:87]
	v_mfma_f32_16x16x128_f8f6f4 v[80:83], v[166:173], v[190:197], v[80:83]
	v_mfma_f32_16x16x128_f8f6f4 v[68:71], v[146:153], v[198:205], v[68:71]
	v_mfma_f32_16x16x128_f8f6f4 v[64:67], v[166:173], v[198:205], v[64:67]
	s_setprio 0
.Lzdd_r0:
	s_barrier
	s_mov_b64 s[48:49], s[22:23]
	ds_read_b128 v[174:177], v165 offset:16384
	ds_read_b128 v[178:181], v165 offset:17408
	ds_read_b128 v[182:185], v165 offset:18432
	ds_read_b128 v[186:189], v165 offset:19456
	ds_read_b128 v[190:193], v165 offset:20480
	ds_read_b128 v[194:197], v165 offset:21504
	ds_read_b128 v[198:201], v165 offset:22528
	ds_read_b128 v[202:205], v165 offset:23552
	s_add_i32 s50, s50, s29
	v_lshl_add_u64 v[156:157], s[48:49], 0, v[112:113]
	s_add_u32 s48, s22, 0x38000
	s_mov_b32 m0, s50
	s_addc_u32 s49, s23, 0
	global_load_lds_dwordx4 v[156:157], off
	s_add_i32 m0, s50, 0x2000
	v_lshl_add_u64 v[156:157], s[48:49], 0, v[112:113]
	s_add_u32 s48, s22, 0x70000
	s_addc_u32 s49, s23, 0
	global_load_lds_dwordx4 v[156:157], off
	s_add_i32 s50, s51, s29
	v_lshl_add_u64 v[156:157], s[48:49], 0, v[112:113]
	s_add_u32 s48, s22, 0xa8000
	s_mov_b32 m0, s50
	s_addc_u32 s49, s23, 0
	global_load_lds_dwordx4 v[156:157], off
	s_add_i32 m0, s50, 0x2000
	v_lshl_add_u64 v[156:157], s[48:49], 0, v[112:113]
	s_mov_b64 s[48:49], s[18:19]
	global_load_lds_dwordx4 v[156:157], off
	s_mov_b32 m0, s30
	v_lshl_add_u64 v[156:157], s[48:49], 0, v[154:155]
	s_add_u32 s48, s18, 0x38000
	s_addc_u32 s49, s19, 0
	global_load_lds_dwordx4 v[156:157], off
	s_mov_b32 m0, s31
	v_lshl_add_u64 v[156:157], s[48:49], 0, v[154:155]
	global_load_lds_dwordx4 v[156:157], off
	s_waitcnt vmcnt(8)
	s_waitcnt lgkmcnt(0)
	s_barrier
	s_setprio 1
	s_waitcnt lgkmcnt(0)
	s_cmp_eq_u32 s47, -2
	s_cbranch_scc1 .Lzdd_s1
	v_mfma_f32_16x16x128_f8f6f4 v[60:63], v[130:137], v[174:181], v[60:63]
	v_mfma_f32_16x16x128_f8f6f4 v[56:59], v[138:145], v[174:181], v[56:59]
	v_mfma_f32_16x16x128_f8f6f4 v[44:47], v[130:137], v[182:189], v[44:47]
	v_mfma_f32_16x16x128_f8f6f4 v[40:43], v[138:145], v[182:189], v[40:43]
	v_mfma_f32_16x16x128_f8f6f4 v[28:31], v[130:137], v[190:197], v[28:31]
	v_mfma_f32_16x16x128_f8f6f4 v[24:27], v[138:145], v[190:197], v[24:27]
	v_mfma_f32_16x16x128_f8f6f4 v[12:15], v[130:137], v[198:205], v[12:15]
	v_mfma_f32_16x16x128_f8f6f4 v[8:11], v[138:145], v[198:205], v[8:11]
	s_setprio 0
	s_setprio 1
	v_mfma_f32_16x16x128_f8f6f4 v[52:55], v[146:153], v[174:181], v[52:55]
	v_mfma_f32_16x16x128_f8f6f4 v[48:51], v[166:173], v[174:181], v[48:51]
	v_mfma_f32_16x16x128_f8f6f4 v[36:39], v[146:153], v[182:189], v[36:39]
	v_mfma_f32_16x16x128_f8f6f4 v[32:35], v[166:173], v[182:189], v[32:35]
	v_mfma_f32_16x16x128_f8f6f4 v[20:23], v[146:153], v[190:197], v[20:23]
	v_mfma_f32_16x16x128_f8f6f4 v[16:19], v[166:173], v[190:197], v[16:19]
	v_mfma_f32_16x16x128_f8f6f4 v[4:7], v[146:153], v[198:205], v[4:7]
	v_mfma_f32_16x16x128_f8f6f4 v[0:3], v[166:173], v[198:205], v[0:3]
	s_setprio 0
; #define PG8_STAGE(bufoff, gbase, voff) do { _Pragma("unroll") for (int _i = 0; _i < 2; ++_i) { const char* gb_ = (const char*)(gbase) + _i * rstep; asm volatile("" : "+s"(gb_));   \
;         __builtin_amdgcn_global_load_lds((const unsigned*)(gb_ + (voff)), (LAS unsigned*)(lds + (bufoff) + ldsw + _i * 8192), 16, 0, 0); } } while (0)
; #define PG8_LDA(dst, b, h) do { _Pragma("unroll") for (int m = 0; m < 4; ++m) _Pragma("unroll") for (int k = 0; k < 2; ++k) dst[m][k] = *(const LAS bf16x8*)(lds + PG8_SA(b, h) + aoff + m * 2048 + k * 1024); } while (0)
; #define PG8_LDB(dst, b, h) do { _Pragma("unroll") for (int n = 0; n < 2; ++n) _Pragma("unroll") for (int k = 0; k < 2; ++k) dst[n][k] = *(const LAS bf16x8*)(lds + PG8_SB(b, h) + boff + n * 2048 + k * 1024); } while (0)
; #define PG8_WAIT_V(n) asm volatile("s_waitcnt vmcnt(" #n ")" ::: "memory")
; #define PG8_WAIT_L(n) asm volatile("s_waitcnt lgkmcnt(" #n ")" ::: "memory")
; #define PG8_BAR __builtin_amdgcn_s_barrier()
; #define PG8_SCHED __builtin_amdgcn_sched_barrier(0)
; template <class Epi, class Sched, bool ALIGN_EPI = true, bool SP2 = true, bool I8 = false, bool F8 = false>
; __device__ __forceinline__ void gemm_phase(LAS unsigned char* lds, const int K, const Sched& S, const Epi& E, const int wave) {
;     ...
;             PG8_LDB(B0, 1, 0); PG8_LDB(B1, 1, 1); PG8_SCHED; PG8_LDA(At, 1, 0); PG8_STAGE(PG8_SA(0, 1), a2 + hstep, voffA);
;             PG8_WAIT_V(8); PG8_WAIT_L(0); PG8_BAR; PG8_MMA(0, 0, At, B0); PG8_MMA(0, 1, At, B1); PG8_BAR; PG8_SCHED;
;             PG8_LDA(At, 1, 1); PG8_STAGE(PG8_SB(1, 0), b3, voffB); PG8_STAGE(PG8_SB(1, 1), b3 + hstep, voffB); PG8_STAGE(PG8_SA(1, 0), a3, voffA);
;             PG8_WAIT_V(8); PG8_WAIT_L(0); PG8_BAR; PG8_MMA(1, 0, At, B0); PG8_MMA(1, 1, At, B1); PG8_BAR; PG8_SCHED;
.Lzdd_r1:
	s_barrier
	s_add_i32 s50, 0, 0x18000
	s_add_i32 s51, 0, 0x1c000
	v_add_u32_e32 v142, s50, v159
	v_add_u32_e32 v156, s51, v159
	ds_read_b128 v[130:133], v142
	ds_read_b128 v[134:137], v142 offset:1024
	ds_read_b128 v[138:141], v142 offset:2048
	ds_read_b128 v[142:145], v142 offset:3072
	ds_read_b128 v[146:149], v156
	ds_read_b128 v[150:153], v156 offset:1024
	ds_read_b128 v[166:169], v156 offset:2048
	ds_read_b128 v[170:173], v156 offset:3072
	s_add_u32 s48, s18, 0x70000
	s_addc_u32 s49, s19, 0
	ds_read_b128 v[174:177], v165 offset:32768
	ds_read_b128 v[178:181], v165 offset:33792
	ds_read_b128 v[182:185], v165 offset:34816
	ds_read_b128 v[186:189], v165 offset:35840
	ds_read_b128 v[190:193], v165 offset:36864
	ds_read_b128 v[194:197], v165 offset:37888
	ds_read_b128 v[198:201], v165 offset:38912
	ds_read_b128 v[202:205], v165 offset:39936
	s_mov_b32 m0, s33
	v_lshl_add_u64 v[156:157], s[48:49], 0, v[154:155]
	s_add_u32 s48, s18, 0xa8000
	s_addc_u32 s49, s19, 0
	global_load_lds_dwordx4 v[156:157], off
	s_mov_b32 m0, s34
	v_lshl_add_u64 v[156:157], s[48:49], 0, v[154:155]
	global_load_lds_dwordx4 v[156:157], off
	s_waitcnt vmcnt(8)
	s_waitcnt lgkmcnt(0)
	s_barrier
	s_setprio 1
	s_waitcnt lgkmcnt(0)
	v_mfma_f32_16x16x128_f8f6f4 v[126:129], v[130:137], v[174:181], v[126:129]
	v_mfma_f32_16x16x128_f8f6f4 v[122:125], v[138:145], v[174:181], v[122:125]
	v_mfma_f32_16x16x128_f8f6f4 v[108:111], v[130:137], v[182:189], v[108:111]
	v_mfma_f32_16x16x128_f8f6f4 v[104:107], v[138:145], v[182:189], v[104:107]
	v_mfma_f32_16x16x128_f8f6f4 v[92:95], v[130:137], v[190:197], v[92:95]
	v_mfma_f32_16x16x128_f8f6f4 v[88:91], v[138:145], v[190:197], v[88:91]
	v_mfma_f32_16x16x128_f8f6f4 v[76:79], v[130:137], v[198:205], v[76:79]
	v_mfma_f32_16x16x128_f8f6f4 v[72:75], v[138:145], v[198:205], v[72:75]
	s_setprio 0
	s_setprio 1
	v_mfma_f32_16x16x128_f8f6f4 v[118:121], v[146:153], v[174:181], v[118:121]
	v_mfma_f32_16x16x128_f8f6f4 v[114:117], v[166:173], v[174:181], v[114:117]
	v_mfma_f32_16x16x128_f8f6f4 v[100:103], v[146:153], v[182:189], v[100:103]
	v_mfma_f32_16x16x128_f8f6f4 v[96:99], v[166:173], v[182:189], v[96:99]
	v_mfma_f32_16x16x128_f8f6f4 v[84:87], v[146:153], v[190:197], v[84:87]
	v_mfma_f32_16x16x128_f8f6f4 v[80:83], v[166:173], v[190:197], v[80:83]
	v_mfma_f32_16x16x128_f8f6f4 v[68:71], v[146:153], v[198:205], v[68:71]
	v_mfma_f32_16x16x128_f8f6f4 v[64:67], v[166:173], v[198:205], v[64:67]
	s_setprio 0
	s_barrier
	s_add_u32 s48, s22, 0x80
	s_addc_u32 s49, s23, 0
	ds_read_b128 v[174:177], v165 offset:49152
	ds_read_b128 v[178:181], v165 offset:50176
	ds_read_b128 v[182:185], v165 offset:51200
	ds_read_b128 v[186:189], v165 offset:52224
	ds_read_b128 v[190:193], v165 offset:53248
	ds_read_b128 v[194:197], v165 offset:54272
	ds_read_b128 v[198:201], v165 offset:55296
	ds_read_b128 v[202:205], v165 offset:56320
	s_add_i32 s50, s50, s29
	v_lshl_add_u64 v[156:157], s[48:49], 0, v[112:113]
	s_add_u32 s48, s22, 0x38080
	s_mov_b32 m0, s50
	s_addc_u32 s49, s23, 0
	global_load_lds_dwordx4 v[156:157], off
	s_add_i32 m0, s50, 0x2000
	v_lshl_add_u64 v[156:157], s[48:49], 0, v[112:113]
	s_add_u32 s48, s22, 0x70080
	s_addc_u32 s49, s23, 0
	global_load_lds_dwordx4 v[156:157], off
	s_nop 0
	v_lshl_add_u64 v[156:157], s[48:49], 0, v[112:113]
	s_add_i32 s48, s51, s29
	s_mov_b32 m0, s48
	s_add_u32 s22, s22, 0xa8080
	global_load_lds_dwordx4 v[156:157], off
	s_addc_u32 s23, s23, 0
	s_add_i32 m0, s48, 0x2000
	s_add_u32 s18, s18, 0x38080
	v_lshl_add_u64 v[156:157], s[22:23], 0, v[112:113]
	global_load_lds_dwordx4 v[156:157], off
	s_mov_b32 m0, s37
	v_lshl_add_u64 v[156:157], s[20:21], 0, v[154:155]
	s_addc_u32 s19, s19, 0
	global_load_lds_dwordx4 v[156:157], off
	s_mov_b32 m0, s38
	v_lshl_add_u64 v[156:157], s[18:19], 0, v[154:155]
	global_load_lds_dwordx4 v[156:157], off
	s_waitcnt vmcnt(8)
	s_waitcnt lgkmcnt(0)
	s_barrier
	s_setprio 1
	s_waitcnt lgkmcnt(0)
	v_mfma_f32_16x16x128_f8f6f4 v[60:63], v[130:137], v[174:181], v[60:63]
	v_mfma_f32_16x16x128_f8f6f4 v[56:59], v[138:145], v[174:181], v[56:59]
	v_mfma_f32_16x16x128_f8f6f4 v[44:47], v[130:137], v[182:189], v[44:47]
	v_mfma_f32_16x16x128_f8f6f4 v[40:43], v[138:145], v[182:189], v[40:43]
	v_mfma_f32_16x16x128_f8f6f4 v[28:31], v[130:137], v[190:197], v[28:31]
	v_mfma_f32_16x16x128_f8f6f4 v[24:27], v[138:145], v[190:197], v[24:27]
	v_mfma_f32_16x16x128_f8f6f4 v[12:15], v[130:137], v[198:205], v[12:15]
	v_mfma_f32_16x16x128_f8f6f4 v[8:11], v[138:145], v[198:205], v[8:11]
	s_setprio 0
	s_setprio 1
	v_mfma_f32_16x16x128_f8f6f4 v[52:55], v[146:153], v[174:181], v[52:55]
	v_mfma_f32_16x16x128_f8f6f4 v[48:51], v[166:173], v[174:181], v[48:51]
	v_mfma_f32_16x16x128_f8f6f4 v[36:39], v[146:153], v[182:189], v[36:39]
	v_mfma_f32_16x16x128_f8f6f4 v[32:35], v[166:173], v[182:189], v[32:35]
	v_mfma_f32_16x16x128_f8f6f4 v[20:23], v[146:153], v[190:197], v[20:23]
	v_mfma_f32_16x16x128_f8f6f4 v[16:19], v[166:173], v[190:197], v[16:19]
	v_mfma_f32_16x16x128_f8f6f4 v[4:7], v[146:153], v[198:205], v[4:7]
	v_mfma_f32_16x16x128_f8f6f4 v[0:3], v[166:173], v[198:205], v[0:3]
	s_setprio 0
	s_barrier
	s_add_i32 s47, s47, 2
	s_add_u32 s45, s45, 0x100
	s_addc_u32 s46, s46, 0
	s_add_u32 s2, s2, 0x100
	s_addc_u32 s3, s3, 0
	s_cmp_gt_u32 s47, 25
	s_cbranch_scc0 .LBB0_1837
	s_and_b64 vcc, exec, s[6:7]
	s_cbranch_vccz .LBB0_1840
	s_barrier
